# speedup vs baseline: 1.0180x; 1.0062x over previous
_Z7kf_mainPKfPKiPfPjS3_S4_:
	s_ashr_i32 s24, s2, 7
	s_load_dwordx4 s[4:7], s[0:1], 0x0
	s_ashr_i32 s9, s2, 3
	s_mul_i32 s8, s24, 5
	s_and_b32 s3, s9, 15
	s_ashr_i32 s10, s8, 31
	s_lshl_b32 s8, s8, 4
	s_or_b32 s8, s8, s3
	s_mul_hi_u32 s11, s8, 0xc8000
	s_mul_i32 s10, s10, 0xc8000
	s_add_i32 s11, s11, s10
	s_mul_i32 s8, s8, 0xc8000
	s_and_b32 s22, s2, 7
	s_waitcnt lgkmcnt(0)
	s_add_u32 s4, s4, s8
	s_mul_i32 s8, s22, 0x1900
	v_add_u32_e32 v137, s8, v0
	s_addc_u32 s5, s5, s11
	v_lshlrev_b32_e32 v74, 4, v137
	v_mov_b32_e32 v75, 0
	v_lshl_add_u64 v[130:131], s[4:5], 0, v[74:75]
	global_load_dwordx4 v[46:49], v74, s[4:5] nt
	s_mov_b32 s4, 0xc80000
	v_add_co_u32_e32 v2, vcc, s4, v130
	s_mov_b32 s4, 0x1900000
	s_nop 0
	v_addc_co_u32_e32 v3, vcc, 0, v131, vcc
	global_load_dwordx4 v[26:29], v[2:3], off nt
	v_add_co_u32_e32 v2, vcc, s4, v130
	s_mov_b32 s5, 0x3200000
	s_nop 0
	v_addc_co_u32_e32 v3, vcc, 0, v131, vcc
	global_load_dwordx4 v[34:37], v[2:3], off nt
	v_add_co_u32_e32 v2, vcc, s5, v130
	s_mov_b32 s4, 0x2580000
	s_nop 0
	v_addc_co_u32_e32 v3, vcc, 0, v131, vcc
	s_mul_hi_i32 s5, s9, 0xc8000
	s_mul_i32 s9, s9, 0xc8000
	global_load_dwordx4 v[18:21], v[2:3], off nt
	v_add_co_u32_e32 v2, vcc, s4, v130
	s_add_u32 s4, s6, s9
	s_nop 0
	v_addc_co_u32_e32 v3, vcc, 0, v131, vcc
	s_addc_u32 s5, s7, s5
	global_load_dwordx4 v[10:13], v[2:3], off nt
	global_load_dwordx4 v[6:9], v74, s[4:5] nt
	v_cvt_f32_ubyte0_e32 v1, s3
	v_mov_b32_e32 v2, 1.0
	s_movk_i32 s6, 0x3000
	v_fmamk_f32 v128, v1, 0x3b53680d, v2
	v_add_co_u32_e32 v2, vcc, s6, v130
	s_mov_b32 s7, 0xc83000
	s_nop 0
	v_addc_co_u32_e32 v3, vcc, 0, v131, vcc
	v_add_co_u32_e32 v4, vcc, s7, v130
	s_mov_b32 s7, 0x1903000
	s_nop 0
	v_addc_co_u32_e32 v5, vcc, 0, v131, vcc
	global_load_dwordx4 v[38:41], v[2:3], off nt
	global_load_dwordx4 v[30:33], v[4:5], off nt
	v_add_co_u32_e32 v2, vcc, s7, v130
	s_mov_b32 s7, 0x2583000
	s_nop 0
	v_addc_co_u32_e32 v3, vcc, 0, v131, vcc
	v_add_co_u32_e32 v4, vcc, s7, v130
	s_mov_b32 s7, 0x3203000
	s_nop 0
	v_addc_co_u32_e32 v5, vcc, 0, v131, vcc
	global_load_dwordx4 v[42:45], v[2:3], off nt
	global_load_dwordx4 v[14:17], v[4:5], off nt
	v_add_co_u32_e32 v2, vcc, s7, v130
	v_lshl_add_u64 v[132:133], s[4:5], 0, v[74:75]
	s_nop 0
	v_addc_co_u32_e32 v3, vcc, 0, v131, vcc
	global_load_dwordx4 v[22:25], v[2:3], off nt
	v_add_co_u32_e32 v2, vcc, s6, v132
	s_mov_b32 s6, 0xcccd
	s_nop 0
	v_addc_co_u32_e32 v3, vcc, 0, v133, vcc
	global_load_dwordx4 v[2:5], v[2:3], off nt
	v_mul_u32_u24_sdwa v1, v137, s6 dst_sel:DWORD dst_unused:UNUSED_PAD src0_sel:WORD_0 src1_sel:DWORD
	v_lshrrev_b32_e32 v1, 23, v1
	v_cvt_f32_u32_e32 v50, v1
	v_mul_i32_i24_e32 v1, 0xffffff60, v1
	v_add_lshl_u32 v1, v1, v137, 2
	v_cvt_f32_i32_e32 v1, v1
	s_mov_b32 s7, 0x3b033c6e
	v_fma_f32 v50, v50, s7, 1.0
	s_mov_b32 s9, 0x3b086211
	v_fma_f32 v1, v1, s9, 1.0
	v_add_f32_e32 v59, 0x3b086211, v1
	v_mov_b32_e32 v136, 0x670
	s_waitcnt vmcnt(11)
	v_mul_f32_e32 v46, 0x4038aa3b, v46
	v_exp_f32_e32 v46, v46
	v_mul_f32_e32 v47, 0x4038aa3b, v47
	v_exp_f32_e32 v47, v47
	v_mul_f32_e32 v48, 0x4038aa3b, v48
	v_add_f32_e32 v46, 1.0, v46
	v_rcp_f32_e32 v46, v46
	s_waitcnt vmcnt(10)
	v_mul_f32_e32 v26, 0x4038aa3b, v26
	v_exp_f32_e32 v26, v26
	v_mul_f32_e32 v27, 0x4038aa3b, v27
	v_exp_f32_e32 v27, v27
	v_fma_f32 v46, -2.0, v46, v128
	v_add_f32_e32 v26, 1.0, v26
	s_waitcnt vmcnt(9)
	v_mul_f32_e32 v34, 0x4038aa3b, v34
	v_exp_f32_e32 v34, v34
	v_mul_f32_e32 v35, 0x4038aa3b, v35
	v_rcp_f32_e32 v26, v26
	v_exp_f32_e32 v35, v35
	v_add_f32_e32 v34, 1.0, v34
	v_rcp_f32_e32 v34, v34
	v_fma_f32 v26, -2.0, v26, v50
	v_add_f32_e32 v47, 1.0, v47
	v_add_f32_e32 v27, 1.0, v27
	v_add_f32_e32 v35, 1.0, v35
	v_fma_f32 v34, -2.0, v34, v1
	v_add_f32_e32 v51, v46, v26
	v_rcp_f32_e32 v47, v47
	v_rcp_f32_e32 v27, v27
	v_rcp_f32_e32 v35, v35
	v_add_f32_e32 v76, v51, v34
	v_mul_f32_e32 v78, v34, v34
	v_fmac_f32_e32 v78, v26, v26
	s_waitcnt vmcnt(7)
	v_mul_f32_e32 v26, v10, v10
	s_waitcnt vmcnt(6)
	v_cmp_eq_u32_e32 vcc, 1, v6
	v_add_f32_e32 v51, 0, v76
	v_add_f32_e32 v10, 0, v10
	v_fmac_f32_e32 v78, v46, v46
	v_cndmask_b32_e64 v34, 0, 1.0, vcc
	v_cndmask_b32_e32 v46, 0, v26, vcc
	v_cndmask_b32_e32 v52, 0, v51, vcc
	v_cndmask_b32_e32 v53, 0, v10, vcc
	v_cmp_eq_u32_e32 vcc, 2, v6
	v_fma_f32 v47, -2.0, v47, v128
	v_fma_f32 v27, -2.0, v27, v50
	v_cndmask_b32_e64 v54, 0, 1.0, vcc
	v_cndmask_b32_e32 v55, 0, v26, vcc
	v_cndmask_b32_e32 v56, 0, v51, vcc
	v_cndmask_b32_e32 v57, 0, v10, vcc
	v_cmp_eq_u32_e32 vcc, 3, v6
	v_fmac_f32_e32 v59, -2.0, v35
	v_add_f32_e32 v35, v47, v27
	v_cndmask_b32_e64 v58, 0, 1.0, vcc
	v_cndmask_b32_e32 v26, 0, v26, vcc
	v_cndmask_b32_e32 v51, 0, v51, vcc
	v_cndmask_b32_e32 v10, 0, v10, vcc
	v_mul_f32_e32 v79, v59, v59
	v_cmp_eq_u32_e32 vcc, 1, v7
	v_add_f32_e32 v77, v35, v59
	v_fmac_f32_e32 v79, v27, v27
	v_mul_f32_e32 v27, v11, v11
	v_cndmask_b32_e64 v35, 0, 1.0, vcc
	v_fmac_f32_e32 v79, v47, v47
	v_add_f32_e32 v34, v35, v34
	v_cndmask_b32_e32 v35, 0, v27, vcc
	v_cndmask_b32_e32 v47, 0, v11, vcc
	v_cndmask_b32_e32 v59, 0, v77, vcc
	v_cmp_eq_u32_e32 vcc, 2, v7
	v_add_f32_e32 v35, v35, v46
	v_add_f32_e32 v52, v52, v59
	v_cndmask_b32_e64 v46, 0, 1.0, vcc
	v_add_f32_e32 v47, v47, v53
	v_add_f32_e32 v46, v46, v54
	v_cndmask_b32_e32 v53, 0, v27, vcc
	v_cndmask_b32_e32 v54, 0, v11, vcc
	v_cndmask_b32_e32 v59, 0, v77, vcc
	v_cmp_eq_u32_e32 vcc, 3, v7
	v_exp_f32_e32 v48, v48
	v_add_f32_e32 v54, v54, v57
	v_cndmask_b32_e32 v27, 0, v27, vcc
	v_cndmask_b32_e32 v11, 0, v11, vcc
	v_add_f32_e32 v10, v11, v10
	v_add_f32_e32 v11, v27, v26
	v_mul_f32_e32 v27, 0x4038aa3b, v28
	v_mul_f32_e32 v28, 0x4038aa3b, v36
	v_exp_f32_e32 v28, v28
	v_exp_f32_e32 v27, v27
	v_add_f32_e32 v26, 1.0, v48
	v_rcp_f32_e32 v26, v26
	v_add_f32_e32 v28, 1.0, v28
	v_add_f32_e32 v27, 1.0, v27
	v_rcp_f32_e32 v28, v28
	v_rcp_f32_e32 v27, v27
	v_add_f32_e32 v36, 0x3b886211, v1
	v_fma_f32 v26, -2.0, v26, v128
	v_fmac_f32_e32 v36, -2.0, v28
	v_fma_f32 v27, -2.0, v27, v50
	v_mul_f32_e32 v82, v36, v36
	v_add_f32_e32 v53, v53, v55
	v_cndmask_b32_e64 v55, 0, 1.0, vcc
	v_cndmask_b32_e32 v57, 0, v77, vcc
	v_add_f32_e32 v28, v26, v27
	v_fmac_f32_e32 v82, v27, v27
	v_cmp_eq_u32_e32 vcc, 1, v8
	v_add_f32_e32 v80, v28, v36
	v_fmac_f32_e32 v82, v26, v26
	v_mul_f32_e32 v26, v12, v12
	v_cndmask_b32_e64 v27, 0, 1.0, vcc
	v_add_f32_e32 v27, v27, v34
	v_cndmask_b32_e32 v28, 0, v26, vcc
	v_cndmask_b32_e32 v34, 0, v12, vcc
	v_cndmask_b32_e32 v36, 0, v80, vcc
	v_cmp_eq_u32_e32 vcc, 2, v8
	v_add_f32_e32 v28, v28, v35
	v_add_f32_e32 v34, v34, v47
	v_cndmask_b32_e64 v35, 0, 1.0, vcc
	v_add_f32_e32 v35, v35, v46
	v_cndmask_b32_e32 v46, 0, v26, vcc
	v_cndmask_b32_e32 v47, 0, v12, vcc
	v_cndmask_b32_e32 v48, 0, v80, vcc
	v_cmp_eq_u32_e32 vcc, 3, v8
	v_mul_f32_e32 v49, 0x4038aa3b, v49
	v_exp_f32_e32 v49, v49
	v_cndmask_b32_e32 v26, 0, v26, vcc
	v_add_f32_e32 v11, v26, v11
	v_mul_f32_e32 v26, 0x4038aa3b, v29
	v_mul_f32_e32 v29, 0x4038aa3b, v37
	v_exp_f32_e32 v26, v26
	v_exp_f32_e32 v29, v29
	v_cndmask_b32_e32 v12, 0, v12, vcc
	v_add_f32_e32 v10, v12, v10
	v_add_f32_e32 v12, 1.0, v49
	v_add_f32_e32 v26, 1.0, v26
	v_add_f32_e32 v29, 1.0, v29
	v_rcp_f32_e32 v12, v12
	v_rcp_f32_e32 v26, v26
	v_rcp_f32_e32 v29, v29
	v_mul_f32_e32 v21, 0xbfb8aa3b, v21
	v_exp_f32_e32 v21, v21
	v_add_f32_e32 v1, 0x3bcc931a, v1
	v_mul_f32_e32 v18, 0xbfb8aa3b, v18
	v_mul_f32_e32 v19, 0xbfb8aa3b, v19
	v_mul_f32_e32 v20, 0xbfb8aa3b, v20
	v_fma_f32 v12, -2.0, v12, v128
	v_fmac_f32_e32 v50, -2.0, v26
	v_fmac_f32_e32 v1, -2.0, v29
	v_exp_f32_e32 v18, v18
	v_exp_f32_e32 v19, v19
	v_exp_f32_e32 v20, v20
	v_add_f32_e32 v26, v12, v50
	v_mul_f32_e32 v83, v1, v1
	v_add_f32_e32 v36, v52, v36
	v_add_f32_e32 v46, v46, v53
	v_cndmask_b32_e64 v52, 0, 1.0, vcc
	v_cndmask_b32_e32 v53, 0, v80, vcc
	v_add_f32_e32 v81, v26, v1
	v_fmac_f32_e32 v83, v50, v50
	v_add_f32_e32 v1, 1.0, v21
	v_cmp_eq_u32_e32 vcc, 1, v9
	v_fmac_f32_e32 v83, v12, v12
	v_rcp_f32_e32 v21, v1
	v_mul_f32_e32 v1, v13, v13
	v_cndmask_b32_e64 v12, 0, 1.0, vcc
	v_add_f32_e32 v47, v47, v54
	v_add_f32_e32 v54, v12, v27
	v_cndmask_b32_e32 v12, 0, v1, vcc
	v_cndmask_b32_e32 v26, 0, v13, vcc
	v_cndmask_b32_e32 v27, 0, v81, vcc
	v_cmp_eq_u32_e32 vcc, 2, v9
	v_add_f32_e32 v18, 1.0, v18
	v_add_f32_e32 v19, 1.0, v19
	v_add_f32_e32 v56, v56, v59
	v_add_f32_e32 v55, v55, v58
	v_add_f32_e32 v51, v51, v57
	v_add_f32_e32 v20, 1.0, v20
	v_add_f32_e32 v57, v12, v28
	v_cndmask_b32_e64 v12, 0, 1.0, vcc
	v_rcp_f32_e32 v18, v18
	v_rcp_f32_e32 v19, v19
	v_rcp_f32_e32 v20, v20
	v_add_f32_e32 v48, v56, v48
	v_add_f32_e32 v52, v52, v55
	v_add_f32_e32 v55, v36, v27
	v_add_f32_e32 v56, v26, v34
	v_add_f32_e32 v58, v12, v35
	v_cndmask_b32_e32 v12, 0, v1, vcc
	v_cndmask_b32_e32 v26, 0, v13, vcc
	v_cndmask_b32_e32 v27, 0, v81, vcc
	v_cmp_eq_u32_e32 vcc, 3, v9
	v_add_f32_e32 v61, v12, v46
	s_movk_i32 s4, 0x100
	v_cndmask_b32_e64 v12, 0, 1.0, vcc
	v_add_f32_e32 v51, v51, v53
	v_add_f32_e32 v62, v12, v52
	v_cndmask_b32_e32 v1, 0, v1, vcc
	v_cndmask_b32_e32 v12, 0, v13, vcc
	v_cndmask_b32_e32 v13, 0, v81, vcc
	v_lshl_add_u32 v134, v0, 4, v136
	v_cmp_gt_u32_e64 s[4:5], s4, v0
	v_add_f32_e32 v59, v48, v27
	v_add_f32_e32 v60, v26, v47
	v_add_f32_e32 v63, v51, v13
	v_add_f32_e32 v64, v12, v10
	v_add_f32_e32 v65, v1, v11
	s_mov_b32 s10, 0xc000
	v_add_u32_e32 v1, 0xc000, v134
	ds_write_b128 v134, v[18:21] offset:49152
	s_movk_i32 s11, 0x6000
	v_add_co_u32_e32 v10, vcc, s11, v130
	s_mov_b32 s12, 0xc86000
	s_nop 0
	v_addc_co_u32_e32 v11, vcc, 0, v131, vcc
	v_add_co_u32_e32 v12, vcc, s12, v130
	s_mov_b32 s12, 0x1906000
	s_nop 0
	v_addc_co_u32_e32 v13, vcc, 0, v131, vcc
	global_load_dwordx4 v[46:49], v[10:11], off nt
	global_load_dwordx4 v[34:37], v[12:13], off nt
	v_add_co_u32_e32 v10, vcc, s12, v130
	s_mov_b32 s12, 0x2586000
	s_nop 0
	v_addc_co_u32_e32 v11, vcc, 0, v131, vcc
	v_add_co_u32_e32 v12, vcc, s12, v130
	s_mov_b32 s12, 0x3206000
	s_nop 0
	v_addc_co_u32_e32 v13, vcc, 0, v131, vcc
	global_load_dwordx4 v[50:53], v[10:11], off nt
	global_load_dwordx4 v[18:21], v[12:13], off nt
	v_add_co_u32_e32 v10, vcc, s12, v130
	v_add_u32_e32 v66, 0x300, v137
	s_nop 0
	v_addc_co_u32_e32 v11, vcc, 0, v131, vcc
	global_load_dwordx4 v[26:29], v[10:11], off nt
	v_add_co_u32_e32 v10, vcc, s11, v132
	s_waitcnt vmcnt(8)
	v_mul_f32_e32 v42, 0x4038aa3b, v42
	v_addc_co_u32_e32 v11, vcc, 0, v133, vcc
	global_load_dwordx4 v[10:13], v[10:11], off nt
	v_mul_u32_u24_sdwa v67, v66, s6 dst_sel:DWORD dst_unused:UNUSED_PAD src0_sel:WORD_0 src1_sel:DWORD
	v_mul_f32_e32 v38, 0x4038aa3b, v38
	v_mul_f32_e32 v30, 0x4038aa3b, v30
	v_exp_f32_e32 v42, v42
	v_lshrrev_b32_e32 v67, 23, v67
	v_exp_f32_e32 v38, v38
	v_exp_f32_e32 v30, v30
	v_cvt_f32_u32_e32 v68, v67
	v_mul_i32_i24_e32 v67, 0xffffff60, v67
	v_add_lshl_u32 v66, v67, v66, 2
	v_cvt_f32_i32_e32 v66, v66
	v_add_f32_e32 v42, 1.0, v42
	v_add_f32_e32 v38, 1.0, v38
	v_add_f32_e32 v30, 1.0, v30
	v_rcp_f32_e32 v42, v42
	v_rcp_f32_e32 v38, v38
	v_rcp_f32_e32 v30, v30
	v_fma_f32 v66, v66, s9, 1.0
	v_mul_f32_e32 v43, 0x4038aa3b, v43
	v_fma_f32 v68, v68, s7, 1.0
	v_fma_f32 v42, -2.0, v42, v66
	v_mul_f32_e32 v39, 0x4038aa3b, v39
	v_mul_f32_e32 v31, 0x4038aa3b, v31
	v_exp_f32_e32 v43, v43
	v_fma_f32 v38, -2.0, v38, v128
	v_fma_f32 v30, -2.0, v30, v68
	v_mul_f32_e32 v86, v42, v42
	v_exp_f32_e32 v39, v39
	v_exp_f32_e32 v31, v31
	v_add_f32_e32 v67, v38, v30
	v_fmac_f32_e32 v86, v30, v30
	s_waitcnt vmcnt(6)
	v_cmp_eq_u32_e32 vcc, 1, v2
	v_add_f32_e32 v84, v67, v42
	v_fmac_f32_e32 v86, v38, v38
	v_mul_f32_e32 v30, v14, v14
	v_cndmask_b32_e64 v38, 0, 1.0, vcc
	v_add_f32_e32 v38, v54, v38
	v_cndmask_b32_e32 v42, 0, v30, vcc
	v_cndmask_b32_e32 v54, 0, v14, vcc
	v_cndmask_b32_e32 v67, 0, v84, vcc
	v_cmp_eq_u32_e32 vcc, 2, v2
	v_add_f32_e32 v43, 1.0, v43
	v_add_f32_e32 v54, v56, v54
	v_cndmask_b32_e64 v56, 0, 1.0, vcc
	v_add_f32_e32 v39, 1.0, v39
	v_add_f32_e32 v31, 1.0, v31
	v_rcp_f32_e32 v43, v43
	v_add_f32_e32 v55, v55, v67
	v_add_f32_e32 v42, v57, v42
	v_add_f32_e32 v56, v58, v56
	v_cndmask_b32_e32 v57, 0, v30, vcc
	v_cndmask_b32_e32 v58, 0, v14, vcc
	v_cndmask_b32_e32 v67, 0, v84, vcc
	v_cmp_eq_u32_e32 vcc, 3, v2
	v_rcp_f32_e32 v39, v39
	v_rcp_f32_e32 v31, v31
	v_add_f32_e32 v58, v60, v58
	v_cndmask_b32_e64 v60, 0, 1.0, vcc
	v_add_f32_e32 v60, v62, v60
	v_add_f32_e32 v62, 0x3b086211, v66
	v_fmac_f32_e32 v62, -2.0, v43
	v_fma_f32 v39, -2.0, v39, v128
	v_fma_f32 v31, -2.0, v31, v68
	v_mul_f32_e32 v87, v62, v62
	v_add_f32_e32 v57, v61, v57
	v_cndmask_b32_e32 v30, 0, v30, vcc
	v_cndmask_b32_e32 v14, 0, v14, vcc
	v_cndmask_b32_e32 v61, 0, v84, vcc
	v_add_f32_e32 v43, v39, v31
	v_fmac_f32_e32 v87, v31, v31
	v_cmp_eq_u32_e32 vcc, 1, v3
	v_add_f32_e32 v85, v43, v62
	v_fmac_f32_e32 v87, v39, v39
	v_mul_f32_e32 v31, v15, v15
	v_cndmask_b32_e64 v39, 0, 1.0, vcc
	v_add_f32_e32 v38, v39, v38
	v_cndmask_b32_e32 v39, 0, v31, vcc
	v_cndmask_b32_e32 v43, 0, v15, vcc
	v_cndmask_b32_e32 v62, 0, v85, vcc
	v_cmp_eq_u32_e32 vcc, 2, v3
	v_add_f32_e32 v39, v39, v42
	v_add_f32_e32 v55, v55, v62
	v_cndmask_b32_e64 v42, 0, 1.0, vcc
	v_add_f32_e32 v43, v43, v54
	v_add_f32_e32 v42, v42, v56
	v_cndmask_b32_e32 v54, 0, v31, vcc
	v_cndmask_b32_e32 v56, 0, v15, vcc
	v_cndmask_b32_e32 v62, 0, v85, vcc
	v_cmp_eq_u32_e32 vcc, 3, v3
	v_add_f32_e32 v14, v64, v14
	v_add_f32_e32 v30, v65, v30
	v_cndmask_b32_e32 v31, 0, v31, vcc
	v_cndmask_b32_e32 v15, 0, v15, vcc
	v_add_f32_e32 v14, v15, v14
	v_add_f32_e32 v15, v31, v30
	v_mul_f32_e32 v31, 0x4038aa3b, v32
	v_mul_f32_e32 v32, 0x4038aa3b, v44
	v_mul_f32_e32 v40, 0x4038aa3b, v40
	v_exp_f32_e32 v32, v32
	v_exp_f32_e32 v40, v40
	v_exp_f32_e32 v31, v31
	v_add_f32_e32 v56, v56, v58
	v_add_f32_e32 v32, 1.0, v32
	v_add_f32_e32 v30, 1.0, v40
	v_add_f32_e32 v31, 1.0, v31
	v_rcp_f32_e32 v32, v32
	v_rcp_f32_e32 v30, v30
	v_rcp_f32_e32 v31, v31
	v_add_f32_e32 v40, 0x3b886211, v66
	v_fmac_f32_e32 v40, -2.0, v32
	v_fma_f32 v30, -2.0, v30, v128
	v_fma_f32 v31, -2.0, v31, v68
	v_mul_f32_e32 v90, v40, v40
	v_add_f32_e32 v54, v54, v57
	v_cndmask_b32_e64 v57, 0, 1.0, vcc
	v_cndmask_b32_e32 v58, 0, v85, vcc
	v_add_f32_e32 v32, v30, v31
	v_fmac_f32_e32 v90, v31, v31
	v_cmp_eq_u32_e32 vcc, 1, v4
	v_add_f32_e32 v88, v32, v40
	v_fmac_f32_e32 v90, v30, v30
	v_mul_f32_e32 v30, v16, v16
	v_cndmask_b32_e64 v31, 0, 1.0, vcc
	v_add_f32_e32 v31, v31, v38
	v_cndmask_b32_e32 v32, 0, v30, vcc
	v_cndmask_b32_e32 v38, 0, v16, vcc
	v_cndmask_b32_e32 v40, 0, v88, vcc
	v_cmp_eq_u32_e32 vcc, 2, v4
	v_add_f32_e32 v32, v32, v39
	v_add_f32_e32 v38, v38, v43
	v_cndmask_b32_e64 v39, 0, 1.0, vcc
	v_add_f32_e32 v39, v39, v42
	v_cndmask_b32_e32 v42, 0, v30, vcc
	v_cndmask_b32_e32 v43, 0, v16, vcc
	v_cndmask_b32_e32 v44, 0, v88, vcc
	v_cmp_eq_u32_e32 vcc, 3, v4
	v_mul_f32_e32 v41, 0x4038aa3b, v41
	v_exp_f32_e32 v41, v41
	v_cndmask_b32_e32 v30, 0, v30, vcc
	v_add_f32_e32 v15, v30, v15
	v_mul_f32_e32 v30, 0x4038aa3b, v33
	v_mul_f32_e32 v33, 0x4038aa3b, v45
	v_exp_f32_e32 v33, v33
	v_exp_f32_e32 v30, v30
	v_cndmask_b32_e32 v16, 0, v16, vcc
	v_add_f32_e32 v14, v16, v14
	v_add_f32_e32 v33, 1.0, v33
	v_add_f32_e32 v30, 1.0, v30
	v_rcp_f32_e32 v33, v33
	v_add_f32_e32 v16, 1.0, v41
	v_rcp_f32_e32 v30, v30
	v_rcp_f32_e32 v16, v16
	v_mul_f32_e32 v25, 0xbfb8aa3b, v25
	v_add_f32_e32 v41, 0x3bcc931a, v66
	v_exp_f32_e32 v25, v25
	v_fmac_f32_e32 v41, -2.0, v33
	v_mul_f32_e32 v22, 0xbfb8aa3b, v22
	v_mul_f32_e32 v23, 0xbfb8aa3b, v23
	v_mul_f32_e32 v24, 0xbfb8aa3b, v24
	v_fmac_f32_e32 v68, -2.0, v30
	v_mul_f32_e32 v91, v41, v41
	v_exp_f32_e32 v22, v22
	v_exp_f32_e32 v23, v23
	v_exp_f32_e32 v24, v24
	v_fma_f32 v16, -2.0, v16, v128
	v_fmac_f32_e32 v91, v68, v68
	v_add_f32_e32 v40, v55, v40
	v_add_f32_e32 v42, v42, v54
	v_cndmask_b32_e64 v54, 0, 1.0, vcc
	v_cndmask_b32_e32 v55, 0, v88, vcc
	v_add_f32_e32 v30, v16, v68
	v_fmac_f32_e32 v91, v16, v16
	v_add_f32_e32 v16, 1.0, v25
	v_cmp_eq_u32_e32 vcc, 1, v5
	v_add_f32_e32 v89, v30, v41
	v_rcp_f32_e32 v25, v16
	v_mul_f32_e32 v16, v17, v17
	v_cndmask_b32_e64 v30, 0, 1.0, vcc
	v_add_f32_e32 v45, v30, v31
	v_cndmask_b32_e32 v30, 0, v16, vcc
	v_cndmask_b32_e32 v31, 0, v17, vcc
	v_cndmask_b32_e32 v33, 0, v89, vcc
	v_cmp_eq_u32_e32 vcc, 2, v5
	v_add_f32_e32 v22, 1.0, v22
	v_add_f32_e32 v23, 1.0, v23
	v_add_f32_e32 v57, v57, v60
	v_add_f32_e32 v24, 1.0, v24
	v_add_f32_e32 v66, v30, v32
	v_cndmask_b32_e64 v30, 0, 1.0, vcc
	v_rcp_f32_e32 v22, v22
	v_add_f32_e32 v59, v59, v67
	v_add_f32_e32 v61, v63, v61
	v_rcp_f32_e32 v23, v23
	v_rcp_f32_e32 v24, v24
	v_add_f32_e32 v54, v54, v57
	v_add_f32_e32 v57, v31, v38
	v_add_f32_e32 v67, v30, v39
	v_cndmask_b32_e32 v30, 0, v16, vcc
	v_cndmask_b32_e32 v31, 0, v17, vcc
	v_cndmask_b32_e32 v32, 0, v89, vcc
	v_cmp_eq_u32_e32 vcc, 3, v5
	v_add_f32_e32 v58, v61, v58
	v_add_f32_e32 v42, v30, v42
	v_cndmask_b32_e64 v30, 0, 1.0, vcc
	v_add_f32_e32 v59, v59, v62
	v_add_f32_e32 v55, v58, v55
	v_add_f32_e32 v54, v30, v54
	v_cndmask_b32_e32 v16, 0, v16, vcc
	v_cndmask_b32_e32 v17, 0, v17, vcc
	v_cndmask_b32_e32 v30, 0, v89, vcc
	v_add_f32_e32 v44, v59, v44
	v_add_f32_e32 v43, v43, v56
	v_add_f32_e32 v55, v55, v30
	v_add_f32_e32 v68, v17, v14
	v_add_f32_e32 v69, v16, v15
	v_add_f32_e32 v56, v40, v33
	v_add_f32_e32 v44, v44, v32
	v_add_f32_e32 v43, v31, v43
	ds_write_b128 v134, v[22:25] offset:61440
	s_mov_b32 s11, 0x9000
	v_add_co_u32_e32 v14, vcc, s11, v130
	s_mov_b32 s12, 0xc89000
	s_nop 0
	v_addc_co_u32_e32 v15, vcc, 0, v131, vcc
	v_add_co_u32_e32 v16, vcc, s12, v130
	s_mov_b32 s12, 0x1909000
	s_nop 0
	v_addc_co_u32_e32 v17, vcc, 0, v131, vcc
	global_load_dwordx4 v[62:65], v[14:15], off nt
	global_load_dwordx4 v[38:41], v[16:17], off nt
	v_add_co_u32_e32 v14, vcc, s12, v130
	s_mov_b32 s12, 0x2589000
	s_nop 0
	v_addc_co_u32_e32 v15, vcc, 0, v131, vcc
	v_add_co_u32_e32 v16, vcc, s12, v130
	s_mov_b32 s12, 0x3209000
	s_nop 0
	v_addc_co_u32_e32 v17, vcc, 0, v131, vcc
	global_load_dwordx4 v[58:61], v[14:15], off nt
	global_load_dwordx4 v[22:25], v[16:17], off nt
	v_add_co_u32_e32 v14, vcc, s12, v130
	v_add_u32_e32 v70, 0x600, v137
	s_nop 0
	v_addc_co_u32_e32 v15, vcc, 0, v131, vcc
	global_load_dwordx4 v[30:33], v[14:15], off nt
	v_add_co_u32_e32 v14, vcc, s11, v132
	s_waitcnt vmcnt(8)
	v_mul_f32_e32 v50, 0x4038aa3b, v50
	v_addc_co_u32_e32 v15, vcc, 0, v133, vcc
	global_load_dwordx4 v[14:17], v[14:15], off nt
	v_mul_u32_u24_sdwa v71, v70, s6 dst_sel:DWORD dst_unused:UNUSED_PAD src0_sel:WORD_0 src1_sel:DWORD
	v_mul_f32_e32 v46, 0x4038aa3b, v46
	v_mul_f32_e32 v34, 0x4038aa3b, v34
	v_exp_f32_e32 v50, v50
	v_lshrrev_b32_e32 v71, 23, v71
	v_exp_f32_e32 v46, v46
	v_exp_f32_e32 v34, v34
	v_cvt_f32_u32_e32 v72, v71
	v_mul_i32_i24_e32 v71, 0xffffff60, v71
	v_add_lshl_u32 v70, v71, v70, 2
	v_cvt_f32_i32_e32 v70, v70
	v_add_f32_e32 v50, 1.0, v50
	v_add_f32_e32 v46, 1.0, v46
	v_add_f32_e32 v34, 1.0, v34
	v_rcp_f32_e32 v50, v50
	v_rcp_f32_e32 v46, v46
	v_rcp_f32_e32 v34, v34
	v_fma_f32 v70, v70, s9, 1.0
	v_fma_f32 v72, v72, s7, 1.0
	v_fma_f32 v50, -2.0, v50, v70
	v_mul_f32_e32 v51, 0x4038aa3b, v51
	v_fma_f32 v46, -2.0, v46, v128
	v_fma_f32 v34, -2.0, v34, v72
	v_mul_f32_e32 v94, v50, v50
	v_mul_f32_e32 v47, 0x4038aa3b, v47
	v_mul_f32_e32 v35, 0x4038aa3b, v35
	v_exp_f32_e32 v51, v51
	v_add_f32_e32 v71, v46, v34
	v_fmac_f32_e32 v94, v34, v34
	s_waitcnt vmcnt(6)
	v_cmp_eq_u32_e32 vcc, 1, v10
	v_exp_f32_e32 v47, v47
	v_exp_f32_e32 v35, v35
	v_add_f32_e32 v92, v71, v50
	v_fmac_f32_e32 v94, v46, v46
	v_mul_f32_e32 v34, v18, v18
	v_cndmask_b32_e64 v46, 0, 1.0, vcc
	v_add_f32_e32 v45, v45, v46
	v_cndmask_b32_e32 v46, 0, v34, vcc
	v_cndmask_b32_e32 v50, 0, v18, vcc
	v_cndmask_b32_e32 v71, 0, v92, vcc
	v_cmp_eq_u32_e32 vcc, 2, v10
	v_add_f32_e32 v50, v57, v50
	v_add_f32_e32 v51, 1.0, v51
	v_cndmask_b32_e64 v57, 0, 1.0, vcc
	v_add_f32_e32 v56, v56, v71
	v_add_f32_e32 v46, v66, v46
	v_add_f32_e32 v57, v67, v57
	v_cndmask_b32_e32 v66, 0, v34, vcc
	v_cndmask_b32_e32 v67, 0, v18, vcc
	v_cndmask_b32_e32 v71, 0, v92, vcc
	v_cmp_eq_u32_e32 vcc, 3, v10
	v_add_f32_e32 v47, 1.0, v47
	v_add_f32_e32 v35, 1.0, v35
	v_rcp_f32_e32 v51, v51
	v_add_f32_e32 v42, v42, v66
	v_cndmask_b32_e64 v66, 0, 1.0, vcc
	v_rcp_f32_e32 v47, v47
	v_rcp_f32_e32 v35, v35
	v_add_f32_e32 v54, v54, v66
	v_cndmask_b32_e32 v66, 0, v92, vcc
	v_add_f32_e32 v55, v55, v66
	v_add_f32_e32 v66, 0x3b086211, v70
	v_fmac_f32_e32 v66, -2.0, v51
	v_fma_f32 v47, -2.0, v47, v128
	v_fma_f32 v35, -2.0, v35, v72
	v_mul_f32_e32 v95, v66, v66
	v_cndmask_b32_e32 v34, 0, v34, vcc
	v_cndmask_b32_e32 v18, 0, v18, vcc
	v_add_f32_e32 v51, v47, v35
	v_fmac_f32_e32 v95, v35, v35
	v_cmp_eq_u32_e32 vcc, 1, v11
	v_add_f32_e32 v93, v51, v66
	v_fmac_f32_e32 v95, v47, v47
	v_mul_f32_e32 v35, v19, v19
	v_cndmask_b32_e64 v47, 0, 1.0, vcc
	v_add_f32_e32 v45, v47, v45
	v_cndmask_b32_e32 v47, 0, v35, vcc
	v_cndmask_b32_e32 v51, 0, v19, vcc
	v_cndmask_b32_e32 v66, 0, v93, vcc
	v_cmp_eq_u32_e32 vcc, 2, v11
	v_add_f32_e32 v46, v47, v46
	v_add_f32_e32 v56, v56, v66
	v_cndmask_b32_e64 v47, 0, 1.0, vcc
	v_add_f32_e32 v50, v51, v50
	v_add_f32_e32 v47, v47, v57
	v_cndmask_b32_e32 v51, 0, v35, vcc
	v_cndmask_b32_e32 v57, 0, v19, vcc
	v_cndmask_b32_e32 v66, 0, v93, vcc
	v_cmp_eq_u32_e32 vcc, 3, v11
	v_add_f32_e32 v18, v68, v18
	v_add_f32_e32 v34, v69, v34
	v_cndmask_b32_e32 v35, 0, v35, vcc
	v_cndmask_b32_e32 v19, 0, v19, vcc
	v_add_f32_e32 v18, v19, v18
	v_add_f32_e32 v19, v35, v34
	v_mul_f32_e32 v35, 0x4038aa3b, v36
	v_mul_f32_e32 v36, 0x4038aa3b, v52
	v_mul_f32_e32 v48, 0x4038aa3b, v48
	v_exp_f32_e32 v36, v36
	v_exp_f32_e32 v48, v48
	v_exp_f32_e32 v35, v35
	v_add_f32_e32 v42, v51, v42
	v_add_f32_e32 v36, 1.0, v36
	v_add_f32_e32 v34, 1.0, v48
	v_add_f32_e32 v35, 1.0, v35
	v_rcp_f32_e32 v36, v36
	v_rcp_f32_e32 v34, v34
	v_rcp_f32_e32 v35, v35
	v_add_f32_e32 v48, 0x3b886211, v70
	v_fmac_f32_e32 v48, -2.0, v36
	v_cndmask_b32_e64 v51, 0, 1.0, vcc
	v_fma_f32 v34, -2.0, v34, v128
	v_fma_f32 v35, -2.0, v35, v72
	v_mul_f32_e32 v98, v48, v48
	v_add_f32_e32 v51, v51, v54
	v_cndmask_b32_e32 v54, 0, v93, vcc
	v_add_f32_e32 v36, v34, v35
	v_fmac_f32_e32 v98, v35, v35
	v_cmp_eq_u32_e32 vcc, 1, v12
	v_add_f32_e32 v96, v36, v48
	v_fmac_f32_e32 v98, v34, v34
	v_mul_f32_e32 v34, v20, v20
	v_cndmask_b32_e64 v35, 0, 1.0, vcc
	v_add_f32_e32 v35, v35, v45
	v_cndmask_b32_e32 v36, 0, v34, vcc
	v_cndmask_b32_e32 v45, 0, v20, vcc
	v_cndmask_b32_e32 v48, 0, v96, vcc
	v_cmp_eq_u32_e32 vcc, 2, v12
	v_add_f32_e32 v36, v36, v46
	v_add_f32_e32 v45, v45, v50
	v_cndmask_b32_e64 v46, 0, 1.0, vcc
	v_add_f32_e32 v46, v46, v47
	v_cndmask_b32_e32 v47, 0, v34, vcc
	v_cndmask_b32_e32 v50, 0, v20, vcc
	v_cndmask_b32_e32 v52, 0, v96, vcc
	v_cmp_eq_u32_e32 vcc, 3, v12
	v_mul_f32_e32 v49, 0x4038aa3b, v49
	v_exp_f32_e32 v49, v49
	v_cndmask_b32_e32 v34, 0, v34, vcc
	v_add_f32_e32 v19, v34, v19
	v_mul_f32_e32 v34, 0x4038aa3b, v37
	v_mul_f32_e32 v37, 0x4038aa3b, v53
	v_exp_f32_e32 v37, v37
	v_exp_f32_e32 v34, v34
	v_cndmask_b32_e32 v20, 0, v20, vcc
	v_add_f32_e32 v18, v20, v18
	v_add_f32_e32 v37, 1.0, v37
	v_add_f32_e32 v34, 1.0, v34
	v_rcp_f32_e32 v37, v37
	v_add_f32_e32 v20, 1.0, v49
	v_rcp_f32_e32 v34, v34
	v_rcp_f32_e32 v20, v20
	v_mul_f32_e32 v29, 0xbfb8aa3b, v29
	v_add_f32_e32 v49, 0x3bcc931a, v70
	v_exp_f32_e32 v29, v29
	v_fmac_f32_e32 v49, -2.0, v37
	v_mul_f32_e32 v26, 0xbfb8aa3b, v26
	v_add_f32_e32 v43, v43, v67
	v_mul_f32_e32 v27, 0xbfb8aa3b, v27
	v_mul_f32_e32 v28, 0xbfb8aa3b, v28
	v_fmac_f32_e32 v72, -2.0, v34
	v_mul_f32_e32 v99, v49, v49
	v_exp_f32_e32 v26, v26
	v_exp_f32_e32 v27, v27
	v_add_f32_e32 v43, v57, v43
	v_exp_f32_e32 v28, v28
	v_fma_f32 v20, -2.0, v20, v128
	v_fmac_f32_e32 v99, v72, v72
	v_add_f32_e32 v43, v50, v43
	v_add_f32_e32 v42, v47, v42
	v_cndmask_b32_e64 v47, 0, 1.0, vcc
	v_cndmask_b32_e32 v50, 0, v96, vcc
	v_add_f32_e32 v34, v20, v72
	v_fmac_f32_e32 v99, v20, v20
	v_add_f32_e32 v20, 1.0, v29
	v_cmp_eq_u32_e32 vcc, 1, v13
	v_add_f32_e32 v97, v34, v49
	v_rcp_f32_e32 v29, v20
	v_mul_f32_e32 v20, v21, v21
	v_cndmask_b32_e64 v34, 0, 1.0, vcc
	v_add_f32_e32 v44, v44, v71
	v_add_f32_e32 v47, v47, v51
	v_add_f32_e32 v51, v34, v35
	v_cndmask_b32_e32 v34, 0, v20, vcc
	v_cndmask_b32_e32 v35, 0, v21, vcc
	v_cndmask_b32_e32 v37, 0, v97, vcc
	v_cmp_eq_u32_e32 vcc, 2, v13
	v_add_f32_e32 v26, 1.0, v26
	v_add_f32_e32 v27, 1.0, v27
	v_add_f32_e32 v44, v44, v66
	v_add_f32_e32 v28, 1.0, v28
	v_add_f32_e32 v66, v34, v36
	v_cndmask_b32_e64 v34, 0, 1.0, vcc
	v_rcp_f32_e32 v26, v26
	v_rcp_f32_e32 v27, v27
	v_rcp_f32_e32 v28, v28
	v_add_f32_e32 v53, v35, v45
	v_add_f32_e32 v67, v34, v46
	v_cndmask_b32_e32 v34, 0, v20, vcc
	v_cndmask_b32_e32 v35, 0, v21, vcc
	v_cndmask_b32_e32 v36, 0, v97, vcc
	v_cmp_eq_u32_e32 vcc, 3, v13
	v_add_f32_e32 v54, v55, v54
	v_add_f32_e32 v70, v34, v42
	v_cndmask_b32_e64 v34, 0, 1.0, vcc
	v_add_f32_e32 v44, v44, v52
	v_add_f32_e32 v50, v54, v50
	v_add_f32_e32 v71, v34, v47
	v_cndmask_b32_e32 v20, 0, v20, vcc
	v_cndmask_b32_e32 v21, 0, v21, vcc
	v_cndmask_b32_e32 v34, 0, v97, vcc
	v_add_f32_e32 v48, v56, v48
	v_add_f32_e32 v68, v44, v36
	v_add_f32_e32 v69, v35, v43
	v_add_f32_e32 v50, v50, v34
	v_add_f32_e32 v72, v21, v18
	v_add_f32_e32 v73, v20, v19
	v_add_f32_e32 v52, v48, v37
	ds_write_b128 v1, v[26:29] offset:24576
	v_add_co_u32_e32 v18, vcc, s10, v130
	s_mov_b32 s11, 0xc8c000
	s_nop 0
	v_addc_co_u32_e32 v19, vcc, 0, v131, vcc
	v_add_co_u32_e32 v20, vcc, s11, v130
	s_mov_b32 s11, 0x190c000
	s_nop 0
	v_addc_co_u32_e32 v21, vcc, 0, v131, vcc
	global_load_dwordx4 v[54:57], v[18:19], off nt
	global_load_dwordx4 v[42:45], v[20:21], off nt
	v_add_co_u32_e32 v18, vcc, s11, v130
	s_mov_b32 s11, 0x258c000
	s_nop 0
	v_addc_co_u32_e32 v19, vcc, 0, v131, vcc
	v_add_co_u32_e32 v20, vcc, s11, v130
	s_mov_b32 s11, 0x320c000
	s_nop 0
	v_addc_co_u32_e32 v21, vcc, 0, v131, vcc
	global_load_dwordx4 v[46:49], v[18:19], off nt
	global_load_dwordx4 v[26:29], v[20:21], off nt
	v_add_co_u32_e32 v18, vcc, s11, v130
	v_add_u32_e32 v74, 0x900, v137
	s_nop 0
	v_addc_co_u32_e32 v19, vcc, 0, v131, vcc
	global_load_dwordx4 v[34:37], v[18:19], off nt
	v_add_co_u32_e32 v18, vcc, s10, v132
	s_waitcnt vmcnt(10)
	v_mul_f32_e32 v62, 0x4038aa3b, v62
	v_addc_co_u32_e32 v19, vcc, 0, v133, vcc
	global_load_dwordx4 v[18:21], v[18:19], off nt
	s_waitcnt vmcnt(10)
	v_mul_f32_e32 v38, 0x4038aa3b, v38
	s_waitcnt vmcnt(9)
	v_mul_f32_e32 v58, 0x4038aa3b, v58
	v_mul_u32_u24_sdwa v100, v74, s6 dst_sel:DWORD dst_unused:UNUSED_PAD src0_sel:WORD_0 src1_sel:DWORD
	v_exp_f32_e32 v62, v62
	v_exp_f32_e32 v38, v38
	v_exp_f32_e32 v58, v58
	v_lshrrev_b32_e32 v100, 23, v100
	v_cvt_f32_u32_e32 v101, v100
	v_mul_i32_i24_e32 v100, 0xffffff60, v100
	v_add_lshl_u32 v74, v100, v74, 2
	v_cvt_f32_i32_e32 v74, v74
	v_add_f32_e32 v62, 1.0, v62
	v_add_f32_e32 v38, 1.0, v38
	v_add_f32_e32 v58, 1.0, v58
	v_rcp_f32_e32 v62, v62
	v_rcp_f32_e32 v38, v38
	v_rcp_f32_e32 v58, v58
	v_mul_f32_e32 v63, 0x4038aa3b, v63
	v_mul_f32_e32 v39, 0x4038aa3b, v39
	v_mul_f32_e32 v59, 0x4038aa3b, v59
	v_fma_f32 v108, v101, s7, 1.0
	v_fma_f32 v74, v74, s9, 1.0
	v_exp_f32_e32 v63, v63
	v_exp_f32_e32 v39, v39
	v_exp_f32_e32 v59, v59
	v_fma_f32 v62, -2.0, v62, v128
	v_fma_f32 v38, -2.0, v38, v108
	v_fma_f32 v58, -2.0, v58, v74
	v_add_f32_e32 v100, v62, v38
	v_mul_f32_e32 v102, v58, v58
	s_waitcnt vmcnt(6)
	v_cmp_eq_u32_e32 vcc, 1, v14
	v_add_f32_e32 v100, v100, v58
	v_fmac_f32_e32 v102, v38, v38
	v_mul_f32_e32 v38, v22, v22
	v_cndmask_b32_e64 v58, 0, 1.0, vcc
	v_fmac_f32_e32 v102, v62, v62
	v_add_f32_e32 v51, v51, v58
	v_cndmask_b32_e32 v58, 0, v38, vcc
	v_cndmask_b32_e32 v62, 0, v22, vcc
	v_cndmask_b32_e32 v101, 0, v100, vcc
	v_cmp_eq_u32_e32 vcc, 2, v14
	v_add_f32_e32 v63, 1.0, v63
	v_add_f32_e32 v39, 1.0, v39
	v_add_f32_e32 v59, 1.0, v59
	v_add_f32_e32 v53, v53, v62
	v_cndmask_b32_e64 v62, 0, 1.0, vcc
	v_rcp_f32_e32 v63, v63
	v_rcp_f32_e32 v39, v39
	v_rcp_f32_e32 v59, v59
	v_add_f32_e32 v52, v52, v101
	v_add_f32_e32 v58, v66, v58
	v_add_f32_e32 v62, v67, v62
	v_cndmask_b32_e32 v66, 0, v38, vcc
	v_cndmask_b32_e32 v67, 0, v22, vcc
	v_cndmask_b32_e32 v101, 0, v100, vcc
	v_cmp_eq_u32_e32 vcc, 3, v14
	v_add_f32_e32 v66, v70, v66
	v_fma_f32 v63, -2.0, v63, v128
	v_cndmask_b32_e32 v70, 0, v100, vcc
	v_add_f32_e32 v50, v50, v70
	v_add_f32_e32 v70, 0x3b086211, v74
	v_fma_f32 v39, -2.0, v39, v108
	v_fmac_f32_e32 v70, -2.0, v59
	v_add_f32_e32 v67, v69, v67
	v_cndmask_b32_e64 v69, 0, 1.0, vcc
	v_cndmask_b32_e32 v38, 0, v38, vcc
	v_cndmask_b32_e32 v22, 0, v22, vcc
	v_add_f32_e32 v59, v63, v39
	v_mul_f32_e32 v103, v70, v70
	v_cmp_eq_u32_e32 vcc, 1, v15
	v_add_f32_e32 v68, v68, v101
	v_add_f32_e32 v101, v59, v70
	v_fmac_f32_e32 v103, v39, v39
	v_mul_f32_e32 v39, v23, v23
	v_cndmask_b32_e64 v59, 0, 1.0, vcc
	v_fmac_f32_e32 v103, v63, v63
	v_add_f32_e32 v51, v59, v51
	v_cndmask_b32_e32 v59, 0, v39, vcc
	v_cndmask_b32_e32 v63, 0, v23, vcc
	v_cndmask_b32_e32 v70, 0, v101, vcc
	v_cmp_eq_u32_e32 vcc, 2, v15
	v_add_f32_e32 v58, v59, v58
	v_add_f32_e32 v52, v52, v70
	v_cndmask_b32_e64 v59, 0, 1.0, vcc
	v_add_f32_e32 v53, v63, v53
	v_add_f32_e32 v59, v59, v62
	v_cndmask_b32_e32 v62, 0, v39, vcc
	v_cndmask_b32_e32 v63, 0, v23, vcc
	v_cndmask_b32_e32 v70, 0, v101, vcc
	v_cmp_eq_u32_e32 vcc, 3, v15
	v_add_f32_e32 v22, v72, v22
	v_add_f32_e32 v38, v73, v38
	v_cndmask_b32_e32 v39, 0, v39, vcc
	v_cndmask_b32_e32 v23, 0, v23, vcc
	v_add_f32_e32 v22, v23, v22
	v_add_f32_e32 v23, v39, v38
	v_mul_f32_e32 v39, 0x4038aa3b, v40
	v_mul_f32_e32 v40, 0x4038aa3b, v60
	v_mul_f32_e32 v64, 0x4038aa3b, v64
	v_exp_f32_e32 v40, v40
	v_exp_f32_e32 v64, v64
	v_exp_f32_e32 v39, v39
	v_add_f32_e32 v60, 0x3b886211, v74
	v_add_f32_e32 v40, 1.0, v40
	v_add_f32_e32 v38, 1.0, v64
	v_add_f32_e32 v39, 1.0, v39
	v_rcp_f32_e32 v40, v40
	v_rcp_f32_e32 v38, v38
	v_rcp_f32_e32 v39, v39
	v_add_f32_e32 v63, v63, v67
	v_fmac_f32_e32 v60, -2.0, v40
	v_fma_f32 v38, -2.0, v38, v128
	v_fma_f32 v39, -2.0, v39, v108
	v_mul_f32_e32 v106, v60, v60
	v_add_f32_e32 v62, v62, v66
	v_cndmask_b32_e64 v66, 0, 1.0, vcc
	v_cndmask_b32_e32 v67, 0, v101, vcc
	v_add_f32_e32 v40, v38, v39
	v_fmac_f32_e32 v106, v39, v39
	v_cmp_eq_u32_e32 vcc, 1, v16
	v_add_f32_e32 v104, v40, v60
	v_fmac_f32_e32 v106, v38, v38
	v_mul_f32_e32 v38, v24, v24
	v_cndmask_b32_e64 v39, 0, 1.0, vcc
	v_add_f32_e32 v39, v39, v51
	v_cndmask_b32_e32 v40, 0, v38, vcc
	v_cndmask_b32_e32 v51, 0, v24, vcc
	v_cndmask_b32_e32 v60, 0, v104, vcc
	v_cmp_eq_u32_e32 vcc, 2, v16
	v_add_f32_e32 v51, v51, v53
	v_add_f32_e32 v52, v52, v60
	v_cndmask_b32_e64 v53, 0, 1.0, vcc
	v_add_f32_e32 v40, v40, v58
	v_add_f32_e32 v53, v53, v59
	v_cndmask_b32_e32 v58, 0, v38, vcc
	v_cndmask_b32_e32 v59, 0, v24, vcc
	v_cndmask_b32_e32 v60, 0, v104, vcc
	v_cmp_eq_u32_e32 vcc, 3, v16
	v_mul_f32_e32 v64, 0x4038aa3b, v65
	v_exp_f32_e32 v64, v64
	v_cndmask_b32_e32 v38, 0, v38, vcc
	v_add_f32_e32 v23, v38, v23
	v_mul_f32_e32 v38, 0x4038aa3b, v41
	v_mul_f32_e32 v41, 0x4038aa3b, v61
	v_exp_f32_e32 v41, v41
	v_exp_f32_e32 v38, v38
	v_cndmask_b32_e32 v24, 0, v24, vcc
	v_add_f32_e32 v22, v24, v22
	v_add_f32_e32 v41, 1.0, v41
	v_add_f32_e32 v38, 1.0, v38
	v_rcp_f32_e32 v41, v41
	v_add_f32_e32 v24, 1.0, v64
	v_rcp_f32_e32 v38, v38
	v_rcp_f32_e32 v24, v24
	v_mul_f32_e32 v33, 0xbfb8aa3b, v33
	v_add_f32_e32 v61, 0x3bcc931a, v74
	v_exp_f32_e32 v33, v33
	v_fmac_f32_e32 v61, -2.0, v41
	v_mul_f32_e32 v30, 0xbfb8aa3b, v30
	v_mul_f32_e32 v31, 0xbfb8aa3b, v31
	v_mul_f32_e32 v32, 0xbfb8aa3b, v32
	v_fmac_f32_e32 v108, -2.0, v38
	v_mul_f32_e32 v107, v61, v61
	v_exp_f32_e32 v30, v30
	v_exp_f32_e32 v31, v31
	v_exp_f32_e32 v32, v32
	v_fma_f32 v24, -2.0, v24, v128
	v_fmac_f32_e32 v107, v108, v108
	v_add_f32_e32 v59, v59, v63
	v_add_f32_e32 v58, v58, v62
	v_cndmask_b32_e64 v62, 0, 1.0, vcc
	v_cndmask_b32_e32 v63, 0, v104, vcc
	v_add_f32_e32 v38, v24, v108
	v_fmac_f32_e32 v107, v24, v24
	v_add_f32_e32 v24, 1.0, v33
	v_cmp_eq_u32_e32 vcc, 1, v17
	v_add_f32_e32 v105, v38, v61
	v_rcp_f32_e32 v33, v24
	v_mul_f32_e32 v24, v25, v25
	v_cndmask_b32_e64 v38, 0, 1.0, vcc
	v_add_f32_e32 v61, v38, v39
	v_cndmask_b32_e32 v38, 0, v24, vcc
	v_cndmask_b32_e32 v39, 0, v25, vcc
	v_cndmask_b32_e32 v41, 0, v105, vcc
	v_cmp_eq_u32_e32 vcc, 2, v17
	v_add_f32_e32 v30, 1.0, v30
	v_add_f32_e32 v69, v71, v69
	v_add_f32_e32 v31, 1.0, v31
	v_add_f32_e32 v32, 1.0, v32
	v_add_f32_e32 v72, v38, v40
	v_cndmask_b32_e64 v38, 0, 1.0, vcc
	v_rcp_f32_e32 v30, v30
	v_rcp_f32_e32 v31, v31
	v_add_f32_e32 v66, v66, v69
	v_rcp_f32_e32 v32, v32
	v_add_f32_e32 v71, v39, v51
	v_add_f32_e32 v73, v38, v53
	v_cndmask_b32_e32 v38, 0, v24, vcc
	v_cndmask_b32_e32 v39, 0, v25, vcc
	v_cndmask_b32_e32 v40, 0, v105, vcc
	v_cmp_eq_u32_e32 vcc, 3, v17
	v_add_f32_e32 v68, v68, v70
	v_add_f32_e32 v50, v50, v67
	v_add_f32_e32 v62, v62, v66
	v_add_f32_e32 v58, v38, v58
	v_cndmask_b32_e64 v38, 0, 1.0, vcc
	v_add_f32_e32 v60, v68, v60
	v_add_f32_e32 v50, v50, v63
	v_add_f32_e32 v74, v38, v62
	v_cndmask_b32_e32 v24, 0, v24, vcc
	v_cndmask_b32_e32 v25, 0, v25, vcc
	v_cndmask_b32_e32 v38, 0, v105, vcc
	v_add_f32_e32 v70, v52, v41
	v_add_f32_e32 v60, v60, v40
	v_add_f32_e32 v59, v39, v59
	v_add_f32_e32 v109, v50, v38
	v_add_f32_e32 v111, v25, v22
	v_add_f32_e32 v112, v24, v23
	ds_write_b128 v1, v[30:33] offset:36864
	s_mov_b32 s10, 0xf000
	v_add_co_u32_e32 v22, vcc, s10, v130
	s_mov_b32 s11, 0xc8f000
	s_nop 0
	v_addc_co_u32_e32 v23, vcc, 0, v131, vcc
	v_add_co_u32_e32 v24, vcc, s11, v130
	s_mov_b32 s11, 0x190f000
	s_nop 0
	v_addc_co_u32_e32 v25, vcc, 0, v131, vcc
	global_load_dwordx4 v[66:69], v[22:23], off nt
	global_load_dwordx4 v[50:53], v[24:25], off nt
	v_add_co_u32_e32 v22, vcc, s11, v130
	s_mov_b32 s11, 0x258f000
	s_nop 0
	v_addc_co_u32_e32 v23, vcc, 0, v131, vcc
	v_add_co_u32_e32 v24, vcc, s11, v130
	s_mov_b32 s11, 0x320f000
	s_nop 0
	v_addc_co_u32_e32 v25, vcc, 0, v131, vcc
	global_load_dwordx4 v[62:65], v[22:23], off nt
	global_load_dwordx4 v[30:33], v[24:25], off nt
	v_add_co_u32_e32 v22, vcc, s11, v130
	v_or_b32_e32 v116, 0xc00, v0
	s_nop 0
	v_addc_co_u32_e32 v23, vcc, 0, v131, vcc
	global_load_dwordx4 v[38:41], v[22:23], off nt
	v_add_co_u32_e32 v22, vcc, s10, v132
	v_add_u32_e32 v108, s8, v116
	s_nop 0
	v_addc_co_u32_e32 v23, vcc, 0, v133, vcc
	global_load_dwordx4 v[22:25], v[22:23], off nt
	s_waitcnt vmcnt(11)
	v_mul_f32_e32 v54, 0x4038aa3b, v54
	s_waitcnt vmcnt(10)
	v_mul_f32_e32 v42, 0x4038aa3b, v42
	s_waitcnt vmcnt(9)
	v_mul_f32_e32 v46, 0x4038aa3b, v46
	v_mul_u32_u24_sdwa v110, v108, s6 dst_sel:DWORD dst_unused:UNUSED_PAD src0_sel:WORD_0 src1_sel:DWORD
	v_exp_f32_e32 v54, v54
	v_exp_f32_e32 v42, v42
	v_exp_f32_e32 v46, v46
	v_lshrrev_b32_e32 v110, 23, v110
	v_cvt_f32_u32_e32 v113, v110
	v_mul_i32_i24_e32 v110, 0xffffff60, v110
	v_add_lshl_u32 v108, v110, v108, 2
	v_cvt_f32_i32_e32 v108, v108
	v_add_f32_e32 v54, 1.0, v54
	v_add_f32_e32 v42, 1.0, v42
	v_add_f32_e32 v46, 1.0, v46
	v_rcp_f32_e32 v54, v54
	v_rcp_f32_e32 v42, v42
	v_rcp_f32_e32 v46, v46
	v_mul_f32_e32 v55, 0x4038aa3b, v55
	v_mul_f32_e32 v43, 0x4038aa3b, v43
	v_mul_f32_e32 v47, 0x4038aa3b, v47
	v_fma_f32 v117, v113, s7, 1.0
	v_fma_f32 v113, v108, s9, 1.0
	v_exp_f32_e32 v55, v55
	v_exp_f32_e32 v43, v43
	v_exp_f32_e32 v47, v47
	v_fma_f32 v54, -2.0, v54, v128
	v_fma_f32 v42, -2.0, v42, v117
	v_fma_f32 v46, -2.0, v46, v113
	v_add_f32_e32 v108, v54, v42
	v_mul_f32_e32 v110, v46, v46
	s_waitcnt vmcnt(6)
	v_cmp_eq_u32_e32 vcc, 1, v18
	v_add_f32_e32 v108, v108, v46
	v_fmac_f32_e32 v110, v42, v42
	v_mul_f32_e32 v42, v26, v26
	v_cndmask_b32_e64 v46, 0, 1.0, vcc
	v_fmac_f32_e32 v110, v54, v54
	v_add_f32_e32 v46, v61, v46
	v_cndmask_b32_e32 v54, 0, v42, vcc
	v_cndmask_b32_e32 v61, 0, v26, vcc
	v_cndmask_b32_e32 v114, 0, v108, vcc
	v_cmp_eq_u32_e32 vcc, 2, v18
	v_add_f32_e32 v55, 1.0, v55
	v_add_f32_e32 v43, 1.0, v43
	v_add_f32_e32 v47, 1.0, v47
	v_add_f32_e32 v61, v71, v61
	v_cndmask_b32_e64 v71, 0, 1.0, vcc
	v_rcp_f32_e32 v55, v55
	v_rcp_f32_e32 v43, v43
	v_rcp_f32_e32 v47, v47
	v_add_f32_e32 v70, v70, v114
	v_add_f32_e32 v54, v72, v54
	v_add_f32_e32 v71, v73, v71
	v_cndmask_b32_e32 v72, 0, v42, vcc
	v_cndmask_b32_e32 v73, 0, v26, vcc
	v_cndmask_b32_e32 v114, 0, v108, vcc
	v_cmp_eq_u32_e32 vcc, 3, v18
	v_add_f32_e32 v58, v58, v72
	v_fma_f32 v55, -2.0, v55, v128
	v_cndmask_b32_e64 v72, 0, 1.0, vcc
	v_add_f32_e32 v72, v74, v72
	v_add_f32_e32 v74, 0x3b086211, v113
	v_cndmask_b32_e32 v26, 0, v26, vcc
	v_fma_f32 v43, -2.0, v43, v117
	v_fmac_f32_e32 v74, -2.0, v47
	v_add_f32_e32 v59, v59, v73
	v_cndmask_b32_e32 v42, 0, v42, vcc
	v_cndmask_b32_e32 v73, 0, v108, vcc
	v_add_f32_e32 v26, v111, v26
	v_add_f32_e32 v47, v55, v43
	v_mul_f32_e32 v111, v74, v74
	v_cmp_eq_u32_e32 vcc, 1, v19
	v_add_f32_e32 v73, v109, v73
	v_add_f32_e32 v109, v47, v74
	v_fmac_f32_e32 v111, v43, v43
	v_mul_f32_e32 v43, v27, v27
	v_cndmask_b32_e64 v47, 0, 1.0, vcc
	v_fmac_f32_e32 v111, v55, v55
	v_add_f32_e32 v46, v47, v46
	v_cndmask_b32_e32 v47, 0, v43, vcc
	v_cndmask_b32_e32 v55, 0, v27, vcc
	v_cndmask_b32_e32 v74, 0, v109, vcc
	v_cmp_eq_u32_e32 vcc, 2, v19
	v_add_f32_e32 v47, v47, v54
	v_add_f32_e32 v70, v70, v74
	v_cndmask_b32_e64 v54, 0, 1.0, vcc
	v_add_f32_e32 v55, v55, v61
	v_add_f32_e32 v54, v54, v71
	v_cndmask_b32_e32 v61, 0, v43, vcc
	v_cndmask_b32_e32 v71, 0, v27, vcc
	v_cndmask_b32_e32 v74, 0, v109, vcc
	v_cmp_eq_u32_e32 vcc, 3, v19
	v_add_f32_e32 v42, v112, v42
	v_mul_f32_e32 v56, 0x4038aa3b, v56
	v_cndmask_b32_e32 v43, 0, v43, vcc
	v_cndmask_b32_e32 v27, 0, v27, vcc
	v_add_f32_e32 v26, v27, v26
	v_add_f32_e32 v27, v43, v42
	v_mul_f32_e32 v43, 0x4038aa3b, v44
	v_mul_f32_e32 v44, 0x4038aa3b, v48
	v_exp_f32_e32 v44, v44
	v_exp_f32_e32 v56, v56
	v_exp_f32_e32 v43, v43
	v_add_f32_e32 v48, 0x3b886211, v113
	v_add_f32_e32 v44, 1.0, v44
	v_add_f32_e32 v42, 1.0, v56
	v_add_f32_e32 v43, 1.0, v43
	v_rcp_f32_e32 v44, v44
	v_rcp_f32_e32 v42, v42
	v_rcp_f32_e32 v43, v43
	v_add_f32_e32 v60, v60, v114
	v_fmac_f32_e32 v48, -2.0, v44
	v_fma_f32 v42, -2.0, v42, v128
	v_fma_f32 v43, -2.0, v43, v117
	v_mul_f32_e32 v114, v48, v48
	v_add_f32_e32 v59, v71, v59
	v_add_f32_e32 v58, v61, v58
	v_cndmask_b32_e64 v61, 0, 1.0, vcc
	v_cndmask_b32_e32 v71, 0, v109, vcc
	v_add_f32_e32 v44, v42, v43
	v_fmac_f32_e32 v114, v43, v43
	v_cmp_eq_u32_e32 vcc, 1, v20
	v_add_f32_e32 v112, v44, v48
	v_fmac_f32_e32 v114, v42, v42
	v_mul_f32_e32 v42, v28, v28
	v_cndmask_b32_e64 v43, 0, 1.0, vcc
	v_add_f32_e32 v43, v43, v46
	v_cndmask_b32_e32 v44, 0, v42, vcc
	v_cndmask_b32_e32 v46, 0, v28, vcc
	v_cndmask_b32_e32 v48, 0, v112, vcc
	v_cmp_eq_u32_e32 vcc, 2, v20
	v_add_f32_e32 v44, v44, v47
	v_add_f32_e32 v46, v46, v55
	v_cndmask_b32_e64 v47, 0, 1.0, vcc
	v_add_f32_e32 v47, v47, v54
	v_cndmask_b32_e32 v54, 0, v42, vcc
	v_cndmask_b32_e32 v55, 0, v28, vcc
	v_cndmask_b32_e32 v56, 0, v112, vcc
	v_cmp_eq_u32_e32 vcc, 3, v20
	v_mul_f32_e32 v57, 0x4038aa3b, v57
	v_exp_f32_e32 v57, v57
	v_cndmask_b32_e32 v42, 0, v42, vcc
	v_add_f32_e32 v27, v42, v27
	v_mul_f32_e32 v42, 0x4038aa3b, v45
	v_mul_f32_e32 v45, 0x4038aa3b, v49
	v_exp_f32_e32 v45, v45
	v_exp_f32_e32 v42, v42
	v_cndmask_b32_e32 v28, 0, v28, vcc
	v_add_f32_e32 v26, v28, v26
	v_add_f32_e32 v45, 1.0, v45
	v_add_f32_e32 v42, 1.0, v42
	v_rcp_f32_e32 v45, v45
	v_add_f32_e32 v28, 1.0, v57
	v_rcp_f32_e32 v42, v42
	v_rcp_f32_e32 v28, v28
	v_mul_f32_e32 v37, 0xbfb8aa3b, v37
	v_add_f32_e32 v49, 0x3bcc931a, v113
	v_exp_f32_e32 v37, v37
	v_fmac_f32_e32 v49, -2.0, v45
	v_mul_f32_e32 v34, 0xbfb8aa3b, v34
	v_mul_f32_e32 v35, 0xbfb8aa3b, v35
	v_mul_f32_e32 v36, 0xbfb8aa3b, v36
	v_fmac_f32_e32 v117, -2.0, v42
	v_mul_f32_e32 v115, v49, v49
	v_exp_f32_e32 v34, v34
	v_exp_f32_e32 v35, v35
	v_exp_f32_e32 v36, v36
	v_fma_f32 v28, -2.0, v28, v128
	v_fmac_f32_e32 v115, v117, v117
	v_add_f32_e32 v55, v55, v59
	v_add_f32_e32 v54, v54, v58
	v_cndmask_b32_e64 v58, 0, 1.0, vcc
	v_cndmask_b32_e32 v59, 0, v112, vcc
	v_add_f32_e32 v42, v28, v117
	v_fmac_f32_e32 v115, v28, v28
	v_add_f32_e32 v28, 1.0, v37
	v_cmp_eq_u32_e32 vcc, 1, v21
	v_add_f32_e32 v113, v42, v49
	v_rcp_f32_e32 v37, v28
	v_mul_f32_e32 v28, v29, v29
	v_cndmask_b32_e64 v42, 0, 1.0, vcc
	v_add_f32_e32 v48, v70, v48
	v_add_f32_e32 v70, v42, v43
	v_cndmask_b32_e32 v42, 0, v28, vcc
	v_cndmask_b32_e32 v43, 0, v29, vcc
	v_cndmask_b32_e32 v45, 0, v113, vcc
	v_cmp_eq_u32_e32 vcc, 2, v21
	v_add_f32_e32 v34, 1.0, v34
	v_add_f32_e32 v35, 1.0, v35
	v_add_f32_e32 v71, v73, v71
	v_add_f32_e32 v36, 1.0, v36
	v_add_f32_e32 v73, v42, v44
	v_cndmask_b32_e64 v42, 0, 1.0, vcc
	v_rcp_f32_e32 v34, v34
	v_rcp_f32_e32 v35, v35
	v_add_f32_e32 v60, v60, v74
	v_add_f32_e32 v61, v61, v72
	v_rcp_f32_e32 v36, v36
	v_add_f32_e32 v72, v43, v46
	v_add_f32_e32 v74, v42, v47
	v_cndmask_b32_e32 v42, 0, v28, vcc
	v_cndmask_b32_e32 v43, 0, v29, vcc
	v_cndmask_b32_e32 v44, 0, v113, vcc
	v_cmp_eq_u32_e32 vcc, 3, v21
	v_add_f32_e32 v58, v58, v61
	v_add_f32_e32 v120, v42, v54
	v_cndmask_b32_e64 v42, 0, 1.0, vcc
	v_add_f32_e32 v56, v60, v56
	v_add_f32_e32 v59, v71, v59
	v_add_f32_e32 v121, v42, v58
	v_cndmask_b32_e32 v28, 0, v28, vcc
	v_cndmask_b32_e32 v29, 0, v29, vcc
	v_cndmask_b32_e32 v42, 0, v113, vcc
	v_add_f32_e32 v71, v48, v45
	v_add_f32_e32 v117, v56, v44
	v_add_f32_e32 v119, v43, v55
	v_add_f32_e32 v122, v59, v42
	v_add_f32_e32 v123, v29, v26
	v_add_f32_e32 v124, v28, v27
	v_lshl_add_u32 v26, v116, 4, v136
	ds_write_b128 v26, v[34:37] offset:49152
	s_mov_b32 s10, 0x12000
	v_add_co_u32_e32 v26, vcc, s10, v130
	s_mov_b32 s11, 0xc92000
	s_nop 0
	v_addc_co_u32_e32 v27, vcc, 0, v131, vcc
	v_add_co_u32_e32 v28, vcc, s11, v130
	s_mov_b32 s11, 0x1912000
	s_nop 0
	v_addc_co_u32_e32 v29, vcc, 0, v131, vcc
	global_load_dwordx4 v[58:61], v[26:27], off nt
	global_load_dwordx4 v[46:49], v[28:29], off nt
	v_add_co_u32_e32 v26, vcc, s11, v130
	s_mov_b32 s11, 0x2592000
	s_nop 0
	v_addc_co_u32_e32 v27, vcc, 0, v131, vcc
	v_add_co_u32_e32 v28, vcc, s11, v130
	s_mov_b32 s11, 0x3212000
	s_nop 0
	v_addc_co_u32_e32 v29, vcc, 0, v131, vcc
	global_load_dwordx4 v[54:57], v[26:27], off nt
	global_load_dwordx4 v[34:37], v[28:29], off nt
	v_add_co_u32_e32 v26, vcc, s11, v130
	v_add_u32_e32 v116, 0xf00, v137
	s_nop 0
	v_addc_co_u32_e32 v27, vcc, 0, v131, vcc
	global_load_dwordx4 v[42:45], v[26:27], off nt
	v_add_co_u32_e32 v26, vcc, s10, v132
	s_waitcnt vmcnt(10)
	v_mul_f32_e32 v66, 0x4038aa3b, v66
	v_addc_co_u32_e32 v27, vcc, 0, v133, vcc
	global_load_dwordx4 v[26:29], v[26:27], off nt
	s_waitcnt vmcnt(10)
	v_mul_f32_e32 v50, 0x4038aa3b, v50
	s_waitcnt vmcnt(9)
	v_mul_f32_e32 v62, 0x4038aa3b, v62
	v_mul_u32_u24_sdwa v118, v116, s6 dst_sel:DWORD dst_unused:UNUSED_PAD src0_sel:WORD_0 src1_sel:DWORD
	v_exp_f32_e32 v66, v66
	v_exp_f32_e32 v50, v50
	v_exp_f32_e32 v62, v62
	v_lshrrev_b32_e32 v118, 23, v118
	v_cvt_f32_u32_e32 v125, v118
	v_mul_i32_i24_e32 v118, 0xffffff60, v118
	v_add_lshl_u32 v116, v118, v116, 2
	v_cvt_f32_i32_e32 v116, v116
	v_add_f32_e32 v66, 1.0, v66
	v_add_f32_e32 v50, 1.0, v50
	v_add_f32_e32 v62, 1.0, v62
	v_rcp_f32_e32 v66, v66
	v_rcp_f32_e32 v50, v50
	v_rcp_f32_e32 v62, v62
	v_mul_f32_e32 v67, 0x4038aa3b, v67
	v_mul_f32_e32 v51, 0x4038aa3b, v51
	v_exp_f32_e32 v67, v67
	v_exp_f32_e32 v51, v51
	v_mul_f32_e32 v63, 0x4038aa3b, v63
	v_exp_f32_e32 v63, v63
	v_fma_f32 v125, v125, s7, 1.0
	v_fma_f32 v126, v116, s9, 1.0
	v_fma_f32 v66, -2.0, v66, v128
	v_fma_f32 v50, -2.0, v50, v125
	v_fma_f32 v62, -2.0, v62, v126
	v_add_f32_e32 v116, v66, v50
	v_mul_f32_e32 v118, v62, v62
	s_waitcnt vmcnt(6)
	v_cmp_eq_u32_e32 vcc, 1, v22
	v_add_f32_e32 v67, 1.0, v67
	v_add_f32_e32 v51, 1.0, v51
	v_add_f32_e32 v116, v116, v62
	v_fmac_f32_e32 v118, v50, v50
	v_mul_f32_e32 v50, v30, v30
	v_cndmask_b32_e64 v62, 0, 1.0, vcc
	v_rcp_f32_e32 v67, v67
	v_rcp_f32_e32 v51, v51
	v_add_f32_e32 v63, 1.0, v63
	v_fmac_f32_e32 v118, v66, v66
	v_add_f32_e32 v62, v70, v62
	v_cndmask_b32_e32 v66, 0, v50, vcc
	v_cndmask_b32_e32 v70, 0, v30, vcc
	v_cndmask_b32_e32 v127, 0, v116, vcc
	v_cmp_eq_u32_e32 vcc, 2, v22
	v_rcp_f32_e32 v63, v63
	v_add_f32_e32 v70, v72, v70
	v_cndmask_b32_e64 v72, 0, 1.0, vcc
	v_add_f32_e32 v71, v71, v127
	v_add_f32_e32 v66, v73, v66
	v_add_f32_e32 v72, v74, v72
	v_cndmask_b32_e32 v73, 0, v50, vcc
	v_cndmask_b32_e32 v74, 0, v30, vcc
	v_cndmask_b32_e32 v127, 0, v116, vcc
	v_cmp_eq_u32_e32 vcc, 3, v22
	v_add_f32_e32 v127, v117, v127
	v_add_f32_e32 v74, v119, v74
	v_cndmask_b32_e64 v117, 0, 1.0, vcc
	v_add_f32_e32 v119, 0x3b086211, v126
	v_fma_f32 v67, -2.0, v67, v128
	v_fma_f32 v51, -2.0, v51, v125
	v_add_f32_e32 v73, v120, v73
	v_add_f32_e32 v120, v121, v117
	v_cndmask_b32_e32 v117, 0, v116, vcc
	v_fmac_f32_e32 v119, -2.0, v63
	v_add_f32_e32 v63, v67, v51
	v_cndmask_b32_e32 v50, 0, v50, vcc
	v_cndmask_b32_e32 v30, 0, v30, vcc
	v_add_f32_e32 v121, v122, v117
	v_add_f32_e32 v117, v63, v119
	v_mul_f32_e32 v119, v119, v119
	v_cmp_eq_u32_e32 vcc, 1, v23
	v_fmac_f32_e32 v119, v51, v51
	v_mul_f32_e32 v51, v31, v31
	v_cndmask_b32_e64 v63, 0, 1.0, vcc
	v_fmac_f32_e32 v119, v67, v67
	v_add_f32_e32 v62, v63, v62
	v_cndmask_b32_e32 v63, 0, v51, vcc
	v_cndmask_b32_e32 v67, 0, v31, vcc
	v_cndmask_b32_e32 v122, 0, v117, vcc
	v_cmp_eq_u32_e32 vcc, 2, v23
	v_add_f32_e32 v63, v63, v66
	v_add_f32_e32 v71, v71, v122
	v_cndmask_b32_e64 v66, 0, 1.0, vcc
	v_add_f32_e32 v67, v67, v70
	v_add_f32_e32 v66, v66, v72
	v_cndmask_b32_e32 v70, 0, v51, vcc
	v_cndmask_b32_e32 v72, 0, v31, vcc
	v_cndmask_b32_e32 v122, 0, v117, vcc
	v_cmp_eq_u32_e32 vcc, 3, v23
	v_add_f32_e32 v30, v123, v30
	v_add_f32_e32 v50, v124, v50
	v_cndmask_b32_e32 v51, 0, v51, vcc
	v_cndmask_b32_e32 v31, 0, v31, vcc
	v_add_f32_e32 v30, v31, v30
	v_add_f32_e32 v31, v51, v50
	v_mul_f32_e32 v51, 0x4038aa3b, v52
	v_mul_f32_e32 v52, 0x4038aa3b, v64
	v_mul_f32_e32 v68, 0x4038aa3b, v68
	v_exp_f32_e32 v52, v52
	v_exp_f32_e32 v68, v68
	v_exp_f32_e32 v51, v51
	v_add_f32_e32 v64, 0x3b886211, v126
	v_add_f32_e32 v52, 1.0, v52
	v_add_f32_e32 v50, 1.0, v68
	v_add_f32_e32 v51, 1.0, v51
	v_rcp_f32_e32 v52, v52
	v_rcp_f32_e32 v50, v50
	v_rcp_f32_e32 v51, v51
	v_add_f32_e32 v123, v127, v122
	v_fmac_f32_e32 v64, -2.0, v52
	v_fma_f32 v50, -2.0, v50, v128
	v_fma_f32 v51, -2.0, v51, v125
	v_mul_f32_e32 v122, v64, v64
	v_add_f32_e32 v72, v72, v74
	v_add_f32_e32 v70, v70, v73
	v_cndmask_b32_e64 v73, 0, 1.0, vcc
	v_cndmask_b32_e32 v74, 0, v117, vcc
	v_add_f32_e32 v52, v50, v51
	v_fmac_f32_e32 v122, v51, v51
	v_cmp_eq_u32_e32 vcc, 1, v24
	v_add_f32_e32 v73, v73, v120
	v_add_f32_e32 v120, v52, v64
	v_fmac_f32_e32 v122, v50, v50
	v_mul_f32_e32 v50, v32, v32
	v_cndmask_b32_e64 v51, 0, 1.0, vcc
	v_add_f32_e32 v51, v51, v62
	v_cndmask_b32_e32 v52, 0, v50, vcc
	v_cndmask_b32_e32 v62, 0, v32, vcc
	v_cndmask_b32_e32 v64, 0, v120, vcc
	v_cmp_eq_u32_e32 vcc, 2, v24
	v_add_f32_e32 v52, v52, v63
	v_add_f32_e32 v62, v62, v67
	v_cndmask_b32_e64 v63, 0, 1.0, vcc
	v_add_f32_e32 v63, v63, v66
	v_cndmask_b32_e32 v66, 0, v50, vcc
	v_cndmask_b32_e32 v67, 0, v32, vcc
	v_cndmask_b32_e32 v68, 0, v120, vcc
	v_cmp_eq_u32_e32 vcc, 3, v24
	v_mul_f32_e32 v69, 0x4038aa3b, v69
	v_exp_f32_e32 v69, v69
	v_cndmask_b32_e32 v50, 0, v50, vcc
	v_add_f32_e32 v31, v50, v31
	v_mul_f32_e32 v50, 0x4038aa3b, v53
	v_mul_f32_e32 v53, 0x4038aa3b, v65
	v_exp_f32_e32 v53, v53
	v_exp_f32_e32 v50, v50
	v_cndmask_b32_e32 v32, 0, v32, vcc
	v_add_f32_e32 v30, v32, v30
	v_add_f32_e32 v53, 1.0, v53
	v_add_f32_e32 v50, 1.0, v50
	v_rcp_f32_e32 v53, v53
	v_add_f32_e32 v32, 1.0, v69
	v_rcp_f32_e32 v50, v50
	v_rcp_f32_e32 v32, v32
	v_mul_f32_e32 v41, 0xbfb8aa3b, v41
	v_add_f32_e32 v65, 0x3bcc931a, v126
	v_exp_f32_e32 v41, v41
	v_fmac_f32_e32 v65, -2.0, v53
	v_mul_f32_e32 v38, 0xbfb8aa3b, v38
	v_mul_f32_e32 v39, 0xbfb8aa3b, v39
	v_mul_f32_e32 v40, 0xbfb8aa3b, v40
	v_add_f32_e32 v68, v123, v68
	v_fmac_f32_e32 v125, -2.0, v50
	v_mul_f32_e32 v123, v65, v65
	v_exp_f32_e32 v38, v38
	v_exp_f32_e32 v39, v39
	v_exp_f32_e32 v40, v40
	v_fma_f32 v32, -2.0, v32, v128
	v_fmac_f32_e32 v123, v125, v125
	v_add_f32_e32 v64, v71, v64
	v_add_f32_e32 v66, v66, v70
	v_cndmask_b32_e64 v70, 0, 1.0, vcc
	v_cndmask_b32_e32 v71, 0, v120, vcc
	v_add_f32_e32 v50, v32, v125
	v_fmac_f32_e32 v123, v32, v32
	v_add_f32_e32 v32, 1.0, v41
	v_cmp_eq_u32_e32 vcc, 1, v25
	v_add_f32_e32 v74, v121, v74
	v_add_f32_e32 v121, v50, v65
	v_rcp_f32_e32 v41, v32
	v_mul_f32_e32 v32, v33, v33
	v_cndmask_b32_e64 v50, 0, 1.0, vcc
	v_add_f32_e32 v71, v74, v71
	v_add_f32_e32 v74, v50, v51
	v_cndmask_b32_e32 v50, 0, v32, vcc
	v_cndmask_b32_e32 v51, 0, v33, vcc
	v_cndmask_b32_e32 v53, 0, v121, vcc
	v_cmp_eq_u32_e32 vcc, 2, v25
	v_add_f32_e32 v38, 1.0, v38
	v_add_f32_e32 v39, 1.0, v39
	v_add_f32_e32 v40, 1.0, v40
	v_add_f32_e32 v139, v50, v52
	v_cndmask_b32_e64 v50, 0, 1.0, vcc
	v_rcp_f32_e32 v38, v38
	v_rcp_f32_e32 v39, v39
	v_rcp_f32_e32 v40, v40
	v_add_f32_e32 v138, v51, v62
	v_add_f32_e32 v140, v50, v63
	v_cndmask_b32_e32 v50, 0, v32, vcc
	v_cndmask_b32_e32 v51, 0, v33, vcc
	v_cndmask_b32_e32 v52, 0, v121, vcc
	v_cmp_eq_u32_e32 vcc, 3, v25
	v_add_f32_e32 v70, v70, v73
	v_add_f32_e32 v143, v50, v66
	v_cndmask_b32_e64 v50, 0, 1.0, vcc
	v_add_f32_e32 v67, v67, v72
	v_add_f32_e32 v144, v50, v70
	v_cndmask_b32_e32 v50, 0, v121, vcc
	v_add_f32_e32 v135, v64, v53
	v_add_f32_e32 v141, v68, v52
	v_add_f32_e32 v142, v51, v67
	v_cndmask_b32_e32 v32, 0, v32, vcc
	v_cndmask_b32_e32 v33, 0, v33, vcc
	v_add_f32_e32 v145, v71, v50
	v_add_f32_e32 v146, v33, v30
	v_add_f32_e32 v147, v32, v31
	ds_write_b128 v1, v[38:41] offset:61440
	s_mov_b32 s10, 0x15000
	v_add_co_u32_e32 v30, vcc, s10, v130
	s_mov_b32 s11, 0xc95000
	s_nop 0
	v_addc_co_u32_e32 v31, vcc, 0, v131, vcc
	v_add_co_u32_e32 v32, vcc, s11, v130
	s_mov_b32 s11, 0x1915000
	s_nop 0
	v_addc_co_u32_e32 v33, vcc, 0, v131, vcc
	global_load_dwordx4 v[70:73], v[30:31], off nt
	global_load_dwordx4 v[62:65], v[32:33], off nt
	v_add_co_u32_e32 v30, vcc, s11, v130
	s_mov_b32 s11, 0x2595000
	s_nop 0
	v_addc_co_u32_e32 v31, vcc, 0, v131, vcc
	v_add_co_u32_e32 v32, vcc, s11, v130
	s_mov_b32 s11, 0x3215000
	s_nop 0
	v_addc_co_u32_e32 v33, vcc, 0, v131, vcc
	global_load_dwordx4 v[66:69], v[30:31], off nt
	global_load_dwordx4 v[38:41], v[32:33], off nt
	v_add_co_u32_e32 v30, vcc, s11, v130
	s_waitcnt vmcnt(8)
	v_mul_f32_e32 v46, 0x4038aa3b, v46
	v_addc_co_u32_e32 v31, vcc, 0, v131, vcc
	global_load_dwordx4 v[50:53], v[30:31], off nt
	v_add_co_u32_e32 v30, vcc, s10, v132
	v_add_u32_e32 v124, 0x1200, v137
	s_nop 0
	v_addc_co_u32_e32 v31, vcc, 0, v133, vcc
	v_mul_f32_e32 v58, 0x4038aa3b, v58
	v_exp_f32_e32 v46, v46
	s_waitcnt vmcnt(8)
	v_mul_f32_e32 v54, 0x4038aa3b, v54
	global_load_dwordx4 v[30:33], v[30:31], off nt
	v_mul_u32_u24_sdwa v125, v124, s6 dst_sel:DWORD dst_unused:UNUSED_PAD src0_sel:WORD_0 src1_sel:DWORD
	v_exp_f32_e32 v58, v58
	v_exp_f32_e32 v54, v54
	v_lshrrev_b32_e32 v125, 23, v125
	v_mul_i32_i24_e32 v126, 0xffffff60, v125
	v_add_lshl_u32 v124, v126, v124, 2
	v_add_f32_e32 v46, 1.0, v46
	v_cvt_f32_u32_e32 v127, v125
	v_cvt_f32_i32_e32 v126, v124
	v_add_f32_e32 v58, 1.0, v58
	v_rcp_f32_e32 v125, v46
	v_add_f32_e32 v46, 1.0, v54
	v_rcp_f32_e32 v124, v58
	v_rcp_f32_e32 v46, v46
	v_fma_f32 v129, v127, s7, 1.0
	v_fma_f32 v54, v126, s9, 1.0
	v_pk_fma_f32 v[126:127], v[124:125], -2.0, v[128:129] op_sel_hi:[1,0,1]
	v_fma_f32 v46, -2.0, v46, v54
	v_add_f32_e32 v58, v126, v127
	v_mul_f32_e32 v124, v46, v46
	s_waitcnt vmcnt(6)
	v_cmp_eq_u32_e32 vcc, 1, v26
	v_add_f32_e32 v58, v58, v46
	v_fmac_f32_e32 v124, v127, v127
	v_mul_f32_e32 v46, v34, v34
	v_cndmask_b32_e64 v125, 0, 1.0, vcc
	v_fmac_f32_e32 v124, v126, v126
	v_add_f32_e32 v74, v74, v125
	v_cndmask_b32_e32 v125, 0, v46, vcc
	v_cndmask_b32_e32 v126, 0, v34, vcc
	v_cndmask_b32_e32 v127, 0, v58, vcc
	v_cmp_eq_u32_e32 vcc, 2, v26
	v_add_f32_e32 v127, v135, v127
	v_add_f32_e32 v135, v139, v125
	v_cndmask_b32_e64 v125, 0, 1.0, vcc
	v_add_f32_e32 v126, v138, v126
	v_add_f32_e32 v138, v140, v125
	v_cndmask_b32_e32 v125, 0, v46, vcc
	v_cndmask_b32_e32 v139, 0, v34, vcc
	v_cndmask_b32_e32 v140, 0, v58, vcc
	v_cmp_eq_u32_e32 vcc, 3, v26
	v_add_f32_e32 v140, v141, v140
	v_add_f32_e32 v141, v143, v125
	v_cndmask_b32_e64 v125, 0, 1.0, vcc
	v_add_f32_e32 v139, v142, v139
	v_add_f32_e32 v142, v144, v125
	v_cndmask_b32_e32 v125, 0, v46, vcc
	v_mul_f32_e32 v46, 0x4038aa3b, v59
	v_mul_f32_e32 v47, 0x4038aa3b, v47
	v_exp_f32_e32 v46, v46
	v_exp_f32_e32 v47, v47
	v_mul_f32_e32 v55, 0x4038aa3b, v55
	v_exp_f32_e32 v55, v55
	v_add_f32_e32 v46, 1.0, v46
	v_add_f32_e32 v47, 1.0, v47
	v_rcp_f32_e32 v46, v46
	v_rcp_f32_e32 v47, v47
	v_add_f32_e32 v55, 1.0, v55
	v_rcp_f32_e32 v55, v55
	v_add_f32_e32 v144, v147, v125
	v_add_f32_e32 v125, 0x3b086211, v54
	v_pk_fma_f32 v[46:47], v[46:47], -2.0, v[128:129] op_sel_hi:[1,0,1]
	v_cndmask_b32_e32 v59, 0, v58, vcc
	v_fmac_f32_e32 v125, -2.0, v55
	v_add_f32_e32 v55, v46, v47
	v_add_f32_e32 v143, v145, v59
	v_add_f32_e32 v59, v55, v125
	v_mul_f32_e32 v125, v125, v125
	v_cndmask_b32_e32 v34, 0, v34, vcc
	v_fmac_f32_e32 v125, v47, v47
	v_cmp_eq_u32_e32 vcc, 1, v27
	v_fmac_f32_e32 v125, v46, v46
	v_mul_f32_e32 v46, v35, v35
	v_cndmask_b32_e64 v47, 0, 1.0, vcc
	v_add_f32_e32 v47, v47, v74
	v_cndmask_b32_e32 v55, 0, v46, vcc
	v_cndmask_b32_e32 v74, 0, v35, vcc
	v_cndmask_b32_e32 v145, 0, v59, vcc
	v_cmp_eq_u32_e32 vcc, 2, v27
	v_add_f32_e32 v74, v74, v126
	v_add_f32_e32 v127, v127, v145
	v_cndmask_b32_e64 v126, 0, 1.0, vcc
	v_add_f32_e32 v55, v55, v135
	v_add_f32_e32 v135, v126, v138
	v_cndmask_b32_e32 v126, 0, v46, vcc
	v_cndmask_b32_e32 v138, 0, v35, vcc
	v_cndmask_b32_e32 v145, 0, v59, vcc
	v_cmp_eq_u32_e32 vcc, 3, v27
	v_add_f32_e32 v138, v138, v139
	v_add_f32_e32 v139, v126, v141
	v_cndmask_b32_e64 v126, 0, 1.0, vcc
	v_add_f32_e32 v34, v146, v34
	v_add_f32_e32 v141, v126, v142
	v_cndmask_b32_e32 v35, 0, v35, vcc
	v_cndmask_b32_e32 v126, 0, v59, vcc
	v_add_f32_e32 v142, v143, v126
	v_add_f32_e32 v143, v35, v34
	v_mul_f32_e32 v35, 0x4038aa3b, v48
	v_mul_f32_e32 v48, 0x4038aa3b, v56
	v_mul_f32_e32 v60, 0x4038aa3b, v60
	v_exp_f32_e32 v48, v48
	v_exp_f32_e32 v60, v60
	v_exp_f32_e32 v35, v35
	v_mul_f32_e32 v44, 0xbfb8aa3b, v44
	v_add_f32_e32 v48, 1.0, v48
	v_add_f32_e32 v34, 1.0, v60
	v_add_f32_e32 v35, 1.0, v35
	v_rcp_f32_e32 v48, v48
	v_rcp_f32_e32 v34, v34
	v_rcp_f32_e32 v35, v35
	v_add_f32_e32 v56, 0x3b886211, v54
	v_exp_f32_e32 v44, v44
	v_fmac_f32_e32 v56, -2.0, v48
	v_pk_fma_f32 v[34:35], v[34:35], -2.0, v[128:129] op_sel_hi:[1,0,1]
	v_mul_f32_e32 v126, v56, v56
	v_fmac_f32_e32 v126, v35, v35
	v_cndmask_b32_e32 v46, 0, v46, vcc
	v_add_f32_e32 v48, v34, v35
	v_fmac_f32_e32 v126, v34, v34
	v_add_f32_e32 v34, 1.0, v44
	v_cmp_eq_u32_e32 vcc, 1, v28
	v_add_f32_e32 v60, v48, v56
	v_rcp_f32_e32 v44, v34
	v_mul_f32_e32 v34, v36, v36
	v_cndmask_b32_e64 v35, 0, 1.0, vcc
	v_add_f32_e32 v47, v35, v47
	v_cndmask_b32_e32 v35, 0, v34, vcc
	v_cndmask_b32_e32 v48, 0, v36, vcc
	v_cndmask_b32_e32 v56, 0, v60, vcc
	v_cmp_eq_u32_e32 vcc, 2, v28
	v_add_f32_e32 v55, v35, v55
	v_add_f32_e32 v56, v127, v56
	v_cndmask_b32_e64 v35, 0, 1.0, vcc
	v_add_f32_e32 v48, v48, v74
	v_add_f32_e32 v74, v35, v135
	v_cndmask_b32_e32 v35, 0, v34, vcc
	v_cndmask_b32_e32 v127, 0, v36, vcc
	v_cndmask_b32_e32 v135, 0, v60, vcc
	v_cmp_eq_u32_e32 vcc, 3, v28
	v_add_f32_e32 v140, v140, v145
	v_add_f32_e32 v139, v35, v139
	v_cndmask_b32_e64 v35, 0, 1.0, vcc
	v_add_f32_e32 v135, v140, v135
	v_add_f32_e32 v140, v35, v141
	v_mul_f32_e32 v35, 0x4038aa3b, v61
	v_exp_f32_e32 v35, v35
	v_add_f32_e32 v138, v127, v138
	v_cndmask_b32_e32 v127, 0, v34, vcc
	v_cndmask_b32_e32 v34, 0, v36, vcc
	v_add_f32_e32 v141, v34, v143
	v_add_f32_e32 v34, 1.0, v35
	v_mul_f32_e32 v35, 0x4038aa3b, v49
	v_mul_f32_e32 v49, 0x4038aa3b, v57
	v_exp_f32_e32 v49, v49
	v_exp_f32_e32 v35, v35
	v_rcp_f32_e32 v34, v34
	v_mul_f32_e32 v45, 0xbfb8aa3b, v45
	v_add_f32_e32 v49, 1.0, v49
	v_add_f32_e32 v35, 1.0, v35
	v_rcp_f32_e32 v49, v49
	v_rcp_f32_e32 v35, v35
	v_add_f32_e32 v54, 0x3bcc931a, v54
	v_exp_f32_e32 v45, v45
	v_mul_f32_e32 v42, 0xbfb8aa3b, v42
	v_mul_f32_e32 v43, 0xbfb8aa3b, v43
	v_add_f32_e32 v46, v46, v144
	v_fmac_f32_e32 v54, -2.0, v49
	v_exp_f32_e32 v42, v42
	v_exp_f32_e32 v43, v43
	v_add_f32_e32 v46, v127, v46
	v_pk_fma_f32 v[34:35], v[34:35], -2.0, v[128:129] op_sel_hi:[1,0,1]
	v_mul_f32_e32 v127, v54, v54
	v_fmac_f32_e32 v127, v35, v35
	v_cndmask_b32_e32 v36, 0, v60, vcc
	v_add_f32_e32 v49, v34, v35
	v_fmac_f32_e32 v127, v34, v34
	v_add_f32_e32 v34, 1.0, v45
	v_cmp_eq_u32_e32 vcc, 1, v29
	v_add_f32_e32 v61, v49, v54
	v_rcp_f32_e32 v45, v34
	v_mul_f32_e32 v34, v37, v37
	v_cndmask_b32_e64 v35, 0, 1.0, vcc
	v_add_f32_e32 v42, 1.0, v42
	v_add_f32_e32 v43, 1.0, v43
	v_add_f32_e32 v47, v35, v47
	v_cndmask_b32_e32 v35, 0, v34, vcc
	v_cndmask_b32_e32 v49, 0, v37, vcc
	v_cndmask_b32_e32 v54, 0, v61, vcc
	v_cmp_eq_u32_e32 vcc, 2, v29
	v_rcp_f32_e32 v42, v42
	v_rcp_f32_e32 v43, v43
	v_add_f32_e32 v48, v49, v48
	v_add_f32_e32 v49, v35, v55
	v_cndmask_b32_e64 v35, 0, 1.0, vcc
	v_add_f32_e32 v54, v56, v54
	v_add_f32_e32 v55, v35, v74
	v_cndmask_b32_e32 v35, 0, v34, vcc
	v_cndmask_b32_e32 v56, 0, v37, vcc
	v_cndmask_b32_e32 v57, 0, v61, vcc
	v_cmp_eq_u32_e32 vcc, 3, v29
	v_add_f32_e32 v74, v35, v139
	v_add_f32_e32 v36, v142, v36
	v_cndmask_b32_e64 v35, 0, 1.0, vcc
	v_cndmask_b32_e32 v34, 0, v34, vcc
	v_add_f32_e32 v57, v135, v57
	v_add_f32_e32 v56, v56, v138
	v_add_f32_e32 v138, v35, v140
	v_cndmask_b32_e32 v35, 0, v37, vcc
	v_cndmask_b32_e32 v37, 0, v61, vcc
	v_add_f32_e32 v46, v34, v46
	v_add_u32_e32 v135, 0x1e000, v134
	v_add_f32_e32 v36, v36, v37
	v_add_f32_e32 v37, v35, v141
	ds_write_b128 v135, v[42:45]
	v_add_u32_e32 v34, 0x1500, v137
	s_waitcnt vmcnt(5)
	v_mul_f32_e32 v43, 0x4038aa3b, v70
	v_mul_u32_u24_sdwa v35, v34, s6 dst_sel:DWORD dst_unused:UNUSED_PAD src0_sel:WORD_0 src1_sel:DWORD
	v_exp_f32_e32 v43, v43
	v_lshrrev_b32_e32 v35, 23, v35
	v_mul_i32_i24_e32 v42, 0xffffff60, v35
	v_cvt_f32_u32_e32 v44, v35
	v_add_lshl_u32 v34, v42, v34, 2
	s_waitcnt vmcnt(4)
	v_mul_f32_e32 v35, 0x4038aa3b, v62
	v_cvt_f32_i32_e32 v42, v34
	v_add_f32_e32 v34, 1.0, v43
	v_exp_f32_e32 v35, v35
	s_waitcnt vmcnt(3)
	v_mul_f32_e32 v43, 0x4038aa3b, v66
	v_exp_f32_e32 v43, v43
	v_rcp_f32_e32 v34, v34
	v_add_f32_e32 v35, 1.0, v35
	v_rcp_f32_e32 v35, v35
	v_add_f32_e32 v43, 1.0, v43
	v_rcp_f32_e32 v43, v43
	v_fma_f32 v129, v44, s7, 1.0
	v_fma_f32 v42, v42, s9, 1.0
	v_pk_fma_f32 v[34:35], v[34:35], -2.0, v[128:129] op_sel_hi:[1,0,1]
	v_fma_f32 v43, -2.0, v43, v42
	v_add_f32_e32 v44, v34, v35
	v_add_f32_e32 v62, v44, v43
	s_waitcnt vmcnt(1)
	v_mul_f32_e32 v44, 0xbfb8aa3b, v50
	v_exp_f32_e32 v44, v44
	v_mul_f32_e32 v66, v43, v43
	s_waitcnt vmcnt(0)
	v_cmp_eq_u32_e32 vcc, 1, v30
	v_fmac_f32_e32 v66, v35, v35
	v_mul_f32_e32 v35, v38, v38
	v_cndmask_b32_e64 v43, 0, 1.0, vcc
	v_fmac_f32_e32 v66, v34, v34
	v_add_f32_e32 v34, 1.0, v44
	v_add_f32_e32 v43, v47, v43
	v_cndmask_b32_e32 v44, 0, v35, vcc
	v_cndmask_b32_e32 v45, 0, v38, vcc
	v_cndmask_b32_e32 v47, 0, v62, vcc
	v_cmp_eq_u32_e32 vcc, 2, v30
	v_add_f32_e32 v47, v54, v47
	v_add_f32_e32 v45, v48, v45
	v_cndmask_b32_e32 v50, 0, v38, vcc
	v_add_f32_e32 v50, v56, v50
	v_mul_f32_e32 v56, 0x4038aa3b, v71
	v_exp_f32_e32 v56, v56
	v_add_f32_e32 v44, v49, v44
	v_cndmask_b32_e64 v48, 0, 1.0, vcc
	v_cndmask_b32_e32 v49, 0, v35, vcc
	v_cndmask_b32_e32 v54, 0, v62, vcc
	v_cmp_eq_u32_e32 vcc, 3, v30
	v_add_f32_e32 v54, v57, v54
	v_mul_f32_e32 v51, 0xbfb8aa3b, v51
	v_cndmask_b32_e32 v57, 0, v62, vcc
	v_cndmask_b32_e32 v38, 0, v38, vcc
	v_add_f32_e32 v57, v36, v57
	v_add_f32_e32 v36, 1.0, v56
	v_mul_f32_e32 v56, 0x4038aa3b, v67
	v_add_f32_e32 v38, v37, v38
	v_mul_f32_e32 v37, 0x4038aa3b, v63
	v_exp_f32_e32 v56, v56
	v_exp_f32_e32 v37, v37
	v_rcp_f32_e32 v36, v36
	v_cndmask_b32_e32 v35, 0, v35, vcc
	v_add_f32_e32 v56, 1.0, v56
	v_add_f32_e32 v37, 1.0, v37
	v_rcp_f32_e32 v56, v56
	v_rcp_f32_e32 v37, v37
	v_add_f32_e32 v46, v46, v35
	v_add_f32_e32 v35, 0x3b086211, v42
	v_fmac_f32_e32 v35, -2.0, v56
	v_exp_f32_e32 v51, v51
	v_pk_fma_f32 v[36:37], v[36:37], -2.0, v[128:129] op_sel_hi:[1,0,1]
	v_mul_f32_e32 v67, v35, v35
	v_add_f32_e32 v48, v55, v48
	v_cndmask_b32_e64 v55, 0, 1.0, vcc
	v_add_f32_e32 v56, v36, v37
	v_fmac_f32_e32 v67, v37, v37
	v_cmp_eq_u32_e32 vcc, 1, v31
	v_add_f32_e32 v63, v56, v35
	v_fmac_f32_e32 v67, v36, v36
	v_mul_f32_e32 v36, v39, v39
	v_cndmask_b32_e64 v37, 0, 1.0, vcc
	v_add_f32_e32 v35, 1.0, v51
	v_add_f32_e32 v43, v37, v43
	v_cndmask_b32_e32 v37, 0, v36, vcc
	v_cndmask_b32_e32 v51, 0, v39, vcc
	v_cndmask_b32_e32 v56, 0, v63, vcc
	v_cmp_eq_u32_e32 vcc, 2, v31
	v_add_f32_e32 v44, v37, v44
	v_add_f32_e32 v49, v74, v49
	v_cndmask_b32_e64 v37, 0, 1.0, vcc
	v_add_f32_e32 v47, v47, v56
	v_add_f32_e32 v45, v51, v45
	v_add_f32_e32 v48, v37, v48
	v_cndmask_b32_e32 v37, 0, v36, vcc
	v_cndmask_b32_e32 v51, 0, v39, vcc
	v_cndmask_b32_e32 v56, 0, v63, vcc
	v_cmp_eq_u32_e32 vcc, 3, v31
	v_add_f32_e32 v55, v138, v55
	v_add_f32_e32 v49, v37, v49
	v_cndmask_b32_e64 v37, 0, 1.0, vcc
	v_add_f32_e32 v50, v51, v50
	v_add_f32_e32 v51, v37, v55
	v_mul_f32_e32 v37, 0x4038aa3b, v72
	v_exp_f32_e32 v37, v37
	v_add_f32_e32 v54, v54, v56
	v_cndmask_b32_e32 v55, 0, v36, vcc
	v_cndmask_b32_e32 v36, 0, v39, vcc
	v_mul_f32_e32 v56, 0x4038aa3b, v68
	v_add_f32_e32 v38, v36, v38
	v_add_f32_e32 v36, 1.0, v37
	v_mul_f32_e32 v37, 0x4038aa3b, v64
	v_exp_f32_e32 v56, v56
	v_exp_f32_e32 v37, v37
	v_rcp_f32_e32 v36, v36
	v_mul_f32_e32 v52, 0xbfb8aa3b, v52
	v_add_f32_e32 v56, 1.0, v56
	v_add_f32_e32 v37, 1.0, v37
	v_rcp_f32_e32 v56, v56
	v_rcp_f32_e32 v37, v37
	v_add_f32_e32 v46, v55, v46
	v_add_f32_e32 v55, 0x3b886211, v42
	v_exp_f32_e32 v52, v52
	v_fmac_f32_e32 v55, -2.0, v56
	v_pk_fma_f32 v[36:37], v[36:37], -2.0, v[128:129] op_sel_hi:[1,0,1]
	v_mul_f32_e32 v68, v55, v55
	v_cndmask_b32_e32 v39, 0, v63, vcc
	v_add_f32_e32 v56, v36, v37
	v_fmac_f32_e32 v68, v37, v37
	v_cmp_eq_u32_e32 vcc, 1, v32
	v_add_f32_e32 v64, v56, v55
	v_fmac_f32_e32 v68, v36, v36
	v_add_f32_e32 v36, 1.0, v52
	v_mul_f32_e32 v37, v40, v40
	v_cndmask_b32_e64 v52, 0, 1.0, vcc
	v_add_f32_e32 v43, v52, v43
	v_cndmask_b32_e32 v52, 0, v37, vcc
	v_cndmask_b32_e32 v55, 0, v40, vcc
	v_cndmask_b32_e32 v56, 0, v64, vcc
	v_cmp_eq_u32_e32 vcc, 2, v32
	v_add_f32_e32 v44, v52, v44
	v_add_f32_e32 v47, v47, v56
	v_cndmask_b32_e64 v52, 0, 1.0, vcc
	v_add_f32_e32 v45, v55, v45
	v_add_f32_e32 v48, v52, v48
	v_cndmask_b32_e32 v52, 0, v37, vcc
	v_cndmask_b32_e32 v55, 0, v40, vcc
	v_cndmask_b32_e32 v56, 0, v64, vcc
	v_cmp_eq_u32_e32 vcc, 3, v32
	v_add_f32_e32 v49, v52, v49
	v_add_f32_e32 v39, v57, v39
	v_cndmask_b32_e64 v52, 0, 1.0, vcc
	v_add_f32_e32 v51, v52, v51
	v_mul_f32_e32 v52, 0x4038aa3b, v73
	v_exp_f32_e32 v52, v52
	v_add_f32_e32 v50, v55, v50
	v_cndmask_b32_e32 v55, 0, v64, vcc
	v_cndmask_b32_e32 v40, 0, v40, vcc
	v_add_f32_e32 v55, v39, v55
	v_mul_f32_e32 v39, 0x4038aa3b, v65
	v_add_f32_e32 v40, v40, v38
	v_add_f32_e32 v38, 1.0, v52
	v_exp_f32_e32 v39, v39
	v_mul_f32_e32 v52, 0x4038aa3b, v69
	v_exp_f32_e32 v52, v52
	v_rcp_f32_e32 v38, v38
	v_add_f32_e32 v39, 1.0, v39
	v_rcp_f32_e32 v39, v39
	v_add_f32_e32 v52, 1.0, v52
	v_rcp_f32_e32 v52, v52
	v_cndmask_b32_e32 v37, 0, v37, vcc
	v_add_f32_e32 v46, v37, v46
	v_add_f32_e32 v37, 0x3bcc931a, v42
	v_pk_fma_f32 v[38:39], v[38:39], -2.0, v[128:129] op_sel_hi:[1,0,1]
	v_fmac_f32_e32 v37, -2.0, v52
	v_add_f32_e32 v42, v38, v39
	v_add_f32_e32 v65, v42, v37
	v_mul_f32_e32 v42, 0xbfb8aa3b, v53
	v_exp_f32_e32 v42, v42
	v_mul_f32_e32 v69, v37, v37
	v_fmac_f32_e32 v69, v39, v39
	v_cmp_eq_u32_e32 vcc, 1, v33
	v_fmac_f32_e32 v69, v38, v38
	v_mul_f32_e32 v38, v41, v41
	v_cndmask_b32_e64 v39, 0, 1.0, vcc
	v_add_f32_e32 v37, 1.0, v42
	v_add_f32_e32 v145, v39, v43
	v_cndmask_b32_e32 v39, 0, v38, vcc
	v_cndmask_b32_e32 v42, 0, v41, vcc
	v_cndmask_b32_e32 v43, 0, v65, vcc
	v_cmp_eq_u32_e32 vcc, 2, v33
	v_add_f32_e32 v142, v39, v44
	v_rcp_f32_e32 v34, v34
	v_cndmask_b32_e64 v39, 0, 1.0, vcc
	v_rcp_f32_e32 v35, v35
	v_rcp_f32_e32 v36, v36
	v_rcp_f32_e32 v37, v37
	v_add_f32_e32 v143, v47, v43
	v_add_f32_e32 v144, v42, v45
	v_add_f32_e32 v141, v39, v48
	v_cndmask_b32_e32 v39, 0, v38, vcc
	v_cndmask_b32_e32 v42, 0, v41, vcc
	v_cndmask_b32_e32 v43, 0, v65, vcc
	v_cmp_eq_u32_e32 vcc, 3, v33
	v_add_f32_e32 v138, v39, v49
	v_add_f32_e32 v54, v54, v56
	v_cndmask_b32_e64 v39, 0, 1.0, vcc
	v_add_f32_e32 v137, v39, v51
	v_cndmask_b32_e32 v38, 0, v38, vcc
	v_cndmask_b32_e32 v39, 0, v41, vcc
	v_cndmask_b32_e32 v41, 0, v65, vcc
	v_add_f32_e32 v139, v54, v43
	v_add_f32_e32 v140, v42, v50
	v_add_f32_e32 v72, v55, v41
	v_add_f32_e32 v73, v39, v40
	v_add_f32_e32 v71, v38, v46
	v_add_u32_e32 v70, 0x21000, v134
	ds_write_b128 v70, v[34:37]
	v_mov_b32_e32 v74, v75
	v_mov_b32_e32 v51, v75
	v_mov_b32_e32 v50, v75
	v_mov_b32_e32 v47, v75
	v_mov_b32_e32 v46, v75
	v_mov_b32_e32 v55, v75
	v_mov_b32_e32 v54, v75
	v_mov_b32_e32 v40, v75
	s_and_saveexec_b64 s[10:11], s[4:5]
	s_cbranch_execz .LBB0_2
	s_mov_b64 s[12:13], 0xc80000
	v_lshl_add_u64 v[34:35], v[130:131], 0, s[12:13]
	s_mov_b64 s[12:13], 0x1900000
	v_lshl_add_u64 v[36:37], v[130:131], 0, s[12:13]
	s_mov_b64 s[12:13], 0x2580000
	v_lshl_add_u64 v[38:39], v[130:131], 0, s[12:13]
	s_mov_b64 s[12:13], 0x3200000
	v_lshl_add_u64 v[42:43], v[130:131], 0, s[12:13]
	s_movk_i32 s12, 0xff
	v_mov_b32_e32 v40, 0x18000
	v_cmp_lt_u32_e32 vcc, s12, v0
	v_mov_b32_e32 v75, 0
	s_nop 0
	v_cndmask_b32_e64 v74, v40, 0, vcc
	v_lshl_add_u64 v[40:41], v[130:131], 0, v[74:75]
	v_lshl_add_u64 v[34:35], v[34:35], 0, v[74:75]
	global_load_dwordx4 v[54:57], v[40:41], off nt
	global_load_dwordx4 v[50:53], v[34:35], off nt
	v_lshl_add_u64 v[34:35], v[36:37], 0, v[74:75]
	v_lshl_add_u64 v[36:37], v[38:39], 0, v[74:75]
	global_load_dwordx4 v[46:49], v[34:35], off nt
	global_load_dwordx4 v[38:41], v[36:37], off nt
	v_lshl_add_u64 v[34:35], v[42:43], 0, v[74:75]
	global_load_dwordx4 v[42:45], v[34:35], off nt
	v_lshl_add_u64 v[34:35], v[132:133], 0, v[74:75]
	global_load_dwordx4 v[34:37], v[34:35], off nt
	v_or_b32_e32 v130, 0x1800, v0
	v_add_u32_e32 v74, s8, v130
	v_mul_u32_u24_sdwa v75, v74, s6 dst_sel:DWORD dst_unused:UNUSED_PAD src0_sel:WORD_0 src1_sel:DWORD
	v_lshrrev_b32_e32 v75, 23, v75
	v_mul_i32_i24_e32 v129, 0xffffff60, v75
	v_add_lshl_u32 v74, v129, v74, 2
	v_cvt_f32_u32_e32 v75, v75
	v_cvt_f32_i32_e32 v74, v74
	v_fma_f32 v129, v75, s7, 1.0
	v_fma_f32 v131, v74, s9, 1.0
	s_waitcnt vmcnt(5)
	v_mul_f32_e32 v54, 0x4038aa3b, v54
	s_waitcnt vmcnt(4)
	v_mul_f32_e32 v50, 0x4038aa3b, v50
	v_exp_f32_e32 v54, v54
	s_waitcnt vmcnt(3)
	v_mul_f32_e32 v46, 0x4038aa3b, v46
	v_exp_f32_e32 v50, v50
	v_exp_f32_e32 v46, v46
	v_mul_f32_e32 v47, 0x4038aa3b, v47
	v_mul_f32_e32 v55, 0x4038aa3b, v55
	v_exp_f32_e32 v148, v47
	v_add_f32_e32 v47, 1.0, v54
	v_add_f32_e32 v50, 1.0, v50
	v_add_f32_e32 v54, 1.0, v46
	v_exp_f32_e32 v55, v55
	v_rcp_f32_e32 v46, v47
	v_rcp_f32_e32 v47, v50
	v_rcp_f32_e32 v50, v54
	v_mul_f32_e32 v51, 0x4038aa3b, v51
	s_waitcnt vmcnt(0)
	v_cmp_eq_u32_e32 vcc, 1, v34
	v_cmp_eq_u32_e64 s[6:7], 2, v34
	v_cmp_eq_u32_e64 s[8:9], 3, v34
	v_exp_f32_e32 v51, v51
	v_mul_f32_e32 v74, v38, v38
	v_cndmask_b32_e64 v75, 0, 1.0, vcc
	v_cndmask_b32_e64 v132, 0, 1.0, s[6:7]
	v_cndmask_b32_e64 v133, 0, 1.0, s[8:9]
	v_add_f32_e32 v55, 1.0, v55
	v_pk_fma_f32 v[46:47], v[46:47], -2.0, v[128:129] op_sel_hi:[1,0,1]
	v_fma_f32 v54, -2.0, v50, v131
	v_add_f32_e32 v145, v145, v75
	v_cndmask_b32_e32 v75, 0, v74, vcc
	v_add_f32_e32 v132, v141, v132
	v_cndmask_b32_e64 v141, 0, v74, s[6:7]
	v_add_f32_e32 v133, v137, v133
	v_cndmask_b32_e64 v137, 0, v74, s[8:9]
	v_rcp_f32_e32 v74, v55
	v_add_f32_e32 v55, v46, v47
	v_mul_f32_e32 v50, v54, v54
	v_add_f32_e32 v54, v55, v54
	v_fmac_f32_e32 v50, v47, v47
	v_cndmask_b32_e32 v146, 0, v38, vcc
	v_cndmask_b32_e64 v147, 0, v38, s[6:7]
	v_cndmask_b32_e64 v38, 0, v38, s[8:9]
	v_add_f32_e32 v51, 1.0, v51
	v_fmac_f32_e32 v50, v46, v46
	v_cndmask_b32_e32 v46, 0, v54, vcc
	v_add_f32_e32 v142, v142, v75
	v_add_f32_e32 v38, v73, v38
	v_add_f32_e32 v73, v143, v46
	v_rcp_f32_e32 v75, v51
	v_add_f32_e32 v46, 1.0, v148
	v_rcp_f32_e32 v51, v46
	v_cndmask_b32_e64 v47, 0, v54, s[6:7]
	v_add_f32_e32 v139, v139, v47
	v_add_f32_e32 v71, v71, v137
	v_add_f32_e32 v137, 0x3b086211, v131
	v_pk_fma_f32 v[46:47], v[74:75], -2.0, v[128:129] op_sel_hi:[1,0,1]
	v_cndmask_b32_e64 v55, 0, v54, s[8:9]
	v_fmac_f32_e32 v137, -2.0, v51
	v_add_f32_e32 v51, v46, v47
	v_add_f32_e32 v72, v72, v55
	v_add_f32_e32 v55, v51, v137
	v_mul_f32_e32 v51, v137, v137
	v_fmac_f32_e32 v51, v47, v47
	v_fmac_f32_e32 v51, v46, v46
	v_mul_f32_e32 v46, v39, v39
	v_cmp_eq_u32_e32 vcc, 1, v35
	v_add_f32_e32 v138, v138, v141
	v_add_f32_e32 v140, v140, v147
	v_cndmask_b32_e64 v47, 0, 1.0, vcc
	v_cndmask_b32_e32 v74, 0, v46, vcc
	v_cndmask_b32_e32 v75, 0, v39, vcc
	v_cndmask_b32_e32 v137, 0, v55, vcc
	v_cmp_eq_u32_e32 vcc, 2, v35
	v_add_f32_e32 v73, v73, v137
	v_add_f32_e32 v137, v74, v142
	v_cndmask_b32_e64 v74, 0, 1.0, vcc
	v_add_f32_e32 v132, v74, v132
	v_cndmask_b32_e32 v74, 0, v46, vcc
	v_cndmask_b32_e32 v141, 0, v39, vcc
	v_cndmask_b32_e32 v142, 0, v55, vcc
	v_cmp_eq_u32_e32 vcc, 3, v35
	v_mul_f32_e32 v48, 0x4038aa3b, v48
	v_add_f32_e32 v140, v141, v140
	v_cndmask_b32_e32 v39, 0, v39, vcc
	v_mul_f32_e32 v56, 0x4038aa3b, v56
	v_add_f32_e32 v141, v39, v38
	v_mul_f32_e32 v39, 0x4038aa3b, v52
	v_exp_f32_e32 v48, v48
	v_exp_f32_e32 v56, v56
	v_exp_f32_e32 v39, v39
	v_mul_f32_e32 v44, 0xbfb8aa3b, v44
	v_add_f32_e32 v48, 1.0, v48
	v_add_f32_e32 v38, 1.0, v56
	v_add_f32_e32 v39, 1.0, v39
	v_rcp_f32_e32 v48, v48
	v_rcp_f32_e32 v38, v38
	v_rcp_f32_e32 v39, v39
	v_add_f32_e32 v138, v74, v138
	v_cndmask_b32_e64 v74, 0, 1.0, vcc
	v_add_f32_e32 v56, 0x3b886211, v131
	v_exp_f32_e32 v44, v44
	v_add_f32_e32 v133, v74, v133
	v_cndmask_b32_e32 v74, 0, v55, vcc
	v_fmac_f32_e32 v56, -2.0, v48
	v_add_f32_e32 v72, v72, v74
	v_pk_fma_f32 v[38:39], v[38:39], -2.0, v[128:129] op_sel_hi:[1,0,1]
	v_mul_f32_e32 v74, v56, v56
	v_cndmask_b32_e32 v46, 0, v46, vcc
	v_fmac_f32_e32 v74, v39, v39
	v_add_f32_e32 v52, v46, v71
	v_add_f32_e32 v46, v38, v39
	v_fmac_f32_e32 v74, v38, v38
	v_add_f32_e32 v38, 1.0, v44
	v_cmp_eq_u32_e32 vcc, 1, v36
	v_add_f32_e32 v47, v47, v145
	v_add_f32_e32 v46, v46, v56
	v_rcp_f32_e32 v44, v38
	v_mul_f32_e32 v38, v40, v40
	v_cndmask_b32_e64 v39, 0, 1.0, vcc
	v_add_f32_e32 v144, v144, v146
	v_add_f32_e32 v48, v39, v47
	v_cndmask_b32_e32 v39, 0, v38, vcc
	v_cndmask_b32_e32 v47, 0, v40, vcc
	v_cndmask_b32_e32 v56, 0, v46, vcc
	v_cmp_eq_u32_e32 vcc, 2, v36
	v_add_f32_e32 v75, v75, v144
	v_add_f32_e32 v56, v73, v56
	v_add_f32_e32 v73, v39, v137
	v_cndmask_b32_e64 v39, 0, 1.0, vcc
	v_add_f32_e32 v71, v47, v75
	v_add_f32_e32 v132, v39, v132
	v_cndmask_b32_e32 v39, 0, v38, vcc
	v_cndmask_b32_e32 v47, 0, v40, vcc
	v_cndmask_b32_e32 v75, 0, v46, vcc
	v_cmp_eq_u32_e32 vcc, 3, v36
	v_add_f32_e32 v138, v39, v138
	v_add_f32_e32 v140, v47, v140
	v_cndmask_b32_e64 v39, 0, 1.0, vcc
	v_add_f32_e32 v133, v39, v133
	v_mul_f32_e32 v39, 0x4038aa3b, v57
	v_exp_f32_e32 v39, v39
	v_cndmask_b32_e32 v47, 0, v38, vcc
	v_cndmask_b32_e32 v38, 0, v40, vcc
	v_mul_f32_e32 v49, 0x4038aa3b, v49
	v_add_f32_e32 v57, v38, v141
	v_add_f32_e32 v38, 1.0, v39
	v_mul_f32_e32 v39, 0x4038aa3b, v53
	v_exp_f32_e32 v49, v49
	v_exp_f32_e32 v39, v39
	v_rcp_f32_e32 v38, v38
	v_mul_f32_e32 v45, 0xbfb8aa3b, v45
	v_add_f32_e32 v49, 1.0, v49
	v_add_f32_e32 v39, 1.0, v39
	v_rcp_f32_e32 v49, v49
	v_rcp_f32_e32 v39, v39
	v_add_f32_e32 v53, 0x3bcc931a, v131
	v_exp_f32_e32 v45, v45
	v_add_f32_e32 v139, v139, v142
	v_fmac_f32_e32 v53, -2.0, v49
	v_mul_f32_e32 v42, 0xbfb8aa3b, v42
	v_mul_f32_e32 v43, 0xbfb8aa3b, v43
	v_add_f32_e32 v137, v139, v75
	v_pk_fma_f32 v[38:39], v[38:39], -2.0, v[128:129] op_sel_hi:[1,0,1]
	v_mul_f32_e32 v75, v53, v53
	v_exp_f32_e32 v42, v42
	v_exp_f32_e32 v43, v43
	v_fmac_f32_e32 v75, v39, v39
	v_cndmask_b32_e32 v40, 0, v46, vcc
	v_add_f32_e32 v52, v47, v52
	v_add_f32_e32 v47, v38, v39
	v_fmac_f32_e32 v75, v38, v38
	v_add_f32_e32 v38, 1.0, v45
	v_cmp_eq_u32_e32 vcc, 1, v37
	v_add_f32_e32 v47, v47, v53
	v_rcp_f32_e32 v45, v38
	v_mul_f32_e32 v38, v41, v41
	v_cndmask_b32_e64 v39, 0, 1.0, vcc
	v_add_f32_e32 v145, v39, v48
	v_cndmask_b32_e32 v39, 0, v38, vcc
	v_cndmask_b32_e32 v48, 0, v41, vcc
	v_cndmask_b32_e32 v49, 0, v47, vcc
	v_cmp_eq_u32_e32 vcc, 2, v37
	v_add_f32_e32 v42, 1.0, v42
	v_add_f32_e32 v43, 1.0, v43
	v_add_f32_e32 v142, v39, v73
	v_cndmask_b32_e64 v39, 0, 1.0, vcc
	v_rcp_f32_e32 v42, v42
	v_rcp_f32_e32 v43, v43
	v_add_f32_e32 v143, v56, v49
	v_add_f32_e32 v144, v48, v71
	v_add_f32_e32 v141, v39, v132
	v_cndmask_b32_e32 v39, 0, v38, vcc
	v_cndmask_b32_e32 v48, 0, v41, vcc
	v_cndmask_b32_e32 v49, 0, v47, vcc
	v_cmp_eq_u32_e32 vcc, 3, v37
	v_add_f32_e32 v138, v39, v138
	v_lshlrev_b32_e32 v36, 16, v36
	v_cndmask_b32_e64 v39, 0, 1.0, vcc
	v_add_f32_e32 v40, v72, v40
	v_add_f32_e32 v139, v137, v49
	v_add_f32_e32 v137, v39, v133
	v_cndmask_b32_e32 v38, 0, v38, vcc
	v_cndmask_b32_e32 v39, 0, v41, vcc
	v_cndmask_b32_e32 v41, 0, v47, vcc
	v_lshlrev_b32_e32 v37, 24, v37
	v_lshl_or_b32 v35, v35, 8, v36
	v_add_f32_e32 v140, v48, v140
	v_add_f32_e32 v72, v40, v41
	v_add_f32_e32 v73, v39, v57
	v_add_f32_e32 v71, v38, v52
	v_lshl_add_u32 v38, v130, 4, v136
	v_or3_b32 v40, v35, v37, v34
	ds_write_b128 v38, v[42:45] offset:49152

.Lkf_par_done:
	s_mov_b64 exec, -1
	v_lshlrev_b32_e32 v4, 16, v4
	v_lshlrev_b32_e32 v5, 24, v5
	v_lshl_or_b32 v3, v3, 8, v4
	v_lshlrev_b32_e32 v4, 16, v12
	v_or3_b32 v3, v3, v5, v2
	v_lshlrev_b32_e32 v5, 24, v13
	v_lshl_or_b32 v4, v11, 8, v4
	v_or3_b32 v43, v4, v5, v10
	v_lshlrev_b32_e32 v4, 16, v16
	v_lshlrev_b32_e32 v5, 24, v17
	v_lshl_or_b32 v4, v15, 8, v4
	v_lshlrev_b32_e32 v8, 16, v8
	v_or3_b32 v42, v4, v5, v14
	v_lshlrev_b32_e32 v4, 16, v20
	v_lshlrev_b32_e32 v9, 24, v9
	v_lshl_or_b32 v7, v7, 8, v8
	v_lshlrev_b32_e32 v5, 24, v21
	v_lshl_or_b32 v4, v19, 8, v4
	v_or3_b32 v44, v7, v9, v6
	v_or3_b32 v41, v4, v5, v18
	v_lshlrev_b32_e32 v4, 16, v24
	v_mov_b32_e32 v7, 0
	v_mov_b32_e32 v8, 0x64c
	v_lshlrev_b32_e32 v5, 24, v25
	v_lshl_or_b32 v4, v23, 8, v4
	s_waitcnt lgkmcnt(0)
	s_barrier
	ds_read_b96 v[36:38], v7 offset:1600
	ds_read_b64 v[16:17], v7 offset:1624
	ds_read2_b32 v[20:21], v8 offset1:1
	v_or3_b32 v19, v4, v5, v22
	v_lshlrev_b32_e32 v4, 16, v28
	v_lshlrev_b32_e32 v5, 24, v29
	v_lshl_or_b32 v4, v27, 8, v4
	v_or3_b32 v13, v4, v5, v26
	v_lshlrev_b32_e32 v4, 16, v32
	v_lshlrev_b32_e32 v5, 24, v33
	v_lshl_or_b32 v4, v31, 8, v4
	v_or3_b32 v9, v4, v5, v30
	ds_read_b32 v8, v7 offset:1620
	ds_read_b32 v12, v7 offset:1632
	ds_read_b128 v[30:33], v134 offset:49152
	s_movk_i32 s3, 0xfff
	v_mov_b32_e32 v11, 0x670
	v_mov_b32_e32 v15, 0x10000
	v_mov_b32_e32 v164, 1
	v_mov_b32_e32 v165, 2
	s_mov_b32 s16, 0xfff0fff0
	s_mov_b32 s17, 1
	s_mov_b32 s18, 2
	s_mov_b32 s19, 3
	s_waitcnt lgkmcnt(0)
	v_mov_b32_e32 v24, v38
	v_pk_fma_f32 v[22:23], v[76:77], v[20:21], v[16:17] op_sel_hi:[1,0,0]
	v_pk_fma_f32 v[22:23], v[78:79], v[36:37], v[22:23] op_sel_hi:[1,0,1]
	s_nop 0
	v_exp_f32_e32 v26, v22
	v_exp_f32_e32 v27, v23
	v_pk_fma_f32 v[154:155], v[76:77], v[20:21], v[16:17] op_sel:[0,1,1]
	v_cmp_eq_u32_sdwa vcc, s17, v44 src0_sel:DWORD src1_sel:BYTE_0
	v_pk_fma_f32 v[154:155], v[78:79], v[36:37], v[154:155] op_sel:[0,1,0]
	v_cvt_pknorm_u16_f32 v158, v26, v27
	v_and_b32_e32 v159, s16, v158
	v_exp_f32_e32 v156, v154
	v_cndmask_b32_e32 v162, v164, v15, vcc
	v_cndmask_b32_e32 v150, 0, v26, vcc
	v_exp_f32_e32 v157, v155
	v_cmp_eq_u32_sdwa vcc, s17, v44 src0_sel:DWORD src1_sel:BYTE_1
	v_lshrrev_b32_sdwa v160, v165, v159 dst_sel:DWORD dst_unused:UNUSED_PAD src0_sel:DWORD src1_sel:WORD_0
	v_lshrrev_b32_sdwa v161, v165, v159 dst_sel:DWORD dst_unused:UNUSED_PAD src0_sel:DWORD src1_sel:WORD_1
	v_cndmask_b32_e32 v163, v164, v15, vcc
	v_cndmask_b32_e32 v151, 0, v27, vcc
	ds_add_u32 v160, v162 offset:1648
	ds_add_u32 v161, v163 offset:1648
	v_pk_fma_f32 v[22:23], v[76:77], v[8:9], v[12:13] op_sel_hi:[1,0,0]
	v_cmp_eq_u32_sdwa vcc, s18, v44 src0_sel:DWORD src1_sel:BYTE_0
	v_pk_fma_f32 v[22:23], v[78:79], v[24:25], v[22:23] op_sel_hi:[1,0,1]
	v_cvt_pknorm_u16_f32 v158, v156, v157
	v_and_b32_e32 v159, s16, v158
	v_exp_f32_e32 v26, v22
	v_cndmask_b32_e32 v162, v164, v15, vcc
	v_cndmask_b32_e32 v150, v150, v156, vcc
	v_exp_f32_e32 v27, v23
	v_cmp_eq_u32_sdwa vcc, s18, v44 src0_sel:DWORD src1_sel:BYTE_1
	v_lshrrev_b32_sdwa v160, v165, v159 dst_sel:DWORD dst_unused:UNUSED_PAD src0_sel:DWORD src1_sel:WORD_0
	v_lshrrev_b32_sdwa v161, v165, v159 dst_sel:DWORD dst_unused:UNUSED_PAD src0_sel:DWORD src1_sel:WORD_1
	v_cndmask_b32_e32 v163, v164, v15, vcc
	v_cndmask_b32_e32 v151, v151, v157, vcc
	ds_add_u32 v160, v162 offset:18032
	ds_add_u32 v161, v163 offset:18032
	v_pk_fma_f32 v[154:155], v[80:81], v[20:21], v[16:17] op_sel_hi:[1,0,0]
	v_cmp_eq_u32_sdwa vcc, s19, v44 src0_sel:DWORD src1_sel:BYTE_0
	v_pk_fma_f32 v[154:155], v[82:83], v[36:37], v[154:155] op_sel_hi:[1,0,1]
	v_cvt_pknorm_u16_f32 v158, v26, v27
	v_and_b32_e32 v159, s16, v158
	v_exp_f32_e32 v156, v154
	v_cndmask_b32_e32 v162, v164, v15, vcc
	v_cndmask_b32_e32 v150, v150, v26, vcc
	v_exp_f32_e32 v157, v155
	v_cmp_eq_u32_sdwa vcc, s19, v44 src0_sel:DWORD src1_sel:BYTE_1
	v_lshrrev_b32_sdwa v160, v165, v159 dst_sel:DWORD dst_unused:UNUSED_PAD src0_sel:DWORD src1_sel:WORD_0
	v_lshrrev_b32_sdwa v161, v165, v159 dst_sel:DWORD dst_unused:UNUSED_PAD src0_sel:DWORD src1_sel:WORD_1
	v_cndmask_b32_e32 v163, v164, v15, vcc
	v_cndmask_b32_e32 v151, v151, v27, vcc
	ds_add_u32 v160, v162 offset:34416
	ds_add_u32 v161, v163 offset:34416
	s_waitcnt lgkmcnt(6)
	v_pk_add_f32 v[166:167], v[30:31], v[150:151] neg_lo:[0,1] neg_hi:[0,1]
	s_nop 0
	v_pk_mul_f32 v[166:167], v[166:167], v[166:167]
	v_pk_fma_f32 v[22:23], v[80:81], v[20:21], v[16:17] op_sel:[0,1,1]
	v_cmp_eq_u32_sdwa vcc, s17, v44 src0_sel:DWORD src1_sel:BYTE_2
	v_pk_fma_f32 v[22:23], v[82:83], v[36:37], v[22:23] op_sel:[0,1,0]
	v_cvt_pknorm_u16_f32 v158, v156, v157
	v_and_b32_e32 v159, s16, v158
	v_exp_f32_e32 v26, v22
	v_cndmask_b32_e32 v162, v164, v15, vcc
	v_cndmask_b32_e32 v152, 0, v156, vcc
	v_exp_f32_e32 v27, v23
	v_cmp_eq_u32_sdwa vcc, s17, v44 src0_sel:DWORD src1_sel:BYTE_3
	v_lshrrev_b32_sdwa v160, v165, v159 dst_sel:DWORD dst_unused:UNUSED_PAD src0_sel:DWORD src1_sel:WORD_0
	v_lshrrev_b32_sdwa v161, v165, v159 dst_sel:DWORD dst_unused:UNUSED_PAD src0_sel:DWORD src1_sel:WORD_1
	v_cndmask_b32_e32 v163, v164, v15, vcc
	v_cndmask_b32_e32 v153, 0, v157, vcc
	ds_add_u32 v160, v162 offset:1648
	ds_add_u32 v161, v163 offset:1648
	v_pk_fma_f32 v[154:155], v[80:81], v[8:9], v[12:13] op_sel_hi:[1,0,0]
	v_cmp_eq_u32_sdwa vcc, s18, v44 src0_sel:DWORD src1_sel:BYTE_2
	v_pk_fma_f32 v[154:155], v[82:83], v[24:25], v[154:155] op_sel_hi:[1,0,1]
	v_cvt_pknorm_u16_f32 v158, v26, v27
	v_and_b32_e32 v159, s16, v158
	v_exp_f32_e32 v156, v154
	v_cndmask_b32_e32 v162, v164, v15, vcc
	v_cndmask_b32_e32 v152, v152, v26, vcc
	v_exp_f32_e32 v157, v155
	v_cmp_eq_u32_sdwa vcc, s18, v44 src0_sel:DWORD src1_sel:BYTE_3
	v_lshrrev_b32_sdwa v160, v165, v159 dst_sel:DWORD dst_unused:UNUSED_PAD src0_sel:DWORD src1_sel:WORD_0
	v_lshrrev_b32_sdwa v161, v165, v159 dst_sel:DWORD dst_unused:UNUSED_PAD src0_sel:DWORD src1_sel:WORD_1
	v_cndmask_b32_e32 v163, v164, v15, vcc
	v_cndmask_b32_e32 v153, v153, v27, vcc
	ds_add_u32 v160, v162 offset:18032
	ds_add_u32 v161, v163 offset:18032
	v_cmp_eq_u32_sdwa vcc, s19, v44 src0_sel:DWORD src1_sel:BYTE_2
	s_nop 0
	v_cvt_pknorm_u16_f32 v158, v156, v157
	v_and_b32_e32 v159, s16, v158
	v_cndmask_b32_e32 v162, v164, v15, vcc
	v_cndmask_b32_e32 v152, v152, v156, vcc
	v_cmp_eq_u32_sdwa vcc, s19, v44 src0_sel:DWORD src1_sel:BYTE_3
	v_lshrrev_b32_sdwa v160, v165, v159 dst_sel:DWORD dst_unused:UNUSED_PAD src0_sel:DWORD src1_sel:WORD_0
	v_lshrrev_b32_sdwa v161, v165, v159 dst_sel:DWORD dst_unused:UNUSED_PAD src0_sel:DWORD src1_sel:WORD_1
	v_cndmask_b32_e32 v163, v164, v15, vcc
	v_cndmask_b32_e32 v153, v153, v157, vcc
	ds_add_u32 v160, v162 offset:34416
	ds_add_u32 v161, v163 offset:34416
	v_pk_add_f32 v[22:23], v[32:33], v[152:153] neg_lo:[0,1] neg_hi:[0,1]
	s_nop 0
	v_pk_fma_f32 v[28:29], v[22:23], v[22:23], v[166:167]
	ds_read_b128 v[76:79], v134 offset:61440
	v_pk_fma_f32 v[80:81], v[84:85], v[20:21], v[16:17] op_sel_hi:[1,0,0]
	v_pk_fma_f32 v[80:81], v[86:87], v[36:37], v[80:81] op_sel_hi:[1,0,1]
	s_nop 0
	v_exp_f32_e32 v82, v80
	v_exp_f32_e32 v83, v81
	v_pk_fma_f32 v[154:155], v[84:85], v[20:21], v[16:17] op_sel:[0,1,1]
	v_cmp_eq_u32_sdwa vcc, s17, v3 src0_sel:DWORD src1_sel:BYTE_0
	v_pk_fma_f32 v[154:155], v[86:87], v[36:37], v[154:155] op_sel:[0,1,0]
	v_cvt_pknorm_u16_f32 v158, v82, v83
	v_and_b32_e32 v159, s16, v158
	v_exp_f32_e32 v156, v154
	v_cndmask_b32_e32 v162, v164, v15, vcc
	v_cndmask_b32_e32 v150, 0, v82, vcc
	v_exp_f32_e32 v157, v155
	v_cmp_eq_u32_sdwa vcc, s17, v3 src0_sel:DWORD src1_sel:BYTE_1
	v_lshrrev_b32_sdwa v160, v165, v159 dst_sel:DWORD dst_unused:UNUSED_PAD src0_sel:DWORD src1_sel:WORD_0
	v_lshrrev_b32_sdwa v161, v165, v159 dst_sel:DWORD dst_unused:UNUSED_PAD src0_sel:DWORD src1_sel:WORD_1
	v_cndmask_b32_e32 v163, v164, v15, vcc
	v_cndmask_b32_e32 v151, 0, v83, vcc
	ds_add_u32 v160, v162 offset:1648
	ds_add_u32 v161, v163 offset:1648
	v_pk_fma_f32 v[80:81], v[84:85], v[8:9], v[12:13] op_sel_hi:[1,0,0]
	v_cmp_eq_u32_sdwa vcc, s18, v3 src0_sel:DWORD src1_sel:BYTE_0
	v_pk_fma_f32 v[80:81], v[86:87], v[24:25], v[80:81] op_sel_hi:[1,0,1]
	v_cvt_pknorm_u16_f32 v158, v156, v157
	v_and_b32_e32 v159, s16, v158
	v_exp_f32_e32 v82, v80
	v_cndmask_b32_e32 v162, v164, v15, vcc
	v_cndmask_b32_e32 v150, v150, v156, vcc
	v_exp_f32_e32 v83, v81
	v_cmp_eq_u32_sdwa vcc, s18, v3 src0_sel:DWORD src1_sel:BYTE_1
	v_lshrrev_b32_sdwa v160, v165, v159 dst_sel:DWORD dst_unused:UNUSED_PAD src0_sel:DWORD src1_sel:WORD_0
	v_lshrrev_b32_sdwa v161, v165, v159 dst_sel:DWORD dst_unused:UNUSED_PAD src0_sel:DWORD src1_sel:WORD_1
	v_cndmask_b32_e32 v163, v164, v15, vcc
	v_cndmask_b32_e32 v151, v151, v157, vcc
	ds_add_u32 v160, v162 offset:18032
	ds_add_u32 v161, v163 offset:18032
	v_pk_fma_f32 v[154:155], v[88:89], v[20:21], v[16:17] op_sel_hi:[1,0,0]
	v_cmp_eq_u32_sdwa vcc, s19, v3 src0_sel:DWORD src1_sel:BYTE_0
	v_pk_fma_f32 v[154:155], v[90:91], v[36:37], v[154:155] op_sel_hi:[1,0,1]
	v_cvt_pknorm_u16_f32 v158, v82, v83
	v_and_b32_e32 v159, s16, v158
	v_exp_f32_e32 v156, v154
	v_cndmask_b32_e32 v162, v164, v15, vcc
	v_cndmask_b32_e32 v150, v150, v82, vcc
	v_exp_f32_e32 v157, v155
	v_cmp_eq_u32_sdwa vcc, s19, v3 src0_sel:DWORD src1_sel:BYTE_1
	v_lshrrev_b32_sdwa v160, v165, v159 dst_sel:DWORD dst_unused:UNUSED_PAD src0_sel:DWORD src1_sel:WORD_0
	v_lshrrev_b32_sdwa v161, v165, v159 dst_sel:DWORD dst_unused:UNUSED_PAD src0_sel:DWORD src1_sel:WORD_1
	v_cndmask_b32_e32 v163, v164, v15, vcc
	v_cndmask_b32_e32 v151, v151, v83, vcc
	ds_add_u32 v160, v162 offset:34416
	ds_add_u32 v161, v163 offset:34416
	s_waitcnt lgkmcnt(6)
	v_pk_add_f32 v[166:167], v[76:77], v[150:151] neg_lo:[0,1] neg_hi:[0,1]
	s_nop 0
	v_pk_fma_f32 v[166:167], v[166:167], v[166:167], v[28:29]
	v_pk_fma_f32 v[80:81], v[88:89], v[20:21], v[16:17] op_sel:[0,1,1]
	v_cmp_eq_u32_sdwa vcc, s17, v3 src0_sel:DWORD src1_sel:BYTE_2
	v_pk_fma_f32 v[80:81], v[90:91], v[36:37], v[80:81] op_sel:[0,1,0]
	v_cvt_pknorm_u16_f32 v158, v156, v157
	v_and_b32_e32 v159, s16, v158
	v_exp_f32_e32 v82, v80
	v_cndmask_b32_e32 v162, v164, v15, vcc
	v_cndmask_b32_e32 v152, 0, v156, vcc
	v_exp_f32_e32 v83, v81
	v_cmp_eq_u32_sdwa vcc, s17, v3 src0_sel:DWORD src1_sel:BYTE_3
	v_lshrrev_b32_sdwa v160, v165, v159 dst_sel:DWORD dst_unused:UNUSED_PAD src0_sel:DWORD src1_sel:WORD_0
	v_lshrrev_b32_sdwa v161, v165, v159 dst_sel:DWORD dst_unused:UNUSED_PAD src0_sel:DWORD src1_sel:WORD_1
	v_cndmask_b32_e32 v163, v164, v15, vcc
	v_cndmask_b32_e32 v153, 0, v157, vcc
	ds_add_u32 v160, v162 offset:1648
	ds_add_u32 v161, v163 offset:1648
	v_pk_fma_f32 v[154:155], v[88:89], v[8:9], v[12:13] op_sel_hi:[1,0,0]
	v_cmp_eq_u32_sdwa vcc, s18, v3 src0_sel:DWORD src1_sel:BYTE_2
	v_pk_fma_f32 v[154:155], v[90:91], v[24:25], v[154:155] op_sel_hi:[1,0,1]
	v_cvt_pknorm_u16_f32 v158, v82, v83
	v_and_b32_e32 v159, s16, v158
	v_exp_f32_e32 v156, v154
	v_cndmask_b32_e32 v162, v164, v15, vcc
	v_cndmask_b32_e32 v152, v152, v82, vcc
	v_exp_f32_e32 v157, v155
	v_cmp_eq_u32_sdwa vcc, s18, v3 src0_sel:DWORD src1_sel:BYTE_3
	v_lshrrev_b32_sdwa v160, v165, v159 dst_sel:DWORD dst_unused:UNUSED_PAD src0_sel:DWORD src1_sel:WORD_0
	v_lshrrev_b32_sdwa v161, v165, v159 dst_sel:DWORD dst_unused:UNUSED_PAD src0_sel:DWORD src1_sel:WORD_1
	v_cndmask_b32_e32 v163, v164, v15, vcc
	v_cndmask_b32_e32 v153, v153, v83, vcc
	ds_add_u32 v160, v162 offset:18032
	ds_add_u32 v161, v163 offset:18032
	v_cmp_eq_u32_sdwa vcc, s19, v3 src0_sel:DWORD src1_sel:BYTE_2
	s_nop 0
	v_cvt_pknorm_u16_f32 v158, v156, v157
	v_and_b32_e32 v159, s16, v158
	v_cndmask_b32_e32 v162, v164, v15, vcc
	v_cndmask_b32_e32 v152, v152, v156, vcc
	v_cmp_eq_u32_sdwa vcc, s19, v3 src0_sel:DWORD src1_sel:BYTE_3
	v_lshrrev_b32_sdwa v160, v165, v159 dst_sel:DWORD dst_unused:UNUSED_PAD src0_sel:DWORD src1_sel:WORD_0
	v_lshrrev_b32_sdwa v161, v165, v159 dst_sel:DWORD dst_unused:UNUSED_PAD src0_sel:DWORD src1_sel:WORD_1
	v_cndmask_b32_e32 v163, v164, v15, vcc
	v_cndmask_b32_e32 v153, v153, v157, vcc
	ds_add_u32 v160, v162 offset:34416
	ds_add_u32 v161, v163 offset:34416
	v_pk_add_f32 v[80:81], v[78:79], v[152:153] neg_lo:[0,1] neg_hi:[0,1]
	s_nop 0
	v_pk_fma_f32 v[6:7], v[80:81], v[80:81], v[166:167]
	ds_read_b128 v[76:79], v1 offset:24576
	v_pk_fma_f32 v[80:81], v[92:93], v[20:21], v[16:17] op_sel_hi:[1,0,0]
	v_pk_fma_f32 v[80:81], v[94:95], v[36:37], v[80:81] op_sel_hi:[1,0,1]
	s_nop 0
	v_exp_f32_e32 v82, v80
	v_exp_f32_e32 v83, v81
	v_pk_fma_f32 v[154:155], v[92:93], v[20:21], v[16:17] op_sel:[0,1,1]
	v_cmp_eq_u32_sdwa vcc, s17, v43 src0_sel:DWORD src1_sel:BYTE_0
	v_pk_fma_f32 v[154:155], v[94:95], v[36:37], v[154:155] op_sel:[0,1,0]
	v_cvt_pknorm_u16_f32 v158, v82, v83
	v_and_b32_e32 v159, s16, v158
	v_exp_f32_e32 v156, v154
	v_cndmask_b32_e32 v162, v164, v15, vcc
	v_cndmask_b32_e32 v150, 0, v82, vcc
	v_exp_f32_e32 v157, v155
	v_cmp_eq_u32_sdwa vcc, s17, v43 src0_sel:DWORD src1_sel:BYTE_1
	v_lshrrev_b32_sdwa v160, v165, v159 dst_sel:DWORD dst_unused:UNUSED_PAD src0_sel:DWORD src1_sel:WORD_0
	v_lshrrev_b32_sdwa v161, v165, v159 dst_sel:DWORD dst_unused:UNUSED_PAD src0_sel:DWORD src1_sel:WORD_1
	v_cndmask_b32_e32 v163, v164, v15, vcc
	v_cndmask_b32_e32 v151, 0, v83, vcc
	ds_add_u32 v160, v162 offset:1648
	ds_add_u32 v161, v163 offset:1648
	v_pk_fma_f32 v[80:81], v[92:93], v[8:9], v[12:13] op_sel_hi:[1,0,0]
	v_cmp_eq_u32_sdwa vcc, s18, v43 src0_sel:DWORD src1_sel:BYTE_0
	v_pk_fma_f32 v[80:81], v[94:95], v[24:25], v[80:81] op_sel_hi:[1,0,1]
	v_cvt_pknorm_u16_f32 v158, v156, v157
	v_and_b32_e32 v159, s16, v158
	v_exp_f32_e32 v82, v80
	v_cndmask_b32_e32 v162, v164, v15, vcc
	v_cndmask_b32_e32 v150, v150, v156, vcc
	v_exp_f32_e32 v83, v81
	v_cmp_eq_u32_sdwa vcc, s18, v43 src0_sel:DWORD src1_sel:BYTE_1
	v_lshrrev_b32_sdwa v160, v165, v159 dst_sel:DWORD dst_unused:UNUSED_PAD src0_sel:DWORD src1_sel:WORD_0
	v_lshrrev_b32_sdwa v161, v165, v159 dst_sel:DWORD dst_unused:UNUSED_PAD src0_sel:DWORD src1_sel:WORD_1
	v_cndmask_b32_e32 v163, v164, v15, vcc
	v_cndmask_b32_e32 v151, v151, v157, vcc
	ds_add_u32 v160, v162 offset:18032
	ds_add_u32 v161, v163 offset:18032
	v_pk_fma_f32 v[154:155], v[96:97], v[20:21], v[16:17] op_sel_hi:[1,0,0]
	v_cmp_eq_u32_sdwa vcc, s19, v43 src0_sel:DWORD src1_sel:BYTE_0
	v_pk_fma_f32 v[154:155], v[98:99], v[36:37], v[154:155] op_sel_hi:[1,0,1]
	v_cvt_pknorm_u16_f32 v158, v82, v83
	v_and_b32_e32 v159, s16, v158
	v_exp_f32_e32 v156, v154
	v_cndmask_b32_e32 v162, v164, v15, vcc
	v_cndmask_b32_e32 v150, v150, v82, vcc
	v_exp_f32_e32 v157, v155
	v_cmp_eq_u32_sdwa vcc, s19, v43 src0_sel:DWORD src1_sel:BYTE_1
	v_lshrrev_b32_sdwa v160, v165, v159 dst_sel:DWORD dst_unused:UNUSED_PAD src0_sel:DWORD src1_sel:WORD_0
	v_lshrrev_b32_sdwa v161, v165, v159 dst_sel:DWORD dst_unused:UNUSED_PAD src0_sel:DWORD src1_sel:WORD_1
	v_cndmask_b32_e32 v163, v164, v15, vcc
	v_cndmask_b32_e32 v151, v151, v83, vcc
	ds_add_u32 v160, v162 offset:34416
	ds_add_u32 v161, v163 offset:34416
	s_waitcnt lgkmcnt(6)
	v_pk_add_f32 v[166:167], v[76:77], v[150:151] neg_lo:[0,1] neg_hi:[0,1]
	s_nop 0
	v_pk_fma_f32 v[166:167], v[166:167], v[166:167], v[6:7]
	v_pk_fma_f32 v[80:81], v[96:97], v[20:21], v[16:17] op_sel:[0,1,1]
	v_cmp_eq_u32_sdwa vcc, s17, v43 src0_sel:DWORD src1_sel:BYTE_2
	v_pk_fma_f32 v[80:81], v[98:99], v[36:37], v[80:81] op_sel:[0,1,0]
	v_cvt_pknorm_u16_f32 v158, v156, v157
	v_and_b32_e32 v159, s16, v158
	v_exp_f32_e32 v82, v80
	v_cndmask_b32_e32 v162, v164, v15, vcc
	v_cndmask_b32_e32 v152, 0, v156, vcc
	v_exp_f32_e32 v83, v81
	v_cmp_eq_u32_sdwa vcc, s17, v43 src0_sel:DWORD src1_sel:BYTE_3
	v_lshrrev_b32_sdwa v160, v165, v159 dst_sel:DWORD dst_unused:UNUSED_PAD src0_sel:DWORD src1_sel:WORD_0
	v_lshrrev_b32_sdwa v161, v165, v159 dst_sel:DWORD dst_unused:UNUSED_PAD src0_sel:DWORD src1_sel:WORD_1
	v_cndmask_b32_e32 v163, v164, v15, vcc
	v_cndmask_b32_e32 v153, 0, v157, vcc
	ds_add_u32 v160, v162 offset:1648
	ds_add_u32 v161, v163 offset:1648
	v_pk_fma_f32 v[154:155], v[96:97], v[8:9], v[12:13] op_sel_hi:[1,0,0]
	v_cmp_eq_u32_sdwa vcc, s18, v43 src0_sel:DWORD src1_sel:BYTE_2
	v_pk_fma_f32 v[154:155], v[98:99], v[24:25], v[154:155] op_sel_hi:[1,0,1]
	v_cvt_pknorm_u16_f32 v158, v82, v83
	v_and_b32_e32 v159, s16, v158
	v_exp_f32_e32 v156, v154
	v_cndmask_b32_e32 v162, v164, v15, vcc
	v_cndmask_b32_e32 v152, v152, v82, vcc
	v_exp_f32_e32 v157, v155
	v_cmp_eq_u32_sdwa vcc, s18, v43 src0_sel:DWORD src1_sel:BYTE_3
	v_lshrrev_b32_sdwa v160, v165, v159 dst_sel:DWORD dst_unused:UNUSED_PAD src0_sel:DWORD src1_sel:WORD_0
	v_lshrrev_b32_sdwa v161, v165, v159 dst_sel:DWORD dst_unused:UNUSED_PAD src0_sel:DWORD src1_sel:WORD_1
	v_cndmask_b32_e32 v163, v164, v15, vcc
	v_cndmask_b32_e32 v153, v153, v83, vcc
	ds_add_u32 v160, v162 offset:18032
	ds_add_u32 v161, v163 offset:18032
	v_cmp_eq_u32_sdwa vcc, s19, v43 src0_sel:DWORD src1_sel:BYTE_2
	s_nop 0
	v_cvt_pknorm_u16_f32 v158, v156, v157
	v_and_b32_e32 v159, s16, v158
	v_cndmask_b32_e32 v162, v164, v15, vcc
	v_cndmask_b32_e32 v152, v152, v156, vcc
	v_cmp_eq_u32_sdwa vcc, s19, v43 src0_sel:DWORD src1_sel:BYTE_3
	v_lshrrev_b32_sdwa v160, v165, v159 dst_sel:DWORD dst_unused:UNUSED_PAD src0_sel:DWORD src1_sel:WORD_0
	v_lshrrev_b32_sdwa v161, v165, v159 dst_sel:DWORD dst_unused:UNUSED_PAD src0_sel:DWORD src1_sel:WORD_1
	v_cndmask_b32_e32 v163, v164, v15, vcc
	v_cndmask_b32_e32 v153, v153, v157, vcc
	ds_add_u32 v160, v162 offset:34416
	ds_add_u32 v161, v163 offset:34416
	v_pk_add_f32 v[80:81], v[78:79], v[152:153] neg_lo:[0,1] neg_hi:[0,1]
	s_nop 0
	v_pk_fma_f32 v[6:7], v[80:81], v[80:81], v[166:167]
	ds_read_b128 v[76:79], v1 offset:36864
	v_pk_fma_f32 v[80:81], v[100:101], v[20:21], v[16:17] op_sel_hi:[1,0,0]
	v_pk_fma_f32 v[80:81], v[102:103], v[36:37], v[80:81] op_sel_hi:[1,0,1]
	s_nop 0
	v_exp_f32_e32 v82, v80
	v_exp_f32_e32 v83, v81
	v_pk_fma_f32 v[154:155], v[100:101], v[20:21], v[16:17] op_sel:[0,1,1]
	v_cmp_eq_u32_sdwa vcc, s17, v42 src0_sel:DWORD src1_sel:BYTE_0
	v_pk_fma_f32 v[154:155], v[102:103], v[36:37], v[154:155] op_sel:[0,1,0]
	v_cvt_pknorm_u16_f32 v158, v82, v83
	v_and_b32_e32 v159, s16, v158
	v_exp_f32_e32 v156, v154
	v_cndmask_b32_e32 v162, v164, v15, vcc
	v_cndmask_b32_e32 v150, 0, v82, vcc
	v_exp_f32_e32 v157, v155
	v_cmp_eq_u32_sdwa vcc, s17, v42 src0_sel:DWORD src1_sel:BYTE_1
	v_lshrrev_b32_sdwa v160, v165, v159 dst_sel:DWORD dst_unused:UNUSED_PAD src0_sel:DWORD src1_sel:WORD_0
	v_lshrrev_b32_sdwa v161, v165, v159 dst_sel:DWORD dst_unused:UNUSED_PAD src0_sel:DWORD src1_sel:WORD_1
	v_cndmask_b32_e32 v163, v164, v15, vcc
	v_cndmask_b32_e32 v151, 0, v83, vcc
	ds_add_u32 v160, v162 offset:1648
	ds_add_u32 v161, v163 offset:1648
	v_pk_fma_f32 v[80:81], v[100:101], v[8:9], v[12:13] op_sel_hi:[1,0,0]
	v_cmp_eq_u32_sdwa vcc, s18, v42 src0_sel:DWORD src1_sel:BYTE_0
	v_pk_fma_f32 v[80:81], v[102:103], v[24:25], v[80:81] op_sel_hi:[1,0,1]
	v_cvt_pknorm_u16_f32 v158, v156, v157
	v_and_b32_e32 v159, s16, v158
	v_exp_f32_e32 v82, v80
	v_cndmask_b32_e32 v162, v164, v15, vcc
	v_cndmask_b32_e32 v150, v150, v156, vcc
	v_exp_f32_e32 v83, v81
	v_cmp_eq_u32_sdwa vcc, s18, v42 src0_sel:DWORD src1_sel:BYTE_1
	v_lshrrev_b32_sdwa v160, v165, v159 dst_sel:DWORD dst_unused:UNUSED_PAD src0_sel:DWORD src1_sel:WORD_0
	v_lshrrev_b32_sdwa v161, v165, v159 dst_sel:DWORD dst_unused:UNUSED_PAD src0_sel:DWORD src1_sel:WORD_1
	v_cndmask_b32_e32 v163, v164, v15, vcc
	v_cndmask_b32_e32 v151, v151, v157, vcc
	ds_add_u32 v160, v162 offset:18032
	ds_add_u32 v161, v163 offset:18032
	v_pk_fma_f32 v[154:155], v[104:105], v[20:21], v[16:17] op_sel_hi:[1,0,0]
	v_cmp_eq_u32_sdwa vcc, s19, v42 src0_sel:DWORD src1_sel:BYTE_0
	v_pk_fma_f32 v[154:155], v[106:107], v[36:37], v[154:155] op_sel_hi:[1,0,1]
	v_cvt_pknorm_u16_f32 v158, v82, v83
	v_and_b32_e32 v159, s16, v158
	v_exp_f32_e32 v156, v154
	v_cndmask_b32_e32 v162, v164, v15, vcc
	v_cndmask_b32_e32 v150, v150, v82, vcc
	v_exp_f32_e32 v157, v155
	v_cmp_eq_u32_sdwa vcc, s19, v42 src0_sel:DWORD src1_sel:BYTE_1
	v_lshrrev_b32_sdwa v160, v165, v159 dst_sel:DWORD dst_unused:UNUSED_PAD src0_sel:DWORD src1_sel:WORD_0
	v_lshrrev_b32_sdwa v161, v165, v159 dst_sel:DWORD dst_unused:UNUSED_PAD src0_sel:DWORD src1_sel:WORD_1
	v_cndmask_b32_e32 v163, v164, v15, vcc
	v_cndmask_b32_e32 v151, v151, v83, vcc
	ds_add_u32 v160, v162 offset:34416
	ds_add_u32 v161, v163 offset:34416
	s_waitcnt lgkmcnt(6)
	v_pk_add_f32 v[166:167], v[76:77], v[150:151] neg_lo:[0,1] neg_hi:[0,1]
	s_nop 0
	v_pk_fma_f32 v[166:167], v[166:167], v[166:167], v[6:7]
	v_pk_fma_f32 v[80:81], v[104:105], v[20:21], v[16:17] op_sel:[0,1,1]
	v_cmp_eq_u32_sdwa vcc, s17, v42 src0_sel:DWORD src1_sel:BYTE_2
	v_pk_fma_f32 v[80:81], v[106:107], v[36:37], v[80:81] op_sel:[0,1,0]
	v_cvt_pknorm_u16_f32 v158, v156, v157
	v_and_b32_e32 v159, s16, v158
	v_exp_f32_e32 v82, v80
	v_cndmask_b32_e32 v162, v164, v15, vcc
	v_cndmask_b32_e32 v152, 0, v156, vcc
	v_exp_f32_e32 v83, v81
	v_cmp_eq_u32_sdwa vcc, s17, v42 src0_sel:DWORD src1_sel:BYTE_3
	v_lshrrev_b32_sdwa v160, v165, v159 dst_sel:DWORD dst_unused:UNUSED_PAD src0_sel:DWORD src1_sel:WORD_0
	v_lshrrev_b32_sdwa v161, v165, v159 dst_sel:DWORD dst_unused:UNUSED_PAD src0_sel:DWORD src1_sel:WORD_1
	v_cndmask_b32_e32 v163, v164, v15, vcc
	v_cndmask_b32_e32 v153, 0, v157, vcc
	ds_add_u32 v160, v162 offset:1648
	ds_add_u32 v161, v163 offset:1648
	v_pk_fma_f32 v[154:155], v[104:105], v[8:9], v[12:13] op_sel_hi:[1,0,0]
	v_cmp_eq_u32_sdwa vcc, s18, v42 src0_sel:DWORD src1_sel:BYTE_2
	v_pk_fma_f32 v[154:155], v[106:107], v[24:25], v[154:155] op_sel_hi:[1,0,1]
	v_cvt_pknorm_u16_f32 v158, v82, v83
	v_and_b32_e32 v159, s16, v158
	v_exp_f32_e32 v156, v154
	v_cndmask_b32_e32 v162, v164, v15, vcc
	v_cndmask_b32_e32 v152, v152, v82, vcc
	v_exp_f32_e32 v157, v155
	v_cmp_eq_u32_sdwa vcc, s18, v42 src0_sel:DWORD src1_sel:BYTE_3
	v_lshrrev_b32_sdwa v160, v165, v159 dst_sel:DWORD dst_unused:UNUSED_PAD src0_sel:DWORD src1_sel:WORD_0
	v_lshrrev_b32_sdwa v161, v165, v159 dst_sel:DWORD dst_unused:UNUSED_PAD src0_sel:DWORD src1_sel:WORD_1
	v_cndmask_b32_e32 v163, v164, v15, vcc
	v_cndmask_b32_e32 v153, v153, v83, vcc
	ds_add_u32 v160, v162 offset:18032
	ds_add_u32 v161, v163 offset:18032
	v_cmp_eq_u32_sdwa vcc, s19, v42 src0_sel:DWORD src1_sel:BYTE_2
	s_nop 0
	v_cvt_pknorm_u16_f32 v158, v156, v157
	v_and_b32_e32 v159, s16, v158
	v_cndmask_b32_e32 v162, v164, v15, vcc
	v_cndmask_b32_e32 v152, v152, v156, vcc
	v_cmp_eq_u32_sdwa vcc, s19, v42 src0_sel:DWORD src1_sel:BYTE_3
	v_lshrrev_b32_sdwa v160, v165, v159 dst_sel:DWORD dst_unused:UNUSED_PAD src0_sel:DWORD src1_sel:WORD_0
	v_lshrrev_b32_sdwa v161, v165, v159 dst_sel:DWORD dst_unused:UNUSED_PAD src0_sel:DWORD src1_sel:WORD_1
	v_cndmask_b32_e32 v163, v164, v15, vcc
	v_cndmask_b32_e32 v153, v153, v157, vcc
	ds_add_u32 v160, v162 offset:34416
	ds_add_u32 v161, v163 offset:34416
	v_pk_add_f32 v[80:81], v[78:79], v[152:153] neg_lo:[0,1] neg_hi:[0,1]
	s_nop 0
	v_pk_fma_f32 v[6:7], v[80:81], v[80:81], v[166:167]
	ds_read_b128 v[76:79], v1 offset:49152
	v_pk_fma_f32 v[80:81], v[108:109], v[20:21], v[16:17] op_sel_hi:[1,0,0]
	v_pk_fma_f32 v[80:81], v[110:111], v[36:37], v[80:81] op_sel_hi:[1,0,1]
	s_nop 0
	v_exp_f32_e32 v82, v80
	v_exp_f32_e32 v83, v81
	v_pk_fma_f32 v[154:155], v[108:109], v[20:21], v[16:17] op_sel:[0,1,1]
	v_cmp_eq_u32_sdwa vcc, s17, v41 src0_sel:DWORD src1_sel:BYTE_0
	v_pk_fma_f32 v[154:155], v[110:111], v[36:37], v[154:155] op_sel:[0,1,0]
	v_cvt_pknorm_u16_f32 v158, v82, v83
	v_and_b32_e32 v159, s16, v158
	v_exp_f32_e32 v156, v154
	v_cndmask_b32_e32 v162, v164, v15, vcc
	v_cndmask_b32_e32 v150, 0, v82, vcc
	v_exp_f32_e32 v157, v155
	v_cmp_eq_u32_sdwa vcc, s17, v41 src0_sel:DWORD src1_sel:BYTE_1
	v_lshrrev_b32_sdwa v160, v165, v159 dst_sel:DWORD dst_unused:UNUSED_PAD src0_sel:DWORD src1_sel:WORD_0
	v_lshrrev_b32_sdwa v161, v165, v159 dst_sel:DWORD dst_unused:UNUSED_PAD src0_sel:DWORD src1_sel:WORD_1
	v_cndmask_b32_e32 v163, v164, v15, vcc
	v_cndmask_b32_e32 v151, 0, v83, vcc
	ds_add_u32 v160, v162 offset:1648
	ds_add_u32 v161, v163 offset:1648
	v_pk_fma_f32 v[80:81], v[108:109], v[8:9], v[12:13] op_sel_hi:[1,0,0]
	v_cmp_eq_u32_sdwa vcc, s18, v41 src0_sel:DWORD src1_sel:BYTE_0
	v_pk_fma_f32 v[80:81], v[110:111], v[24:25], v[80:81] op_sel_hi:[1,0,1]
	v_cvt_pknorm_u16_f32 v158, v156, v157
	v_and_b32_e32 v159, s16, v158
	v_exp_f32_e32 v82, v80
	v_cndmask_b32_e32 v162, v164, v15, vcc
	v_cndmask_b32_e32 v150, v150, v156, vcc
	v_exp_f32_e32 v83, v81
	v_cmp_eq_u32_sdwa vcc, s18, v41 src0_sel:DWORD src1_sel:BYTE_1
	v_lshrrev_b32_sdwa v160, v165, v159 dst_sel:DWORD dst_unused:UNUSED_PAD src0_sel:DWORD src1_sel:WORD_0
	v_lshrrev_b32_sdwa v161, v165, v159 dst_sel:DWORD dst_unused:UNUSED_PAD src0_sel:DWORD src1_sel:WORD_1
	v_cndmask_b32_e32 v163, v164, v15, vcc
	v_cndmask_b32_e32 v151, v151, v157, vcc
	ds_add_u32 v160, v162 offset:18032
	ds_add_u32 v161, v163 offset:18032
	v_pk_fma_f32 v[154:155], v[112:113], v[20:21], v[16:17] op_sel_hi:[1,0,0]
	v_cmp_eq_u32_sdwa vcc, s19, v41 src0_sel:DWORD src1_sel:BYTE_0
	v_pk_fma_f32 v[154:155], v[114:115], v[36:37], v[154:155] op_sel_hi:[1,0,1]
	v_cvt_pknorm_u16_f32 v158, v82, v83
	v_and_b32_e32 v159, s16, v158
	v_exp_f32_e32 v156, v154
	v_cndmask_b32_e32 v162, v164, v15, vcc
	v_cndmask_b32_e32 v150, v150, v82, vcc
	v_exp_f32_e32 v157, v155
	v_cmp_eq_u32_sdwa vcc, s19, v41 src0_sel:DWORD src1_sel:BYTE_1
	v_lshrrev_b32_sdwa v160, v165, v159 dst_sel:DWORD dst_unused:UNUSED_PAD src0_sel:DWORD src1_sel:WORD_0
	v_lshrrev_b32_sdwa v161, v165, v159 dst_sel:DWORD dst_unused:UNUSED_PAD src0_sel:DWORD src1_sel:WORD_1
	v_cndmask_b32_e32 v163, v164, v15, vcc
	v_cndmask_b32_e32 v151, v151, v83, vcc
	ds_add_u32 v160, v162 offset:34416
	ds_add_u32 v161, v163 offset:34416
	s_waitcnt lgkmcnt(6)
	v_pk_add_f32 v[166:167], v[76:77], v[150:151] neg_lo:[0,1] neg_hi:[0,1]
	s_nop 0
	v_pk_fma_f32 v[166:167], v[166:167], v[166:167], v[6:7]
	v_pk_fma_f32 v[80:81], v[112:113], v[20:21], v[16:17] op_sel:[0,1,1]
	v_cmp_eq_u32_sdwa vcc, s17, v41 src0_sel:DWORD src1_sel:BYTE_2
	v_pk_fma_f32 v[80:81], v[114:115], v[36:37], v[80:81] op_sel:[0,1,0]
	v_cvt_pknorm_u16_f32 v158, v156, v157
	v_and_b32_e32 v159, s16, v158
	v_exp_f32_e32 v82, v80
	v_cndmask_b32_e32 v162, v164, v15, vcc
	v_cndmask_b32_e32 v152, 0, v156, vcc
	v_exp_f32_e32 v83, v81
	v_cmp_eq_u32_sdwa vcc, s17, v41 src0_sel:DWORD src1_sel:BYTE_3
	v_lshrrev_b32_sdwa v160, v165, v159 dst_sel:DWORD dst_unused:UNUSED_PAD src0_sel:DWORD src1_sel:WORD_0
	v_lshrrev_b32_sdwa v161, v165, v159 dst_sel:DWORD dst_unused:UNUSED_PAD src0_sel:DWORD src1_sel:WORD_1
	v_cndmask_b32_e32 v163, v164, v15, vcc
	v_cndmask_b32_e32 v153, 0, v157, vcc
	ds_add_u32 v160, v162 offset:1648
	ds_add_u32 v161, v163 offset:1648
	v_pk_fma_f32 v[154:155], v[112:113], v[8:9], v[12:13] op_sel_hi:[1,0,0]
	v_cmp_eq_u32_sdwa vcc, s18, v41 src0_sel:DWORD src1_sel:BYTE_2
	v_pk_fma_f32 v[154:155], v[114:115], v[24:25], v[154:155] op_sel_hi:[1,0,1]
	v_cvt_pknorm_u16_f32 v158, v82, v83
	v_and_b32_e32 v159, s16, v158
	v_exp_f32_e32 v156, v154
	v_cndmask_b32_e32 v162, v164, v15, vcc
	v_cndmask_b32_e32 v152, v152, v82, vcc
	v_exp_f32_e32 v157, v155
	v_cmp_eq_u32_sdwa vcc, s18, v41 src0_sel:DWORD src1_sel:BYTE_3
	v_lshrrev_b32_sdwa v160, v165, v159 dst_sel:DWORD dst_unused:UNUSED_PAD src0_sel:DWORD src1_sel:WORD_0
	v_lshrrev_b32_sdwa v161, v165, v159 dst_sel:DWORD dst_unused:UNUSED_PAD src0_sel:DWORD src1_sel:WORD_1
	v_cndmask_b32_e32 v163, v164, v15, vcc
	v_cndmask_b32_e32 v153, v153, v83, vcc
	ds_add_u32 v160, v162 offset:18032
	ds_add_u32 v161, v163 offset:18032
	v_cmp_eq_u32_sdwa vcc, s19, v41 src0_sel:DWORD src1_sel:BYTE_2
	s_nop 0
	v_cvt_pknorm_u16_f32 v158, v156, v157
	v_and_b32_e32 v159, s16, v158
	v_cndmask_b32_e32 v162, v164, v15, vcc
	v_cndmask_b32_e32 v152, v152, v156, vcc
	v_cmp_eq_u32_sdwa vcc, s19, v41 src0_sel:DWORD src1_sel:BYTE_3
	v_lshrrev_b32_sdwa v160, v165, v159 dst_sel:DWORD dst_unused:UNUSED_PAD src0_sel:DWORD src1_sel:WORD_0
	v_lshrrev_b32_sdwa v161, v165, v159 dst_sel:DWORD dst_unused:UNUSED_PAD src0_sel:DWORD src1_sel:WORD_1
	v_cndmask_b32_e32 v163, v164, v15, vcc
	v_cndmask_b32_e32 v153, v153, v157, vcc
	ds_add_u32 v160, v162 offset:34416
	ds_add_u32 v161, v163 offset:34416
	v_pk_add_f32 v[80:81], v[78:79], v[152:153] neg_lo:[0,1] neg_hi:[0,1]
	s_nop 0
	v_pk_fma_f32 v[6:7], v[80:81], v[80:81], v[166:167]
	ds_read_b128 v[76:79], v1 offset:61440
	v_pk_fma_f32 v[80:81], v[116:117], v[20:21], v[16:17] op_sel_hi:[1,0,0]
	v_pk_fma_f32 v[80:81], v[118:119], v[36:37], v[80:81] op_sel_hi:[1,0,1]
	s_nop 0
	v_exp_f32_e32 v82, v80
	v_exp_f32_e32 v83, v81
	v_pk_fma_f32 v[154:155], v[116:117], v[20:21], v[16:17] op_sel:[0,1,1]
	v_cmp_eq_u32_sdwa vcc, s17, v19 src0_sel:DWORD src1_sel:BYTE_0
	v_pk_fma_f32 v[154:155], v[118:119], v[36:37], v[154:155] op_sel:[0,1,0]
	v_cvt_pknorm_u16_f32 v158, v82, v83
	v_and_b32_e32 v159, s16, v158
	v_exp_f32_e32 v156, v154
	v_cndmask_b32_e32 v162, v164, v15, vcc
	v_cndmask_b32_e32 v150, 0, v82, vcc
	v_exp_f32_e32 v157, v155
	v_cmp_eq_u32_sdwa vcc, s17, v19 src0_sel:DWORD src1_sel:BYTE_1
	v_lshrrev_b32_sdwa v160, v165, v159 dst_sel:DWORD dst_unused:UNUSED_PAD src0_sel:DWORD src1_sel:WORD_0
	v_lshrrev_b32_sdwa v161, v165, v159 dst_sel:DWORD dst_unused:UNUSED_PAD src0_sel:DWORD src1_sel:WORD_1
	v_cndmask_b32_e32 v163, v164, v15, vcc
	v_cndmask_b32_e32 v151, 0, v83, vcc
	ds_add_u32 v160, v162 offset:1648
	ds_add_u32 v161, v163 offset:1648
	v_pk_fma_f32 v[80:81], v[116:117], v[8:9], v[12:13] op_sel_hi:[1,0,0]
	v_cmp_eq_u32_sdwa vcc, s18, v19 src0_sel:DWORD src1_sel:BYTE_0
	v_pk_fma_f32 v[80:81], v[118:119], v[24:25], v[80:81] op_sel_hi:[1,0,1]
	v_cvt_pknorm_u16_f32 v158, v156, v157
	v_and_b32_e32 v159, s16, v158
	v_exp_f32_e32 v82, v80
	v_cndmask_b32_e32 v162, v164, v15, vcc
	v_cndmask_b32_e32 v150, v150, v156, vcc
	v_exp_f32_e32 v83, v81
	v_cmp_eq_u32_sdwa vcc, s18, v19 src0_sel:DWORD src1_sel:BYTE_1
	v_lshrrev_b32_sdwa v160, v165, v159 dst_sel:DWORD dst_unused:UNUSED_PAD src0_sel:DWORD src1_sel:WORD_0
	v_lshrrev_b32_sdwa v161, v165, v159 dst_sel:DWORD dst_unused:UNUSED_PAD src0_sel:DWORD src1_sel:WORD_1
	v_cndmask_b32_e32 v163, v164, v15, vcc
	v_cndmask_b32_e32 v151, v151, v157, vcc
	ds_add_u32 v160, v162 offset:18032
	ds_add_u32 v161, v163 offset:18032
	v_pk_fma_f32 v[154:155], v[120:121], v[20:21], v[16:17] op_sel_hi:[1,0,0]
	v_cmp_eq_u32_sdwa vcc, s19, v19 src0_sel:DWORD src1_sel:BYTE_0
	v_pk_fma_f32 v[154:155], v[122:123], v[36:37], v[154:155] op_sel_hi:[1,0,1]
	v_cvt_pknorm_u16_f32 v158, v82, v83
	v_and_b32_e32 v159, s16, v158
	v_exp_f32_e32 v156, v154
	v_cndmask_b32_e32 v162, v164, v15, vcc
	v_cndmask_b32_e32 v150, v150, v82, vcc
	v_exp_f32_e32 v157, v155
	v_cmp_eq_u32_sdwa vcc, s19, v19 src0_sel:DWORD src1_sel:BYTE_1
	v_lshrrev_b32_sdwa v160, v165, v159 dst_sel:DWORD dst_unused:UNUSED_PAD src0_sel:DWORD src1_sel:WORD_0
	v_lshrrev_b32_sdwa v161, v165, v159 dst_sel:DWORD dst_unused:UNUSED_PAD src0_sel:DWORD src1_sel:WORD_1
	v_cndmask_b32_e32 v163, v164, v15, vcc
	v_cndmask_b32_e32 v151, v151, v83, vcc
	ds_add_u32 v160, v162 offset:34416
	ds_add_u32 v161, v163 offset:34416
	s_waitcnt lgkmcnt(6)
	v_pk_add_f32 v[166:167], v[76:77], v[150:151] neg_lo:[0,1] neg_hi:[0,1]
	s_nop 0
	v_pk_fma_f32 v[166:167], v[166:167], v[166:167], v[6:7]
	v_pk_fma_f32 v[80:81], v[120:121], v[20:21], v[16:17] op_sel:[0,1,1]
	v_cmp_eq_u32_sdwa vcc, s17, v19 src0_sel:DWORD src1_sel:BYTE_2
	v_pk_fma_f32 v[80:81], v[122:123], v[36:37], v[80:81] op_sel:[0,1,0]
	v_cvt_pknorm_u16_f32 v158, v156, v157
	v_and_b32_e32 v159, s16, v158
	v_exp_f32_e32 v82, v80
	v_cndmask_b32_e32 v162, v164, v15, vcc
	v_cndmask_b32_e32 v152, 0, v156, vcc
	v_exp_f32_e32 v83, v81
	v_cmp_eq_u32_sdwa vcc, s17, v19 src0_sel:DWORD src1_sel:BYTE_3
	v_lshrrev_b32_sdwa v160, v165, v159 dst_sel:DWORD dst_unused:UNUSED_PAD src0_sel:DWORD src1_sel:WORD_0
	v_lshrrev_b32_sdwa v161, v165, v159 dst_sel:DWORD dst_unused:UNUSED_PAD src0_sel:DWORD src1_sel:WORD_1
	v_cndmask_b32_e32 v163, v164, v15, vcc
	v_cndmask_b32_e32 v153, 0, v157, vcc
	ds_add_u32 v160, v162 offset:1648
	ds_add_u32 v161, v163 offset:1648
	v_pk_fma_f32 v[154:155], v[120:121], v[8:9], v[12:13] op_sel_hi:[1,0,0]
	v_cmp_eq_u32_sdwa vcc, s18, v19 src0_sel:DWORD src1_sel:BYTE_2
	v_pk_fma_f32 v[154:155], v[122:123], v[24:25], v[154:155] op_sel_hi:[1,0,1]
	v_cvt_pknorm_u16_f32 v158, v82, v83
	v_and_b32_e32 v159, s16, v158
	v_exp_f32_e32 v156, v154
	v_cndmask_b32_e32 v162, v164, v15, vcc
	v_cndmask_b32_e32 v152, v152, v82, vcc
	v_exp_f32_e32 v157, v155
	v_cmp_eq_u32_sdwa vcc, s18, v19 src0_sel:DWORD src1_sel:BYTE_3
	v_lshrrev_b32_sdwa v160, v165, v159 dst_sel:DWORD dst_unused:UNUSED_PAD src0_sel:DWORD src1_sel:WORD_0
	v_lshrrev_b32_sdwa v161, v165, v159 dst_sel:DWORD dst_unused:UNUSED_PAD src0_sel:DWORD src1_sel:WORD_1
	v_cndmask_b32_e32 v163, v164, v15, vcc
	v_cndmask_b32_e32 v153, v153, v83, vcc
	ds_add_u32 v160, v162 offset:18032
	ds_add_u32 v161, v163 offset:18032
	v_cmp_eq_u32_sdwa vcc, s19, v19 src0_sel:DWORD src1_sel:BYTE_2
	s_nop 0
	v_cvt_pknorm_u16_f32 v158, v156, v157
	v_and_b32_e32 v159, s16, v158
	v_cndmask_b32_e32 v162, v164, v15, vcc
	v_cndmask_b32_e32 v152, v152, v156, vcc
	v_cmp_eq_u32_sdwa vcc, s19, v19 src0_sel:DWORD src1_sel:BYTE_3
	v_lshrrev_b32_sdwa v160, v165, v159 dst_sel:DWORD dst_unused:UNUSED_PAD src0_sel:DWORD src1_sel:WORD_0
	v_lshrrev_b32_sdwa v161, v165, v159 dst_sel:DWORD dst_unused:UNUSED_PAD src0_sel:DWORD src1_sel:WORD_1
	v_cndmask_b32_e32 v163, v164, v15, vcc
	v_cndmask_b32_e32 v153, v153, v157, vcc
	ds_add_u32 v160, v162 offset:34416
	ds_add_u32 v161, v163 offset:34416
	v_pk_add_f32 v[80:81], v[78:79], v[152:153] neg_lo:[0,1] neg_hi:[0,1]
	s_nop 0
	v_pk_fma_f32 v[6:7], v[80:81], v[80:81], v[166:167]
	ds_read_b128 v[76:79], v135
	v_pk_fma_f32 v[80:81], v[58:59], v[20:21], v[16:17] op_sel_hi:[1,0,0]
	v_pk_fma_f32 v[80:81], v[124:125], v[36:37], v[80:81] op_sel_hi:[1,0,1]
	s_nop 0
	v_exp_f32_e32 v82, v80
	v_exp_f32_e32 v83, v81
	v_pk_fma_f32 v[154:155], v[58:59], v[20:21], v[16:17] op_sel:[0,1,1]
	v_cmp_eq_u32_sdwa vcc, s17, v13 src0_sel:DWORD src1_sel:BYTE_0
	v_pk_fma_f32 v[154:155], v[124:125], v[36:37], v[154:155] op_sel:[0,1,0]
	v_cvt_pknorm_u16_f32 v158, v82, v83
	v_and_b32_e32 v159, s16, v158
	v_exp_f32_e32 v156, v154
	v_cndmask_b32_e32 v162, v164, v15, vcc
	v_cndmask_b32_e32 v150, 0, v82, vcc
	v_exp_f32_e32 v157, v155
	v_cmp_eq_u32_sdwa vcc, s17, v13 src0_sel:DWORD src1_sel:BYTE_1
	v_lshrrev_b32_sdwa v160, v165, v159 dst_sel:DWORD dst_unused:UNUSED_PAD src0_sel:DWORD src1_sel:WORD_0
	v_lshrrev_b32_sdwa v161, v165, v159 dst_sel:DWORD dst_unused:UNUSED_PAD src0_sel:DWORD src1_sel:WORD_1
	v_cndmask_b32_e32 v163, v164, v15, vcc
	v_cndmask_b32_e32 v151, 0, v83, vcc
	ds_add_u32 v160, v162 offset:1648
	ds_add_u32 v161, v163 offset:1648
	v_pk_fma_f32 v[80:81], v[58:59], v[8:9], v[12:13] op_sel_hi:[1,0,0]
	v_cmp_eq_u32_sdwa vcc, s18, v13 src0_sel:DWORD src1_sel:BYTE_0
	v_pk_fma_f32 v[80:81], v[124:125], v[24:25], v[80:81] op_sel_hi:[1,0,1]
	v_cvt_pknorm_u16_f32 v158, v156, v157
	v_and_b32_e32 v159, s16, v158
	v_exp_f32_e32 v82, v80
	v_cndmask_b32_e32 v162, v164, v15, vcc
	v_cndmask_b32_e32 v150, v150, v156, vcc
	v_exp_f32_e32 v83, v81
	v_cmp_eq_u32_sdwa vcc, s18, v13 src0_sel:DWORD src1_sel:BYTE_1
	v_lshrrev_b32_sdwa v160, v165, v159 dst_sel:DWORD dst_unused:UNUSED_PAD src0_sel:DWORD src1_sel:WORD_0
	v_lshrrev_b32_sdwa v161, v165, v159 dst_sel:DWORD dst_unused:UNUSED_PAD src0_sel:DWORD src1_sel:WORD_1
	v_cndmask_b32_e32 v163, v164, v15, vcc
	v_cndmask_b32_e32 v151, v151, v157, vcc
	ds_add_u32 v160, v162 offset:18032
	ds_add_u32 v161, v163 offset:18032
	v_pk_fma_f32 v[154:155], v[60:61], v[20:21], v[16:17] op_sel_hi:[1,0,0]
	v_cmp_eq_u32_sdwa vcc, s19, v13 src0_sel:DWORD src1_sel:BYTE_0
	v_pk_fma_f32 v[154:155], v[126:127], v[36:37], v[154:155] op_sel_hi:[1,0,1]
	v_cvt_pknorm_u16_f32 v158, v82, v83
	v_and_b32_e32 v159, s16, v158
	v_exp_f32_e32 v156, v154
	v_cndmask_b32_e32 v162, v164, v15, vcc
	v_cndmask_b32_e32 v150, v150, v82, vcc
	v_exp_f32_e32 v157, v155
	v_cmp_eq_u32_sdwa vcc, s19, v13 src0_sel:DWORD src1_sel:BYTE_1
	v_lshrrev_b32_sdwa v160, v165, v159 dst_sel:DWORD dst_unused:UNUSED_PAD src0_sel:DWORD src1_sel:WORD_0
	v_lshrrev_b32_sdwa v161, v165, v159 dst_sel:DWORD dst_unused:UNUSED_PAD src0_sel:DWORD src1_sel:WORD_1
	v_cndmask_b32_e32 v163, v164, v15, vcc
	v_cndmask_b32_e32 v151, v151, v83, vcc
	ds_add_u32 v160, v162 offset:34416
	ds_add_u32 v161, v163 offset:34416
	s_waitcnt lgkmcnt(6)
	v_pk_add_f32 v[166:167], v[76:77], v[150:151] neg_lo:[0,1] neg_hi:[0,1]
	s_nop 0
	v_pk_fma_f32 v[166:167], v[166:167], v[166:167], v[6:7]
	v_pk_fma_f32 v[80:81], v[60:61], v[20:21], v[16:17] op_sel:[0,1,1]
	v_cmp_eq_u32_sdwa vcc, s17, v13 src0_sel:DWORD src1_sel:BYTE_2
	v_pk_fma_f32 v[80:81], v[126:127], v[36:37], v[80:81] op_sel:[0,1,0]
	v_cvt_pknorm_u16_f32 v158, v156, v157
	v_and_b32_e32 v159, s16, v158
	v_exp_f32_e32 v82, v80
	v_cndmask_b32_e32 v162, v164, v15, vcc
	v_cndmask_b32_e32 v152, 0, v156, vcc
	v_exp_f32_e32 v83, v81
	v_cmp_eq_u32_sdwa vcc, s17, v13 src0_sel:DWORD src1_sel:BYTE_3
	v_lshrrev_b32_sdwa v160, v165, v159 dst_sel:DWORD dst_unused:UNUSED_PAD src0_sel:DWORD src1_sel:WORD_0
	v_lshrrev_b32_sdwa v161, v165, v159 dst_sel:DWORD dst_unused:UNUSED_PAD src0_sel:DWORD src1_sel:WORD_1
	v_cndmask_b32_e32 v163, v164, v15, vcc
	v_cndmask_b32_e32 v153, 0, v157, vcc
	ds_add_u32 v160, v162 offset:1648
	ds_add_u32 v161, v163 offset:1648
	v_pk_fma_f32 v[154:155], v[60:61], v[8:9], v[12:13] op_sel_hi:[1,0,0]
	v_cmp_eq_u32_sdwa vcc, s18, v13 src0_sel:DWORD src1_sel:BYTE_2
	v_pk_fma_f32 v[154:155], v[126:127], v[24:25], v[154:155] op_sel_hi:[1,0,1]
	v_cvt_pknorm_u16_f32 v158, v82, v83
	v_and_b32_e32 v159, s16, v158
	v_exp_f32_e32 v156, v154
	v_cndmask_b32_e32 v162, v164, v15, vcc
	v_cndmask_b32_e32 v152, v152, v82, vcc
	v_exp_f32_e32 v157, v155
	v_cmp_eq_u32_sdwa vcc, s18, v13 src0_sel:DWORD src1_sel:BYTE_3
	v_lshrrev_b32_sdwa v160, v165, v159 dst_sel:DWORD dst_unused:UNUSED_PAD src0_sel:DWORD src1_sel:WORD_0
	v_lshrrev_b32_sdwa v161, v165, v159 dst_sel:DWORD dst_unused:UNUSED_PAD src0_sel:DWORD src1_sel:WORD_1
	v_cndmask_b32_e32 v163, v164, v15, vcc
	v_cndmask_b32_e32 v153, v153, v83, vcc
	ds_add_u32 v160, v162 offset:18032
	ds_add_u32 v161, v163 offset:18032
	v_cmp_eq_u32_sdwa vcc, s19, v13 src0_sel:DWORD src1_sel:BYTE_2
	s_nop 0
	v_cvt_pknorm_u16_f32 v158, v156, v157
	v_and_b32_e32 v159, s16, v158
	v_cndmask_b32_e32 v162, v164, v15, vcc
	v_cndmask_b32_e32 v152, v152, v156, vcc
	v_cmp_eq_u32_sdwa vcc, s19, v13 src0_sel:DWORD src1_sel:BYTE_3
	v_lshrrev_b32_sdwa v160, v165, v159 dst_sel:DWORD dst_unused:UNUSED_PAD src0_sel:DWORD src1_sel:WORD_0
	v_lshrrev_b32_sdwa v161, v165, v159 dst_sel:DWORD dst_unused:UNUSED_PAD src0_sel:DWORD src1_sel:WORD_1
	v_cndmask_b32_e32 v163, v164, v15, vcc
	v_cndmask_b32_e32 v153, v153, v157, vcc
	ds_add_u32 v160, v162 offset:34416
	ds_add_u32 v161, v163 offset:34416
	v_pk_add_f32 v[80:81], v[78:79], v[152:153] neg_lo:[0,1] neg_hi:[0,1]
	s_nop 0
	v_pk_fma_f32 v[6:7], v[80:81], v[80:81], v[166:167]
	ds_read_b128 v[76:79], v70
	v_pk_fma_f32 v[80:81], v[62:63], v[20:21], v[16:17] op_sel_hi:[1,0,0]
	v_pk_fma_f32 v[80:81], v[66:67], v[36:37], v[80:81] op_sel_hi:[1,0,1]
	s_nop 0
	v_exp_f32_e32 v82, v80
	v_exp_f32_e32 v83, v81
	v_pk_fma_f32 v[154:155], v[62:63], v[20:21], v[16:17] op_sel:[0,1,1]
	v_cmp_eq_u32_sdwa vcc, s17, v9 src0_sel:DWORD src1_sel:BYTE_0
	v_pk_fma_f32 v[154:155], v[66:67], v[36:37], v[154:155] op_sel:[0,1,0]
	v_cvt_pknorm_u16_f32 v158, v82, v83
	v_and_b32_e32 v159, s16, v158
	v_exp_f32_e32 v156, v154
	v_cndmask_b32_e32 v162, v164, v15, vcc
	v_cndmask_b32_e32 v150, 0, v82, vcc
	v_exp_f32_e32 v157, v155
	v_cmp_eq_u32_sdwa vcc, s17, v9 src0_sel:DWORD src1_sel:BYTE_1
	v_lshrrev_b32_sdwa v160, v165, v159 dst_sel:DWORD dst_unused:UNUSED_PAD src0_sel:DWORD src1_sel:WORD_0
	v_lshrrev_b32_sdwa v161, v165, v159 dst_sel:DWORD dst_unused:UNUSED_PAD src0_sel:DWORD src1_sel:WORD_1
	v_cndmask_b32_e32 v163, v164, v15, vcc
	v_cndmask_b32_e32 v151, 0, v83, vcc
	ds_add_u32 v160, v162 offset:1648
	ds_add_u32 v161, v163 offset:1648
	v_pk_fma_f32 v[80:81], v[62:63], v[8:9], v[12:13] op_sel_hi:[1,0,0]
	v_cmp_eq_u32_sdwa vcc, s18, v9 src0_sel:DWORD src1_sel:BYTE_0
	v_pk_fma_f32 v[80:81], v[66:67], v[24:25], v[80:81] op_sel_hi:[1,0,1]
	v_cvt_pknorm_u16_f32 v158, v156, v157
	v_and_b32_e32 v159, s16, v158
	v_exp_f32_e32 v82, v80
	v_cndmask_b32_e32 v162, v164, v15, vcc
	v_cndmask_b32_e32 v150, v150, v156, vcc
	v_exp_f32_e32 v83, v81
	v_cmp_eq_u32_sdwa vcc, s18, v9 src0_sel:DWORD src1_sel:BYTE_1
	v_lshrrev_b32_sdwa v160, v165, v159 dst_sel:DWORD dst_unused:UNUSED_PAD src0_sel:DWORD src1_sel:WORD_0
	v_lshrrev_b32_sdwa v161, v165, v159 dst_sel:DWORD dst_unused:UNUSED_PAD src0_sel:DWORD src1_sel:WORD_1
	v_cndmask_b32_e32 v163, v164, v15, vcc
	v_cndmask_b32_e32 v151, v151, v157, vcc
	ds_add_u32 v160, v162 offset:18032
	ds_add_u32 v161, v163 offset:18032
	v_pk_fma_f32 v[154:155], v[64:65], v[20:21], v[16:17] op_sel_hi:[1,0,0]
	v_cmp_eq_u32_sdwa vcc, s19, v9 src0_sel:DWORD src1_sel:BYTE_0
	v_pk_fma_f32 v[154:155], v[68:69], v[36:37], v[154:155] op_sel_hi:[1,0,1]
	v_cvt_pknorm_u16_f32 v158, v82, v83
	v_and_b32_e32 v159, s16, v158
	v_exp_f32_e32 v156, v154
	v_cndmask_b32_e32 v162, v164, v15, vcc
	v_cndmask_b32_e32 v150, v150, v82, vcc
	v_exp_f32_e32 v157, v155
	v_cmp_eq_u32_sdwa vcc, s19, v9 src0_sel:DWORD src1_sel:BYTE_1
	v_lshrrev_b32_sdwa v160, v165, v159 dst_sel:DWORD dst_unused:UNUSED_PAD src0_sel:DWORD src1_sel:WORD_0
	v_lshrrev_b32_sdwa v161, v165, v159 dst_sel:DWORD dst_unused:UNUSED_PAD src0_sel:DWORD src1_sel:WORD_1
	v_cndmask_b32_e32 v163, v164, v15, vcc
	v_cndmask_b32_e32 v151, v151, v83, vcc
	ds_add_u32 v160, v162 offset:34416
	ds_add_u32 v161, v163 offset:34416
	s_waitcnt lgkmcnt(6)
	v_pk_add_f32 v[166:167], v[76:77], v[150:151] neg_lo:[0,1] neg_hi:[0,1]
	s_nop 0
	v_pk_fma_f32 v[166:167], v[166:167], v[166:167], v[6:7]
	v_pk_fma_f32 v[80:81], v[64:65], v[20:21], v[16:17] op_sel:[0,1,1]
	v_cmp_eq_u32_sdwa vcc, s17, v9 src0_sel:DWORD src1_sel:BYTE_2
	v_pk_fma_f32 v[80:81], v[68:69], v[36:37], v[80:81] op_sel:[0,1,0]
	v_cvt_pknorm_u16_f32 v158, v156, v157
	v_and_b32_e32 v159, s16, v158
	v_exp_f32_e32 v82, v80
	v_cndmask_b32_e32 v162, v164, v15, vcc
	v_cndmask_b32_e32 v152, 0, v156, vcc
	v_exp_f32_e32 v83, v81
	v_cmp_eq_u32_sdwa vcc, s17, v9 src0_sel:DWORD src1_sel:BYTE_3
	v_lshrrev_b32_sdwa v160, v165, v159 dst_sel:DWORD dst_unused:UNUSED_PAD src0_sel:DWORD src1_sel:WORD_0
	v_lshrrev_b32_sdwa v161, v165, v159 dst_sel:DWORD dst_unused:UNUSED_PAD src0_sel:DWORD src1_sel:WORD_1
	v_cndmask_b32_e32 v163, v164, v15, vcc
	v_cndmask_b32_e32 v153, 0, v157, vcc
	ds_add_u32 v160, v162 offset:1648
	ds_add_u32 v161, v163 offset:1648
	v_pk_fma_f32 v[154:155], v[64:65], v[8:9], v[12:13] op_sel_hi:[1,0,0]
	v_cmp_eq_u32_sdwa vcc, s18, v9 src0_sel:DWORD src1_sel:BYTE_2
	v_pk_fma_f32 v[154:155], v[68:69], v[24:25], v[154:155] op_sel_hi:[1,0,1]
	v_cvt_pknorm_u16_f32 v158, v82, v83
	v_and_b32_e32 v159, s16, v158
	v_exp_f32_e32 v156, v154
	v_cndmask_b32_e32 v162, v164, v15, vcc
	v_cndmask_b32_e32 v152, v152, v82, vcc
	v_exp_f32_e32 v157, v155
	v_cmp_eq_u32_sdwa vcc, s18, v9 src0_sel:DWORD src1_sel:BYTE_3
	v_lshrrev_b32_sdwa v160, v165, v159 dst_sel:DWORD dst_unused:UNUSED_PAD src0_sel:DWORD src1_sel:WORD_0
	v_lshrrev_b32_sdwa v161, v165, v159 dst_sel:DWORD dst_unused:UNUSED_PAD src0_sel:DWORD src1_sel:WORD_1
	v_cndmask_b32_e32 v163, v164, v15, vcc
	v_cndmask_b32_e32 v153, v153, v83, vcc
	ds_add_u32 v160, v162 offset:18032
	ds_add_u32 v161, v163 offset:18032
	v_cmp_eq_u32_sdwa vcc, s19, v9 src0_sel:DWORD src1_sel:BYTE_2
	s_nop 0
	v_cvt_pknorm_u16_f32 v158, v156, v157
	v_and_b32_e32 v159, s16, v158
	v_cndmask_b32_e32 v162, v164, v15, vcc
	v_cndmask_b32_e32 v152, v152, v156, vcc
	v_cmp_eq_u32_sdwa vcc, s19, v9 src0_sel:DWORD src1_sel:BYTE_3
	v_lshrrev_b32_sdwa v160, v165, v159 dst_sel:DWORD dst_unused:UNUSED_PAD src0_sel:DWORD src1_sel:WORD_0
	v_lshrrev_b32_sdwa v161, v165, v159 dst_sel:DWORD dst_unused:UNUSED_PAD src0_sel:DWORD src1_sel:WORD_1
	v_cndmask_b32_e32 v163, v164, v15, vcc
	v_cndmask_b32_e32 v153, v153, v157, vcc
	ds_add_u32 v160, v162 offset:34416
	ds_add_u32 v161, v163 offset:34416
	v_pk_add_f32 v[80:81], v[78:79], v[152:153] neg_lo:[0,1] neg_hi:[0,1]
	s_nop 0
	v_pk_fma_f32 v[6:7], v[80:81], v[80:81], v[166:167]
	s_and_saveexec_b64 s[8:9], s[4:5]
	s_cbranch_execz .LBB0_60
	v_add_u32_e32 v149, 0x18000, v1
	ds_read_b128 v[76:79], v149
	v_pk_fma_f32 v[80:81], v[54:55], v[20:21], v[16:17] op_sel_hi:[1,0,0]
	v_pk_fma_f32 v[80:81], v[50:51], v[36:37], v[80:81] op_sel_hi:[1,0,1]
	s_nop 0
	v_exp_f32_e32 v82, v80
	v_exp_f32_e32 v83, v81
	v_pk_fma_f32 v[154:155], v[54:55], v[20:21], v[16:17] op_sel:[0,1,1]
	v_cmp_eq_u32_sdwa vcc, s17, v40 src0_sel:DWORD src1_sel:BYTE_0
	v_pk_fma_f32 v[154:155], v[50:51], v[36:37], v[154:155] op_sel:[0,1,0]
	v_cvt_pknorm_u16_f32 v158, v82, v83
	v_and_b32_e32 v159, s16, v158
	v_exp_f32_e32 v156, v154
	v_cndmask_b32_e32 v162, v164, v15, vcc
	v_cndmask_b32_e32 v150, 0, v82, vcc
	v_exp_f32_e32 v157, v155
	v_cmp_eq_u32_sdwa vcc, s17, v40 src0_sel:DWORD src1_sel:BYTE_1
	v_lshrrev_b32_sdwa v160, v165, v159 dst_sel:DWORD dst_unused:UNUSED_PAD src0_sel:DWORD src1_sel:WORD_0
	v_lshrrev_b32_sdwa v161, v165, v159 dst_sel:DWORD dst_unused:UNUSED_PAD src0_sel:DWORD src1_sel:WORD_1
	v_cndmask_b32_e32 v163, v164, v15, vcc
	v_cndmask_b32_e32 v151, 0, v83, vcc
	ds_add_u32 v160, v162 offset:1648
	ds_add_u32 v161, v163 offset:1648
	v_pk_fma_f32 v[80:81], v[54:55], v[8:9], v[12:13] op_sel_hi:[1,0,0]
	v_cmp_eq_u32_sdwa vcc, s18, v40 src0_sel:DWORD src1_sel:BYTE_0
	v_pk_fma_f32 v[80:81], v[50:51], v[24:25], v[80:81] op_sel_hi:[1,0,1]
	v_cvt_pknorm_u16_f32 v158, v156, v157
	v_and_b32_e32 v159, s16, v158
	v_exp_f32_e32 v82, v80
	v_cndmask_b32_e32 v162, v164, v15, vcc
	v_cndmask_b32_e32 v150, v150, v156, vcc
	v_exp_f32_e32 v83, v81
	v_cmp_eq_u32_sdwa vcc, s18, v40 src0_sel:DWORD src1_sel:BYTE_1
	v_lshrrev_b32_sdwa v160, v165, v159 dst_sel:DWORD dst_unused:UNUSED_PAD src0_sel:DWORD src1_sel:WORD_0
	v_lshrrev_b32_sdwa v161, v165, v159 dst_sel:DWORD dst_unused:UNUSED_PAD src0_sel:DWORD src1_sel:WORD_1
	v_cndmask_b32_e32 v163, v164, v15, vcc
	v_cndmask_b32_e32 v151, v151, v157, vcc
	ds_add_u32 v160, v162 offset:18032
	ds_add_u32 v161, v163 offset:18032
	v_pk_fma_f32 v[154:155], v[46:47], v[20:21], v[16:17] op_sel_hi:[1,0,0]
	v_cmp_eq_u32_sdwa vcc, s19, v40 src0_sel:DWORD src1_sel:BYTE_0
	v_pk_fma_f32 v[154:155], v[74:75], v[36:37], v[154:155] op_sel_hi:[1,0,1]
	v_cvt_pknorm_u16_f32 v158, v82, v83
	v_and_b32_e32 v159, s16, v158
	v_exp_f32_e32 v156, v154
	v_cndmask_b32_e32 v162, v164, v15, vcc
	v_cndmask_b32_e32 v150, v150, v82, vcc
	v_exp_f32_e32 v157, v155
	v_cmp_eq_u32_sdwa vcc, s19, v40 src0_sel:DWORD src1_sel:BYTE_1
	v_lshrrev_b32_sdwa v160, v165, v159 dst_sel:DWORD dst_unused:UNUSED_PAD src0_sel:DWORD src1_sel:WORD_0
	v_lshrrev_b32_sdwa v161, v165, v159 dst_sel:DWORD dst_unused:UNUSED_PAD src0_sel:DWORD src1_sel:WORD_1
	v_cndmask_b32_e32 v163, v164, v15, vcc
	v_cndmask_b32_e32 v151, v151, v83, vcc
	ds_add_u32 v160, v162 offset:34416
	ds_add_u32 v161, v163 offset:34416
	s_waitcnt lgkmcnt(6)
	v_pk_add_f32 v[166:167], v[76:77], v[150:151] neg_lo:[0,1] neg_hi:[0,1]
	s_nop 0
	v_pk_fma_f32 v[166:167], v[166:167], v[166:167], v[6:7]
	v_pk_fma_f32 v[80:81], v[46:47], v[20:21], v[16:17] op_sel:[0,1,1]
	v_cmp_eq_u32_sdwa vcc, s17, v40 src0_sel:DWORD src1_sel:BYTE_2
	v_pk_fma_f32 v[80:81], v[74:75], v[36:37], v[80:81] op_sel:[0,1,0]
	v_cvt_pknorm_u16_f32 v158, v156, v157
	v_and_b32_e32 v159, s16, v158
	v_exp_f32_e32 v82, v80
	v_cndmask_b32_e32 v162, v164, v15, vcc
	v_cndmask_b32_e32 v152, 0, v156, vcc
	v_exp_f32_e32 v83, v81
	v_cmp_eq_u32_sdwa vcc, s17, v40 src0_sel:DWORD src1_sel:BYTE_3
	v_lshrrev_b32_sdwa v160, v165, v159 dst_sel:DWORD dst_unused:UNUSED_PAD src0_sel:DWORD src1_sel:WORD_0
	v_lshrrev_b32_sdwa v161, v165, v159 dst_sel:DWORD dst_unused:UNUSED_PAD src0_sel:DWORD src1_sel:WORD_1
	v_cndmask_b32_e32 v163, v164, v15, vcc
	v_cndmask_b32_e32 v153, 0, v157, vcc
	ds_add_u32 v160, v162 offset:1648
	ds_add_u32 v161, v163 offset:1648
	v_pk_fma_f32 v[154:155], v[46:47], v[8:9], v[12:13] op_sel_hi:[1,0,0]
	v_cmp_eq_u32_sdwa vcc, s18, v40 src0_sel:DWORD src1_sel:BYTE_2
	v_pk_fma_f32 v[154:155], v[74:75], v[24:25], v[154:155] op_sel_hi:[1,0,1]
	v_cvt_pknorm_u16_f32 v158, v82, v83
	v_and_b32_e32 v159, s16, v158
	v_exp_f32_e32 v156, v154
	v_cndmask_b32_e32 v162, v164, v15, vcc
	v_cndmask_b32_e32 v152, v152, v82, vcc
	v_exp_f32_e32 v157, v155
	v_cmp_eq_u32_sdwa vcc, s18, v40 src0_sel:DWORD src1_sel:BYTE_3
	v_lshrrev_b32_sdwa v160, v165, v159 dst_sel:DWORD dst_unused:UNUSED_PAD src0_sel:DWORD src1_sel:WORD_0
	v_lshrrev_b32_sdwa v161, v165, v159 dst_sel:DWORD dst_unused:UNUSED_PAD src0_sel:DWORD src1_sel:WORD_1
	v_cndmask_b32_e32 v163, v164, v15, vcc
	v_cndmask_b32_e32 v153, v153, v83, vcc
	ds_add_u32 v160, v162 offset:18032
	ds_add_u32 v161, v163 offset:18032
	v_cmp_eq_u32_sdwa vcc, s19, v40 src0_sel:DWORD src1_sel:BYTE_2
	s_nop 0
	v_cvt_pknorm_u16_f32 v158, v156, v157
	v_and_b32_e32 v159, s16, v158
	v_cndmask_b32_e32 v162, v164, v15, vcc
	v_cndmask_b32_e32 v152, v152, v156, vcc
	v_cmp_eq_u32_sdwa vcc, s19, v40 src0_sel:DWORD src1_sel:BYTE_3
	v_lshrrev_b32_sdwa v160, v165, v159 dst_sel:DWORD dst_unused:UNUSED_PAD src0_sel:DWORD src1_sel:WORD_0
	v_lshrrev_b32_sdwa v161, v165, v159 dst_sel:DWORD dst_unused:UNUSED_PAD src0_sel:DWORD src1_sel:WORD_1
	v_cndmask_b32_e32 v163, v164, v15, vcc
	v_cndmask_b32_e32 v153, v153, v157, vcc
	ds_add_u32 v160, v162 offset:34416
	ds_add_u32 v161, v163 offset:34416
	v_pk_add_f32 v[80:81], v[78:79], v[152:153] neg_lo:[0,1] neg_hi:[0,1]
	s_nop 0
	v_pk_fma_f32 v[6:7], v[80:81], v[80:81], v[166:167]
